# GEMM phase output stores (P1,P5,P6,P8,P9) write-through sc0 sc1, on top of P11 trims
# speedup vs baseline: 1.0028x; 1.0028x over previous
; __device__ __forceinline__ unsigned cvt_pk_bf16(float lo, float hi) { unsigned r; asm volatile("v_cvt_pk_bf16_f32 %0, %1, %2" : "=v"(r) : "v"(lo), "v"(hi)); return r; }
; #define PG8_BAR __builtin_amdgcn_s_barrier()
; template <class Epi, class Sched, bool ALIGN_EPI = false, bool SP2 = false>
; __device__ __forceinline__ void gemm_phase(PG8_LAS unsigned char* lds, const Gemm g, const Sched& S, const Epi& E) {
;     ...
;         if constexpr (ALIGN_EPI) { if (wr == 0) PG8_BAR; }
;         if constexpr (!Epi::AFTER_DRAIN) { E(acc, cur, wr, wc, fr, fq); S.done(cur); }
;         if (!has_next) break;
; #pragma unroll
;         for (int a = 0; a < 2; ++a)
; #pragma unroll
;             for (int b = 0; b < 2; ++b)
; #pragma unroll
;                 for (int m = 0; m < 4; ++m)
; #pragma unroll
;                     for (int n = 0; n < 2; ++n) acc[a][b][m][n] = (f32x4){0.f, 0.f, 0.f, 0.f};
;         cur = nxt; cA = nA; cB = nB; ++ui;
;         if constexpr (ALIGN_EPI) { if (wr == 1) PG8_BAR; }
;     __device__ __forceinline__ void operator()(const f32x4 (&acc)[2][2][4][2], const Unit& u, int wr, int wc, int fr, int fq) const {
;         bf16_t* base; int ld, colt;
;         if (u.pn < ntile0) { base = O0; ld = ld0; colt = u.pn * BM; }
;         else { const int q = u.pn - ntile0, per = ld1 / BM; base = O1 + (size_t)(q / per) * stride1; ld = ld1; colt = (q % per) * BM; }
;         const int row0 = u.pm * BM + wr * 64 + fr, col0 = colt + wc * 32 + 8 * fq;
; #pragma unroll
;         for (int ai = 0; ai < 2; ++ai)
; #pragma unroll
;             for (int m = 0; m < 4; ++m) {
;                 const int row = row0 + ai * HALF + m * 16;
;                 float sc = cs; if (ssq) sc *= rsqrtf(ssq[row] * (1.0f / 1024.0f) + 1e-6f);
;                 bf16_t* rowp = base + (size_t)row * ld + col0;
; #pragma unroll
;                 for (int bj = 0; bj < 2; ++bj) { const f32x4 v0 = acc[ai][bj][m][0] * sc, v1 = acc[ai][bj][m][1] * sc;
;                     u32x4 w; w.x = cvt_pk_bf16(v0[0], v0[1]); w.y = cvt_pk_bf16(v0[2], v0[3]); w.z = cvt_pk_bf16(v1[0], v1[1]); w.w = cvt_pk_bf16(v1[2], v1[3]);
;                     *(u32x4*)(rowp + bj * HALF) = w; } }
.LBB0_126:
	v_lshl_or_b32 v146, s61, 8, v149
	v_lshl_add_u32 v153, s40, 8, v1
	v_ashrrev_i32_e32 v147, 31, v146
	v_lshl_add_u64 v[146:147], v[146:147], 1, s[22:23]
	v_mad_i64_i32 v[154:155], s[22:23], s42, v153, 0
	v_lshl_add_u64 v[154:155], v[154:155], 1, v[146:147]
	v_cvt_pk_bf16_f32 v126, v126, v127
	v_cvt_pk_bf16_f32 v127, v128, v129
	v_cvt_pk_bf16_f32 v128, v122, v123
	v_cvt_pk_bf16_f32 v129, v124, v125
	global_store_dwordx4 v[154:155], v[126:129], off sc0 sc1
	v_cvt_pk_bf16_f32 v114, v114, v115
	v_cvt_pk_bf16_f32 v115, v116, v117
	v_cvt_pk_bf16_f32 v116, v106, v107
	v_or_b32_e32 v106, 16, v153
	v_mad_i64_i32 v[106:107], s[22:23], s42, v106, 0
	v_cvt_pk_bf16_f32 v117, v108, v109
	global_store_dwordx4 v[154:155], v[114:117], off offset:256 sc0 sc1
	s_andn2_b64 vcc, exec, s[4:5]
	s_mov_b64 s[4:5], -1
	v_lshl_add_u64 v[114:115], v[106:107], 1, v[146:147]
	v_cvt_pk_bf16_f32 v106, v118, v119
	v_cvt_pk_bf16_f32 v107, v120, v121
	v_cvt_pk_bf16_f32 v108, v110, v111
	v_cvt_pk_bf16_f32 v109, v112, v113
	global_store_dwordx4 v[114:115], v[106:109], off sc0 sc1
	v_cvt_pk_bf16_f32 v98, v98, v99
	v_cvt_pk_bf16_f32 v99, v100, v101
	v_cvt_pk_bf16_f32 v100, v90, v91
	v_or_b32_e32 v90, 32, v153
	v_mad_i64_i32 v[90:91], s[22:23], s42, v90, 0
	v_cvt_pk_bf16_f32 v101, v92, v93
	global_store_dwordx4 v[114:115], v[98:101], off offset:256 sc0 sc1
	s_nop 1
	v_lshl_add_u64 v[98:99], v[90:91], 1, v[146:147]
	v_cvt_pk_bf16_f32 v90, v102, v103
	v_cvt_pk_bf16_f32 v91, v104, v105
	v_cvt_pk_bf16_f32 v92, v94, v95
	v_cvt_pk_bf16_f32 v93, v96, v97
	global_store_dwordx4 v[98:99], v[90:93], off sc0 sc1
	v_cvt_pk_bf16_f32 v82, v82, v83
	v_cvt_pk_bf16_f32 v83, v84, v85
	v_cvt_pk_bf16_f32 v84, v74, v75
	v_or_b32_e32 v74, 48, v153
	v_mad_i64_i32 v[74:75], s[22:23], s42, v74, 0
	v_cvt_pk_bf16_f32 v85, v76, v77
	global_store_dwordx4 v[98:99], v[82:85], off offset:256 sc0 sc1
	s_nop 1
	v_lshl_add_u64 v[82:83], v[74:75], 1, v[146:147]
	v_cvt_pk_bf16_f32 v74, v86, v87
	v_cvt_pk_bf16_f32 v75, v88, v89
	v_cvt_pk_bf16_f32 v76, v78, v79
	v_cvt_pk_bf16_f32 v77, v80, v81
	global_store_dwordx4 v[82:83], v[74:77], off sc0 sc1
	v_cvt_pk_bf16_f32 v70, v70, v71
	v_cvt_pk_bf16_f32 v71, v72, v73
	v_cvt_pk_bf16_f32 v72, v66, v67
	v_add_u32_e32 v66, 0x80, v153
	v_mad_i64_i32 v[66:67], s[22:23], s42, v66, 0
	v_lshl_add_u64 v[66:67], v[66:67], 1, v[146:147]
	v_cvt_pk_bf16_f32 v73, v68, v69
	global_store_dwordx4 v[82:83], v[70:73], off offset:256 sc0 sc1
	v_cvt_pk_bf16_f32 v62, v62, v63
	v_cvt_pk_bf16_f32 v63, v64, v65
	v_cvt_pk_bf16_f32 v64, v58, v59
	v_cvt_pk_bf16_f32 v65, v60, v61
	global_store_dwordx4 v[66:67], v[62:65], off sc0 sc1
	v_cvt_pk_bf16_f32 v50, v50, v51
	v_cvt_pk_bf16_f32 v51, v52, v53
	v_cvt_pk_bf16_f32 v52, v42, v43
	v_add_u32_e32 v42, 0x90, v153
	v_mad_i64_i32 v[42:43], s[22:23], s42, v42, 0
	v_cvt_pk_bf16_f32 v53, v44, v45
	global_store_dwordx4 v[66:67], v[50:53], off offset:256 sc0 sc1
	s_nop 1
	v_lshl_add_u64 v[50:51], v[42:43], 1, v[146:147]
	v_cvt_pk_bf16_f32 v42, v54, v55
	v_cvt_pk_bf16_f32 v43, v56, v57
	v_cvt_pk_bf16_f32 v44, v46, v47
	v_cvt_pk_bf16_f32 v45, v48, v49
	global_store_dwordx4 v[50:51], v[42:45], off sc0 sc1
	v_cvt_pk_bf16_f32 v34, v34, v35
	v_cvt_pk_bf16_f32 v35, v36, v37
	v_cvt_pk_bf16_f32 v36, v26, v27
	v_add_u32_e32 v26, 0xa0, v153
	v_mad_i64_i32 v[26:27], s[22:23], s42, v26, 0
	v_cvt_pk_bf16_f32 v37, v28, v29
	global_store_dwordx4 v[50:51], v[34:37], off offset:256 sc0 sc1
	s_nop 1
	v_lshl_add_u64 v[34:35], v[26:27], 1, v[146:147]
	v_cvt_pk_bf16_f32 v26, v38, v39
	v_cvt_pk_bf16_f32 v27, v40, v41
	v_cvt_pk_bf16_f32 v28, v30, v31
	v_cvt_pk_bf16_f32 v29, v32, v33
	global_store_dwordx4 v[34:35], v[26:29], off sc0 sc1
	v_cvt_pk_bf16_f32 v18, v18, v19
	v_cvt_pk_bf16_f32 v19, v20, v21
	v_cvt_pk_bf16_f32 v20, v10, v11
	v_add_u32_e32 v10, 0xb0, v153
	v_mad_i64_i32 v[10:11], s[22:23], s42, v10, 0
	v_cvt_pk_bf16_f32 v21, v12, v13
	global_store_dwordx4 v[34:35], v[18:21], off offset:256 sc0 sc1
	s_nop 1
	v_lshl_add_u64 v[18:19], v[10:11], 1, v[146:147]
	v_cvt_pk_bf16_f32 v10, v22, v23
	v_cvt_pk_bf16_f32 v11, v24, v25
	v_cvt_pk_bf16_f32 v12, v14, v15
	v_cvt_pk_bf16_f32 v13, v16, v17
	global_store_dwordx4 v[18:19], v[10:13], off sc0 sc1
	v_cvt_pk_bf16_f32 v6, v6, v7
	v_cvt_pk_bf16_f32 v7, v8, v9
	v_cvt_pk_bf16_f32 v8, v2, v3
	v_cvt_pk_bf16_f32 v9, v4, v5
	global_store_dwordx4 v[18:19], v[6:9], off offset:256 sc0 sc1
	s_cbranch_vccnz .LBB0_116
	s_andn2_b64 vcc, exec, s[8:9]
	s_cbranch_vccnz .LBB0_115
	s_barrier
	s_branch .LBB0_115

; __device__ __forceinline__ unsigned cvt_pk_bf16(float lo, float hi) { unsigned r; asm volatile("v_cvt_pk_bf16_f32 %0, %1, %2" : "=v"(r) : "v"(lo), "v"(hi)); return r; }
;     __device__ __forceinline__ void operator()(const f32x4 (&acc)[2][2][4][2], const Unit& u, int wr, int wc, int fr, int fq) const {
;         bf16_t* base; int ld, colt;
;         if (u.pn < ntile0) { base = O0; ld = ld0; colt = u.pn * BM; }
;         else { const int q = u.pn - ntile0, per = ld1 / BM; base = O1 + (size_t)(q / per) * stride1; ld = ld1; colt = (q % per) * BM; }
;         const int row0 = u.pm * BM + wr * 64 + fr, col0 = colt + wc * 32 + 8 * fq;
; #pragma unroll
;         for (int ai = 0; ai < 2; ++ai)
; #pragma unroll
;             for (int m = 0; m < 4; ++m) {
;                 const int row = row0 + ai * HALF + m * 16;
;                 float sc = cs; if (ssq) sc *= rsqrtf(ssq[row] * (1.0f / 1024.0f) + 1e-6f);
;                 bf16_t* rowp = base + (size_t)row * ld + col0;
; #pragma unroll
;                 for (int bj = 0; bj < 2; ++bj) { const f32x4 v0 = acc[ai][bj][m][0] * sc, v1 = acc[ai][bj][m][1] * sc;
;                     u32x4 w; w.x = cvt_pk_bf16(v0[0], v0[1]); w.y = cvt_pk_bf16(v0[2], v0[3]); w.z = cvt_pk_bf16(v1[0], v1[1]); w.w = cvt_pk_bf16(v1[2], v1[3]);
;                     *(u32x4*)(rowp + bj * HALF) = w; } }
.LBB0_2442:
	v_lshl_add_u32 v146, s0, 8, v152
	v_ashrrev_i32_e32 v147, 31, v146
	v_lshl_add_u64 v[148:149], v[146:147], 2, s[8:9]
	global_load_dword v159, v[148:149], off
	s_lshl_b32 s0, s1, 8
	s_cmp_lt_i32 s1, 4
	s_cselect_b32 s15, 10, 8
	v_lshlrev_b64 v[164:165], s15, v[146:147]
	s_cselect_b32 s0, s0, 0
	s_cselect_b32 s1, s28, 0
	s_cselect_b32 s17, s3, 0
	v_or_b32_e32 v162, s0, v154
	v_mov_b32_e32 v150, s17
	v_mov_b32_e32 v151, s1
	v_ashrrev_i32_e32 v163, 31, v162
	v_lshl_add_u64 v[150:151], v[162:163], 1, v[150:151]
	v_or_b32_e32 v160, 16, v146
	v_lshl_add_u64 v[162:163], v[164:165], 1, v[150:151]
	v_ashrrev_i32_e32 v161, 31, v160
	v_lshl_add_u64 v[166:167], v[160:161], 2, s[8:9]
	s_waitcnt vmcnt(0)
	v_fmamk_f32 v147, v159, 0x3a800000, v158
	v_mul_f32_e32 v159, 0x4b800000, v147
	v_cmp_gt_f32_e32 vcc, s47, v147
	s_nop 1
	v_cndmask_b32_e32 v147, v147, v159, vcc
	v_rsq_f32_e32 v147, v147
	s_nop 0
	v_mul_f32_e32 v159, 0x45800000, v147
	v_cndmask_b32_e32 v147, v147, v159, vcc
	v_mul_f32_e32 v164, 0x3d800000, v147
	v_pk_mul_f32 v[128:129], v[128:129], v[164:165] op_sel_hi:[1,0]
	v_pk_mul_f32 v[126:127], v[126:127], v[164:165] op_sel_hi:[1,0]
	v_pk_mul_f32 v[124:125], v[124:125], v[164:165] op_sel_hi:[1,0]
	v_pk_mul_f32 v[122:123], v[122:123], v[164:165] op_sel_hi:[1,0]
	v_pk_mul_f32 v[120:121], v[120:121], v[164:165] op_sel_hi:[1,0]
	v_pk_mul_f32 v[118:119], v[118:119], v[164:165] op_sel_hi:[1,0]
	v_pk_mul_f32 v[168:169], v[116:117], v[164:165] op_sel_hi:[1,0]
	v_pk_mul_f32 v[164:165], v[114:115], v[164:165] op_sel_hi:[1,0]
	v_cvt_pk_bf16_f32 v114, v126, v127
	v_cvt_pk_bf16_f32 v115, v128, v129
	v_cvt_pk_bf16_f32 v116, v122, v123
	v_cvt_pk_bf16_f32 v117, v124, v125
	global_store_dwordx4 v[162:163], v[114:117], off sc0 sc1
	s_nop 1
	v_cvt_pk_bf16_f32 v114, v118, v119
	v_cvt_pk_bf16_f32 v115, v120, v121
	v_cvt_pk_bf16_f32 v116, v164, v165
	v_cvt_pk_bf16_f32 v117, v168, v169
	global_store_dwordx4 v[162:163], v[114:117], off offset:256 sc0 sc1
	global_load_dword v116, v[166:167], off
	s_nop 0
	v_or_b32_e32 v114, 32, v146
	v_ashrrev_i32_e32 v115, 31, v114
	v_lshl_add_u64 v[118:119], v[114:115], 2, s[8:9]
	s_waitcnt vmcnt(0)
	v_fmamk_f32 v116, v116, 0x3a800000, v158
	v_mul_f32_e32 v117, 0x4b800000, v116
	v_cmp_gt_f32_e32 vcc, s47, v116
	s_nop 1
	v_cndmask_b32_e32 v116, v116, v117, vcc
	v_rsq_f32_e32 v120, v116
	v_lshlrev_b64 v[116:117], s15, v[160:161]
	v_lshl_add_u64 v[116:117], v[116:117], 1, v[150:151]
	v_mul_f32_e32 v121, 0x45800000, v120
	v_cndmask_b32_e32 v120, v120, v121, vcc
	v_mul_f32_e32 v120, 0x3d800000, v120
	v_pk_mul_f32 v[112:113], v[112:113], v[120:121] op_sel_hi:[1,0]
	v_pk_mul_f32 v[110:111], v[110:111], v[120:121] op_sel_hi:[1,0]
	v_pk_mul_f32 v[108:109], v[108:109], v[120:121] op_sel_hi:[1,0]
	v_pk_mul_f32 v[106:107], v[106:107], v[120:121] op_sel_hi:[1,0]
	v_pk_mul_f32 v[104:105], v[104:105], v[120:121] op_sel_hi:[1,0]
	v_pk_mul_f32 v[102:103], v[102:103], v[120:121] op_sel_hi:[1,0]
	v_pk_mul_f32 v[122:123], v[100:101], v[120:121] op_sel_hi:[1,0]
	v_pk_mul_f32 v[120:121], v[98:99], v[120:121] op_sel_hi:[1,0]
	v_cvt_pk_bf16_f32 v98, v110, v111
	v_cvt_pk_bf16_f32 v99, v112, v113
	v_cvt_pk_bf16_f32 v100, v106, v107
	v_cvt_pk_bf16_f32 v101, v108, v109
	global_store_dwordx4 v[116:117], v[98:101], off sc0 sc1
	s_nop 1
	v_cvt_pk_bf16_f32 v98, v102, v103
	v_cvt_pk_bf16_f32 v99, v104, v105
	v_cvt_pk_bf16_f32 v100, v120, v121
	v_cvt_pk_bf16_f32 v101, v122, v123
	global_store_dwordx4 v[116:117], v[98:101], off offset:256 sc0 sc1
	global_load_dword v100, v[118:119], off
	s_nop 0
	v_or_b32_e32 v98, 48, v146
	v_ashrrev_i32_e32 v99, 31, v98
	v_lshl_add_u64 v[102:103], v[98:99], 2, s[8:9]
	s_waitcnt vmcnt(0)
	v_fmamk_f32 v100, v100, 0x3a800000, v158
	v_mul_f32_e32 v101, 0x4b800000, v100
	v_cmp_gt_f32_e32 vcc, s47, v100
	s_nop 1
	v_cndmask_b32_e32 v100, v100, v101, vcc
	v_rsq_f32_e32 v104, v100
	v_lshlrev_b64 v[100:101], s15, v[114:115]
	v_lshl_add_u64 v[100:101], v[100:101], 1, v[150:151]
	v_mul_f32_e32 v105, 0x45800000, v104
	v_cndmask_b32_e32 v104, v104, v105, vcc
	v_mul_f32_e32 v104, 0x3d800000, v104
	v_pk_mul_f32 v[96:97], v[96:97], v[104:105] op_sel_hi:[1,0]
	v_pk_mul_f32 v[94:95], v[94:95], v[104:105] op_sel_hi:[1,0]
	v_pk_mul_f32 v[92:93], v[92:93], v[104:105] op_sel_hi:[1,0]
	v_pk_mul_f32 v[90:91], v[90:91], v[104:105] op_sel_hi:[1,0]
	v_pk_mul_f32 v[88:89], v[88:89], v[104:105] op_sel_hi:[1,0]
	v_pk_mul_f32 v[86:87], v[86:87], v[104:105] op_sel_hi:[1,0]
	v_pk_mul_f32 v[106:107], v[84:85], v[104:105] op_sel_hi:[1,0]
	v_pk_mul_f32 v[104:105], v[82:83], v[104:105] op_sel_hi:[1,0]
	v_cvt_pk_bf16_f32 v82, v94, v95
	v_cvt_pk_bf16_f32 v83, v96, v97
	v_cvt_pk_bf16_f32 v84, v90, v91
	v_cvt_pk_bf16_f32 v85, v92, v93
	global_store_dwordx4 v[100:101], v[82:85], off sc0 sc1
	s_nop 1
	v_cvt_pk_bf16_f32 v82, v86, v87
	v_cvt_pk_bf16_f32 v83, v88, v89
	v_cvt_pk_bf16_f32 v84, v104, v105
	v_cvt_pk_bf16_f32 v85, v106, v107
	global_store_dwordx4 v[100:101], v[82:85], off offset:256 sc0 sc1
	global_load_dword v82, v[102:103], off
	s_waitcnt vmcnt(0)
; __device__ __forceinline__ unsigned cvt_pk_bf16(float lo, float hi) { unsigned r; asm volatile("v_cvt_pk_bf16_f32 %0, %1, %2" : "=v"(r) : "v"(lo), "v"(hi)); return r; }
;     __device__ __forceinline__ void operator()(const f32x4 (&acc)[2][2][4][2], const Unit& u, int wr, int wc, int fr, int fq) const {
;         bf16_t* base; int ld, colt;
;         if (u.pn < ntile0) { base = O0; ld = ld0; colt = u.pn * BM; }
;         else { const int q = u.pn - ntile0, per = ld1 / BM; base = O1 + (size_t)(q / per) * stride1; ld = ld1; colt = (q % per) * BM; }
;         const int row0 = u.pm * BM + wr * 64 + fr, col0 = colt + wc * 32 + 8 * fq;
; #pragma unroll
;         for (int ai = 0; ai < 2; ++ai)
; #pragma unroll
;             for (int m = 0; m < 4; ++m) {
;                 const int row = row0 + ai * HALF + m * 16;
;                 float sc = cs; if (ssq) sc *= rsqrtf(ssq[row] * (1.0f / 1024.0f) + 1e-6f);
;                 bf16_t* rowp = base + (size_t)row * ld + col0;
; #pragma unroll
;                 for (int bj = 0; bj < 2; ++bj) { const f32x4 v0 = acc[ai][bj][m][0] * sc, v1 = acc[ai][bj][m][1] * sc;
;                     u32x4 w; w.x = cvt_pk_bf16(v0[0], v0[1]); w.y = cvt_pk_bf16(v0[2], v0[3]); w.z = cvt_pk_bf16(v1[0], v1[1]); w.w = cvt_pk_bf16(v1[2], v1[3]);
;                     *(u32x4*)(rowp + bj * HALF) = w; } }
	v_fmamk_f32 v82, v82, 0x3a800000, v158
	v_mul_f32_e32 v83, 0x4b800000, v82
	v_cmp_gt_f32_e32 vcc, s47, v82
	s_nop 1
	v_cndmask_b32_e32 v82, v82, v83, vcc
	v_rsq_f32_e32 v84, v82
	v_lshlrev_b64 v[82:83], s15, v[98:99]
	v_lshl_add_u64 v[82:83], v[82:83], 1, v[150:151]
	v_mul_f32_e32 v85, 0x45800000, v84
	v_cndmask_b32_e32 v84, v84, v85, vcc
	v_mul_f32_e32 v84, 0x3d800000, v84
	v_pk_mul_f32 v[80:81], v[80:81], v[84:85] op_sel_hi:[1,0]
	v_pk_mul_f32 v[78:79], v[78:79], v[84:85] op_sel_hi:[1,0]
	v_pk_mul_f32 v[76:77], v[76:77], v[84:85] op_sel_hi:[1,0]
	v_pk_mul_f32 v[74:75], v[74:75], v[84:85] op_sel_hi:[1,0]
	v_pk_mul_f32 v[72:73], v[72:73], v[84:85] op_sel_hi:[1,0]
	v_pk_mul_f32 v[70:71], v[70:71], v[84:85] op_sel_hi:[1,0]
	v_pk_mul_f32 v[86:87], v[68:69], v[84:85] op_sel_hi:[1,0]
	v_pk_mul_f32 v[84:85], v[66:67], v[84:85] op_sel_hi:[1,0]
	v_cvt_pk_bf16_f32 v66, v78, v79
	v_cvt_pk_bf16_f32 v67, v80, v81
	v_cvt_pk_bf16_f32 v68, v74, v75
	v_cvt_pk_bf16_f32 v69, v76, v77
	global_store_dwordx4 v[82:83], v[66:69], off sc0 sc1
	s_nop 1
	v_cvt_pk_bf16_f32 v66, v70, v71
	v_cvt_pk_bf16_f32 v67, v72, v73
	v_cvt_pk_bf16_f32 v68, v84, v85
	v_cvt_pk_bf16_f32 v69, v86, v87
	global_store_dwordx4 v[82:83], v[66:69], off offset:256 sc0 sc1
	global_load_dword v67, v[148:149], off offset:512
	s_nop 0
	v_add_u32_e32 v66, 0x80, v146
	s_waitcnt vmcnt(0)
	v_fmamk_f32 v67, v67, 0x3a800000, v158
	v_mul_f32_e32 v68, 0x4b800000, v67
	v_cmp_gt_f32_e32 vcc, s47, v67
	s_nop 1
	v_cndmask_b32_e32 v67, v67, v68, vcc
	v_rsq_f32_e32 v68, v67
	v_ashrrev_i32_e32 v67, 31, v66
	v_lshlrev_b64 v[66:67], s15, v[66:67]
	v_lshl_add_u64 v[66:67], v[66:67], 1, v[150:151]
	v_mul_f32_e32 v69, 0x45800000, v68
	v_cndmask_b32_e32 v68, v68, v69, vcc
	v_mul_f32_e32 v68, 0x3d800000, v68
	v_pk_mul_f32 v[64:65], v[64:65], v[68:69] op_sel_hi:[1,0]
	v_pk_mul_f32 v[62:63], v[62:63], v[68:69] op_sel_hi:[1,0]
	v_pk_mul_f32 v[60:61], v[60:61], v[68:69] op_sel_hi:[1,0]
	v_pk_mul_f32 v[58:59], v[58:59], v[68:69] op_sel_hi:[1,0]
	v_pk_mul_f32 v[56:57], v[56:57], v[68:69] op_sel_hi:[1,0]
	v_pk_mul_f32 v[54:55], v[54:55], v[68:69] op_sel_hi:[1,0]
	v_pk_mul_f32 v[70:71], v[52:53], v[68:69] op_sel_hi:[1,0]
	v_pk_mul_f32 v[68:69], v[50:51], v[68:69] op_sel_hi:[1,0]
	v_cvt_pk_bf16_f32 v50, v62, v63
	v_cvt_pk_bf16_f32 v51, v64, v65
	v_cvt_pk_bf16_f32 v52, v58, v59
	v_cvt_pk_bf16_f32 v53, v60, v61
	global_store_dwordx4 v[66:67], v[50:53], off sc0 sc1
	s_nop 1
	v_cvt_pk_bf16_f32 v50, v54, v55
	v_cvt_pk_bf16_f32 v51, v56, v57
	v_cvt_pk_bf16_f32 v52, v68, v69
	v_cvt_pk_bf16_f32 v53, v70, v71
	global_store_dwordx4 v[66:67], v[50:53], off offset:256 sc0 sc1
	global_load_dword v51, v[148:149], off offset:576
	s_nop 0
	v_add_u32_e32 v50, 0x90, v146
	s_waitcnt vmcnt(0)
	v_fmamk_f32 v51, v51, 0x3a800000, v158
	v_mul_f32_e32 v52, 0x4b800000, v51
	v_cmp_gt_f32_e32 vcc, s47, v51
	s_nop 1
	v_cndmask_b32_e32 v51, v51, v52, vcc
	v_rsq_f32_e32 v52, v51
	v_ashrrev_i32_e32 v51, 31, v50
	v_lshlrev_b64 v[50:51], s15, v[50:51]
	v_lshl_add_u64 v[50:51], v[50:51], 1, v[150:151]
	v_mul_f32_e32 v53, 0x45800000, v52
	v_cndmask_b32_e32 v52, v52, v53, vcc
	v_mul_f32_e32 v52, 0x3d800000, v52
	v_pk_mul_f32 v[48:49], v[48:49], v[52:53] op_sel_hi:[1,0]
	v_pk_mul_f32 v[46:47], v[46:47], v[52:53] op_sel_hi:[1,0]
	v_pk_mul_f32 v[44:45], v[44:45], v[52:53] op_sel_hi:[1,0]
	v_pk_mul_f32 v[42:43], v[42:43], v[52:53] op_sel_hi:[1,0]
	v_pk_mul_f32 v[40:41], v[40:41], v[52:53] op_sel_hi:[1,0]
	v_pk_mul_f32 v[38:39], v[38:39], v[52:53] op_sel_hi:[1,0]
	v_pk_mul_f32 v[54:55], v[36:37], v[52:53] op_sel_hi:[1,0]
	v_pk_mul_f32 v[52:53], v[34:35], v[52:53] op_sel_hi:[1,0]
	v_cvt_pk_bf16_f32 v34, v46, v47
	v_cvt_pk_bf16_f32 v35, v48, v49
	v_cvt_pk_bf16_f32 v36, v42, v43
	v_cvt_pk_bf16_f32 v37, v44, v45
	global_store_dwordx4 v[50:51], v[34:37], off sc0 sc1
	s_nop 1
	v_cvt_pk_bf16_f32 v34, v38, v39
	v_cvt_pk_bf16_f32 v35, v40, v41
	v_cvt_pk_bf16_f32 v36, v52, v53
	v_cvt_pk_bf16_f32 v37, v54, v55
	global_store_dwordx4 v[50:51], v[34:37], off offset:256 sc0 sc1
	global_load_dword v35, v[148:149], off offset:640
	s_nop 0
	v_add_u32_e32 v34, 0xa0, v146
	s_waitcnt vmcnt(0)
	v_fmamk_f32 v35, v35, 0x3a800000, v158
	v_mul_f32_e32 v36, 0x4b800000, v35
	v_cmp_gt_f32_e32 vcc, s47, v35
	s_nop 1
	v_cndmask_b32_e32 v35, v35, v36, vcc
	v_rsq_f32_e32 v36, v35
	v_ashrrev_i32_e32 v35, 31, v34
	v_lshlrev_b64 v[34:35], s15, v[34:35]
	v_lshl_add_u64 v[34:35], v[34:35], 1, v[150:151]
	v_mul_f32_e32 v37, 0x45800000, v36
	v_cndmask_b32_e32 v36, v36, v37, vcc
	v_mul_f32_e32 v36, 0x3d800000, v36
	v_pk_mul_f32 v[32:33], v[32:33], v[36:37] op_sel_hi:[1,0]
	v_pk_mul_f32 v[30:31], v[30:31], v[36:37] op_sel_hi:[1,0]
	v_pk_mul_f32 v[28:29], v[28:29], v[36:37] op_sel_hi:[1,0]
	v_pk_mul_f32 v[26:27], v[26:27], v[36:37] op_sel_hi:[1,0]
	v_pk_mul_f32 v[24:25], v[24:25], v[36:37] op_sel_hi:[1,0]
	v_pk_mul_f32 v[22:23], v[22:23], v[36:37] op_sel_hi:[1,0]
	v_pk_mul_f32 v[38:39], v[20:21], v[36:37] op_sel_hi:[1,0]
	v_pk_mul_f32 v[36:37], v[18:19], v[36:37] op_sel_hi:[1,0]
	v_cvt_pk_bf16_f32 v18, v30, v31
	v_cvt_pk_bf16_f32 v19, v32, v33
	v_cvt_pk_bf16_f32 v20, v26, v27
	v_cvt_pk_bf16_f32 v21, v28, v29
	global_store_dwordx4 v[34:35], v[18:21], off sc0 sc1
	s_andn2_b64 vcc, exec, s[4:5]
	s_nop 0
	v_cvt_pk_bf16_f32 v18, v22, v23
	v_cvt_pk_bf16_f32 v19, v24, v25
	v_cvt_pk_bf16_f32 v20, v36, v37
	v_cvt_pk_bf16_f32 v21, v38, v39
	global_store_dwordx4 v[34:35], v[18:21], off offset:256 sc0 sc1
	global_load_dword v20, v[148:149], off offset:704
	s_nop 0
	v_add_u32_e32 v18, 0xb0, v146
	v_ashrrev_i32_e32 v19, 31, v18
	v_lshlrev_b64 v[18:19], s15, v[18:19]
	v_lshl_add_u64 v[18:19], v[18:19], 1, v[150:151]
	s_waitcnt vmcnt(0)
	v_fmamk_f32 v20, v20, 0x3a800000, v158
	v_mul_f32_e32 v21, 0x4b800000, v20
	v_cmp_gt_f32_e64 s[0:1], s47, v20
	s_nop 1
	v_cndmask_b32_e64 v20, v20, v21, s[0:1]
	v_rsq_f32_e32 v20, v20
	s_nop 0
	v_mul_f32_e32 v21, 0x45800000, v20
	v_cndmask_b32_e64 v20, v20, v21, s[0:1]
	v_mul_f32_e32 v20, 0x3d800000, v20
	v_pk_mul_f32 v[16:17], v[16:17], v[20:21] op_sel_hi:[1,0]
	v_pk_mul_f32 v[14:15], v[14:15], v[20:21] op_sel_hi:[1,0]
	v_pk_mul_f32 v[12:13], v[12:13], v[20:21] op_sel_hi:[1,0]
	v_pk_mul_f32 v[10:11], v[10:11], v[20:21] op_sel_hi:[1,0]
	v_pk_mul_f32 v[8:9], v[8:9], v[20:21] op_sel_hi:[1,0]
	v_pk_mul_f32 v[6:7], v[6:7], v[20:21] op_sel_hi:[1,0]
	v_pk_mul_f32 v[22:23], v[4:5], v[20:21] op_sel_hi:[1,0]
	v_pk_mul_f32 v[20:21], v[2:3], v[20:21] op_sel_hi:[1,0]
	v_cvt_pk_bf16_f32 v2, v14, v15
	v_cvt_pk_bf16_f32 v3, v16, v17
	v_cvt_pk_bf16_f32 v4, v10, v11
	v_cvt_pk_bf16_f32 v5, v12, v13
	s_mov_b64 s[0:1], -1
	global_store_dwordx4 v[18:19], v[2:5], off sc0 sc1
	s_nop 1
	v_cvt_pk_bf16_f32 v2, v6, v7
	v_cvt_pk_bf16_f32 v3, v8, v9
	v_cvt_pk_bf16_f32 v4, v20, v21
	v_cvt_pk_bf16_f32 v5, v22, v23
	global_store_dwordx4 v[18:19], v[2:5], off offset:256 sc0 sc1
	s_cbranch_vccnz .LBB0_2431
	s_andn2_b64 vcc, exec, s[6:7]
	s_cbranch_vccnz .LBB0_2430
	s_barrier
	s_branch .LBB0_2430

; #define LAS __attribute__((address_space(3)))
; __device__ __forceinline__ void xattn_stage(LAS unsigned char* lds, const bf16* src, int tid) {
;     v4u tmp[16];
;     asm volatile("" : "+v"(tid));
;     const unsigned voff = (unsigned)tid * 16u;
; #pragma unroll
;     for (int r = 0; r < 16; ++r) { const unsigned char* sb = (const unsigned char*)src + r * 8192;
;         asm volatile("s_nop 4\n\tglobal_load_dwordx4 %0, %1, %2" : "=&v"(tmp[r]) : "v"(voff), "s"(sb) : "memory"); }
;     asm volatile("s_waitcnt vmcnt(0)" : "+v"(tmp[0]), "+v"(tmp[1]), "+v"(tmp[2]), "+v"(tmp[3]), "+v"(tmp[4]), "+v"(tmp[5]), "+v"(tmp[6]), "+v"(tmp[7]),
;                                         "+v"(tmp[8]), "+v"(tmp[9]), "+v"(tmp[10]), "+v"(tmp[11]), "+v"(tmp[12]), "+v"(tmp[13]), "+v"(tmp[14]), "+v"(tmp[15]) :: "memory");
; #pragma unroll
;     for (int r = 0; r < 16; ++r) { const int id = tid + 512 * r; *(LAS v4u*)(lds + (id >> 5) * 528 + (id & 31) * 16) = tmp[r]; }
; __global__ void __launch_bounds__(NWAVES * 64, 2) hybrid_fwd(Params P) {
;     ...
;         { const int wgid = (bx & 7) * 32 + (bx >> 3); u.pm = (wgid >> 5) * 8 + (wgid & 7); u.pn = (wgid & 31) >> 3; }
;         if (G == 256) {
;             asm volatile("s_waitcnt vmcnt(0)" ::: "memory");
;             __syncthreads();
;             const int b = u.pm >> 5, qb0 = (u.pm & 31) * 2, h = u.pn;
; #pragma unroll 1
;             for (int qq = 0; qq < (((TWICE_MASK >> 7) & 1) ? 4 : 2); qq += XA_NPS) xattn_unit(P, lds, (b << 8) | ((qb0 + (qq & 1)) << 2) | h, tid, lane, wave);
.LBB0_2446:
	s_cmpk_lg_i32 s26, 0x100
	s_cbranch_scc1 .LBB0_2448
	s_lshl_b32 s1, s2, 5
	s_ashr_i32 s0, s2, 3
	s_and_b32 s1, s1, 0xe0
	s_add_i32 s1, s1, s0
	s_lshr_b32 s4, s1, 2
	s_and_b32 s4, s4, 24
	s_and_b32 s5, s0, 7
	s_or_b32 s4, s4, s5
	s_ashr_i32 s1, s1, 7
	s_lshl_b32 s5, s1, 13
	s_lshl_b32 s4, s4, 8
	s_or_b32 s23, s4, s5
	v_readlane_b32 s4, v254, 56
	s_lshl_b32 s4, s4, 4
	s_lshl_b32 s0, s0, 5
	s_add_i32 s23, s23, s4
	s_lshl_b32 s1, s1, 10
	s_and_b32 s4, s0, 0x300
	s_or_b32 s0, s1, s4
	s_ashr_i32 s1, s0, 31
	s_lshl_b64 s[0:1], s[0:1], 9
	s_add_u32 s0, s24, s0
	s_addc_u32 s1, s25, s1
	s_add_u32 s54, s0, 0x1900000
	s_addc_u32 s55, s1, 0
	s_add_u32 s56, s0, 0x1902000
	s_addc_u32 s57, s1, 0
	s_add_u32 s58, s0, 0x1904000
	s_addc_u32 s59, s1, 0
	s_add_u32 s60, s0, 0x1906000
	s_addc_u32 s61, s1, 0
	s_add_u32 s62, s0, 0x1908000
	s_addc_u32 s63, s1, 0
	s_add_u32 s64, s0, 0x190a000
	s_addc_u32 s65, s1, 0
	s_add_u32 s66, s0, 0x190c000
	s_addc_u32 s67, s1, 0
	s_add_u32 s68, s0, 0x190e000
	s_addc_u32 s69, s1, 0
	v_mul_u32_u24_e32 v2, 0x210, v1
	s_waitcnt lgkmcnt(0)
	v_and_b32_e32 v3, 48, v0
	v_mov_b32_e32 v67, v0
	s_add_u32 s70, s0, 0x1910000
	v_add3_u32 v191, 0, v2, v3
	s_waitcnt vmcnt(0)
	s_waitcnt vmcnt(0)
	s_barrier
	s_addc_u32 s71, s1, 0
	v_lshlrev_b32_e32 v66, 4, v67
	s_nop 4
	global_load_dwordx4 v[2:5], v66, s[54:55]
	s_nop 4
	global_load_dwordx4 v[6:9], v66, s[56:57]
	s_add_u32 s76, s0, 0x1912000
	s_nop 4
	global_load_dwordx4 v[10:13], v66, s[58:59]
	s_addc_u32 s77, s1, 0
	s_nop 4
	global_load_dwordx4 v[14:17], v66, s[60:61]
	s_add_u32 s52, s0, 0x1914000
	s_nop 4
	global_load_dwordx4 v[18:21], v66, s[62:63]
	s_addc_u32 s53, s1, 0
	s_nop 4
	global_load_dwordx4 v[22:25], v66, s[64:65]
	s_mov_b64 s[34:35], s[78:79]
	s_add_u32 s78, s0, 0x1916000
	s_nop 4
	global_load_dwordx4 v[26:29], v66, s[66:67]
	s_addc_u32 s79, s1, 0
	s_nop 4
	global_load_dwordx4 v[30:33], v66, s[68:69]
	s_add_u32 s82, s0, 0x1918000
	s_nop 4
	global_load_dwordx4 v[34:37], v66, s[70:71]
	s_addc_u32 s83, s1, 0
	s_nop 4
	global_load_dwordx4 v[38:41], v66, s[76:77]
	s_add_u32 s84, s0, 0x191a000
	s_nop 4
	global_load_dwordx4 v[42:45], v66, s[52:53]
	s_addc_u32 s85, s1, 0
	s_nop 4
	global_load_dwordx4 v[46:49], v66, s[78:79]
	s_add_u32 s30, s0, 0x191c000
	s_nop 4
	global_load_dwordx4 v[50:53], v66, s[82:83]
	s_addc_u32 s31, s1, 0
	s_nop 4
	global_load_dwordx4 v[54:57], v66, s[84:85]
	s_add_u32 s86, s0, 0x191e000
	s_nop 4
	global_load_dwordx4 v[58:61], v66, s[30:31]
	s_addc_u32 s87, s1, 0
	s_lshl_b32 s22, s4, 1
	s_nop 4
	global_load_dwordx4 v[62:65], v66, s[86:87]
	v_and_b32_e32 v66, 0x1f0, v66
	s_movk_i32 s27, 0x210
	s_add_u32 s50, s3, s22
	v_add_u32_e32 v66, 0, v66
	v_ashrrev_i32_e32 v68, 5, v67
	s_addc_u32 s51, s28, 0
	s_waitcnt vmcnt(0)
	v_mad_u64_u32 v[68:69], s[28:29], v68, s27, v[66:67]
	ds_write_b128 v68, v[2:5]
	v_add_u32_e32 v2, 0x200, v67
	v_ashrrev_i32_e32 v2, 5, v2
	v_mad_u64_u32 v[2:3], s[28:29], v2, s27, v[66:67]
	ds_write_b128 v2, v[6:9]
	v_add_u32_e32 v2, 0x400, v67
	v_ashrrev_i32_e32 v2, 5, v2
	v_mad_u64_u32 v[2:3], s[28:29], v2, s27, v[66:67]
	ds_write_b128 v2, v[10:13]
	v_add_u32_e32 v2, 0x600, v67
	v_ashrrev_i32_e32 v2, 5, v2
	v_mad_u64_u32 v[2:3], s[28:29], v2, s27, v[66:67]
	s_add_i32 s3, s23, 0x80
	ds_write_b128 v2, v[14:17]
	v_add_u32_e32 v2, 0x800, v67
	v_readlane_b32 s5, v254, 57
	s_add_u32 s4, s0, 0x1a00000
	v_ashrrev_i32_e32 v2, 5, v2
	s_addc_u32 s5, s1, 0
	v_mad_u64_u32 v[2:3], s[28:29], v2, s27, v[66:67]
	s_add_u32 s6, s0, 0x1a02000
	ds_write_b128 v2, v[18:21]
	v_add_u32_e32 v2, 0xa00, v67
	s_addc_u32 s7, s1, 0
	v_ashrrev_i32_e32 v2, 5, v2
	s_add_u32 s8, s0, 0x1a04000
	v_mad_u64_u32 v[2:3], s[28:29], v2, s27, v[66:67]
	s_addc_u32 s9, s1, 0
	ds_write_b128 v2, v[22:25]
	v_add_u32_e32 v2, 0xc00, v67
	s_add_u32 s10, s0, 0x1a06000
	v_ashrrev_i32_e32 v2, 5, v2
	s_addc_u32 s11, s1, 0
	v_mad_u64_u32 v[2:3], s[28:29], v2, s27, v[66:67]
	s_add_u32 s12, s0, 0x1a08000
	ds_write_b128 v2, v[26:29]
	v_add_u32_e32 v2, 0xe00, v67
	s_addc_u32 s13, s1, 0
	v_ashrrev_i32_e32 v2, 5, v2
	s_add_u32 s14, s0, 0x1a0a000
	v_mad_u64_u32 v[2:3], s[28:29], v2, s27, v[66:67]
	s_addc_u32 s15, s1, 0
	ds_write_b128 v2, v[30:33]
	v_add_u32_e32 v2, 0x1000, v67
	s_add_u32 s16, s0, 0x1a0c000
	v_ashrrev_i32_e32 v2, 5, v2
	s_addc_u32 s17, s1, 0
	v_mad_u64_u32 v[2:3], s[28:29], v2, s27, v[66:67]
	s_add_u32 s18, s0, 0x1a0e000
	ds_write_b128 v2, v[34:37]
	v_add_u32_e32 v2, 0x1200, v67
	s_addc_u32 s19, s1, 0
	v_ashrrev_i32_e32 v2, 5, v2
	s_add_u32 s20, s0, 0x1a10000
	v_mad_u64_u32 v[2:3], s[28:29], v2, s27, v[66:67]
	s_addc_u32 s21, s1, 0
	ds_write_b128 v2, v[38:41]
	v_add_u32_e32 v2, 0x1400, v67
	s_add_u32 s36, s0, 0x1a12000
	v_ashrrev_i32_e32 v2, 5, v2
	s_addc_u32 s37, s1, 0
	v_mad_u64_u32 v[2:3], s[28:29], v2, s27, v[66:67]
	s_add_u32 s38, s0, 0x1a14000
	ds_write_b128 v2, v[42:45]
	v_add_u32_e32 v2, 0x1600, v67
	s_addc_u32 s39, s1, 0
	v_ashrrev_i32_e32 v2, 5, v2
	s_add_u32 s40, s0, 0x1a16000
	v_mad_u64_u32 v[2:3], s[28:29], v2, s27, v[66:67]
	s_addc_u32 s41, s1, 0
	ds_write_b128 v2, v[46:49]
	v_add_u32_e32 v2, 0x1800, v67
	s_add_u32 s42, s0, 0x1a18000
	v_ashrrev_i32_e32 v2, 5, v2
	s_addc_u32 s43, s1, 0
	v_mad_u64_u32 v[2:3], s[28:29], v2, s27, v[66:67]
	s_add_u32 s44, s0, 0x1a1a000
	ds_write_b128 v2, v[50:53]
	v_add_u32_e32 v2, 0x1a00, v67
	s_addc_u32 s45, s1, 0
	v_ashrrev_i32_e32 v2, 5, v2
	s_add_u32 s46, s0, 0x1a1c000
	v_mad_u64_u32 v[2:3], s[28:29], v2, s27, v[66:67]
	s_addc_u32 s47, s1, 0
	ds_write_b128 v2, v[54:57]
	v_add_u32_e32 v2, 0x1c00, v67
	s_add_u32 s48, s0, 0x1a1e000
	v_ashrrev_i32_e32 v2, 5, v2
	s_addc_u32 s49, s1, 0
	v_mad_u64_u32 v[2:3], s[28:29], v2, s27, v[66:67]
; __device__ __forceinline__ void xattn_stage(LAS unsigned char* lds, const bf16* src, int tid) {
;     ...
;     for (int r = 0; r < 16; ++r) { const unsigned char* sb = (const unsigned char*)src + r * 8192;
;         asm volatile("s_nop 4\n\tglobal_load_dwordx4 %0, %1, %2" : "=&v"(tmp[r]) : "v"(voff), "s"(sb) : "memory"); }
;     asm volatile("s_waitcnt vmcnt(0)" : "+v"(tmp[0]), "+v"(tmp[1]), "+v"(tmp[2]), "+v"(tmp[3]), "+v"(tmp[4]), "+v"(tmp[5]), "+v"(tmp[6]), "+v"(tmp[7]),
;                                         "+v"(tmp[8]), "+v"(tmp[9]), "+v"(tmp[10]), "+v"(tmp[11]), "+v"(tmp[12]), "+v"(tmp[13]), "+v"(tmp[14]), "+v"(tmp[15]) :: "memory");
; #pragma unroll
;     for (int r = 0; r < 16; ++r) { const int id = tid + 512 * r; *(LAS v4u*)(lds + (id >> 5) * 528 + (id & 31) * 16) = tmp[r]; }
; }
; __device__ __forceinline__ void xattn_unit(const Params& P, LAS unsigned char* lds, int unit, int tid, int lane, int wave) {
;     const unsigned char* ws = P.ws;
;     const int h = unit & 3, qb = (unit >> 2) & 63, b = unit >> 8; int col = lane & 15, g = lane >> 4;
;     const int tw = b * SEQ + qb * 128 + 16 * wave;
;     const bf16* Kb = (const bf16*)(ws + WS_KB) + (size_t)((b * 4 + h) * 256) * 256;
;     const bf16* Vt = (const bf16*)(ws + WS_VTP) + (size_t)((b * 4 + h) * 256) * 256;
;     xattn_stage(lds, Kb, tid);
;     __syncthreads();
;     const LAS unsigned char* arow = lds + col * 528 + g * 16;
;     bf16x8 Bp[XA_NPS][8]; float inv[XA_NPS];
; #pragma unroll
;     for (int ps = 0; ps < XA_NPS; ++ps) {
;         __builtin_amdgcn_sched_barrier(0); asm volatile("" : "+v"(col), "+v"(g) :: "memory");
;         const bf16* Q = (const bf16*)(ws + WS_Q) + (size_t)(tw + 128 * ps + col) * 1024 + h * 256 + 8 * g;
;         bf16x8 Bq[8];
; #pragma unroll
;         for (int s = 0; s < 8; ++s) Bq[s] = *(const bf16x8*)(Q + 32 * s);
;         f32x4 St[16];
;         bf16x8 fr[2][8];
; #pragma unroll
;         for (int s = 0; s < 8; ++s) fr[0][s] = *(const LAS bf16x8*)(arow + 64 * s);
; #pragma unroll
;         for (int kap = 0; kap < 16; ++kap) {
;             if (kap + 1 < 16) {
; #pragma unroll
;                 for (int s = 0; s < 8; ++s) fr[(kap + 1) & 1][s] = *(const LAS bf16x8*)(arow + (16 * (kap + 1)) * 528 + 64 * s);
;             }
;             __builtin_amdgcn_sched_barrier(0);
;             PIN8(fr[kap & 1]);
;             f32x4 acc = (f32x4){0.f, 0.f, 0.f, 0.f};
	s_add_u32 s0, s24, s22
	ds_write_b128 v2, v[58:61]
	v_add_u32_e32 v2, 0x1e00, v67
	s_addc_u32 s1, s25, 0
	v_readlane_b32 s72, v255, 2
	v_ashrrev_i32_e32 v2, 5, v2
	s_add_u32 s0, s0, 0x7c00000
	v_readlane_b32 s73, v255, 3
	s_mov_b64 s[78:79], s[34:35]
	v_mad_u64_u32 v[2:3], s[28:29], v2, s27, v[66:67]
	v_lshrrev_b32_e32 v192, 4, v182
	v_add_u32_e32 v183, 0x10800, v191
	v_add_u32_e32 v184, 0x10840, v191
	v_add_u32_e32 v185, 0x10880, v191
	v_add_u32_e32 v186, 0x108c0, v191
	v_add_u32_e32 v187, 0x10900, v191
	v_add_u32_e32 v188, 0x10940, v191
	v_add_u32_e32 v189, 0x10980, v191
	v_add_u32_e32 v190, 0x109c0, v191
	v_add_u32_e32 v175, 0x12900, v191
	v_add_u32_e32 v176, 0x12940, v191
	v_add_u32_e32 v177, 0x12980, v191
	v_add_u32_e32 v178, 0x129c0, v191
	v_add_u32_e32 v179, 0x12a00, v191
	v_add_u32_e32 v180, 0x12a40, v191
	v_add_u32_e32 v181, 0x12a80, v191
	v_add_u32_e32 v182, 0x12ac0, v191
	v_add_u32_e32 v167, 0x14a00, v191
	v_add_u32_e32 v168, 0x14a40, v191
	v_add_u32_e32 v169, 0x14a80, v191
	v_add_u32_e32 v170, 0x14ac0, v191
	v_add_u32_e32 v171, 0x14b00, v191
	v_add_u32_e32 v172, 0x14b40, v191
	v_add_u32_e32 v173, 0x14b80, v191
	v_add_u32_e32 v174, 0x14bc0, v191
	v_add_u32_e32 v159, 0x16b00, v191
	v_add_u32_e32 v160, 0x16b40, v191
	v_add_u32_e32 v161, 0x16b80, v191
	v_add_u32_e32 v162, 0x16bc0, v191
	v_add_u32_e32 v163, 0x16c00, v191
	v_add_u32_e32 v164, 0x16c40, v191
	v_add_u32_e32 v165, 0x16c80, v191
	v_add_u32_e32 v166, 0x16cc0, v191
	v_add_u32_e32 v151, 0x18c00, v191
	v_add_u32_e32 v152, 0x18c40, v191
	v_add_u32_e32 v153, 0x18c80, v191
	v_add_u32_e32 v154, 0x18cc0, v191
	v_add_u32_e32 v155, 0x18d00, v191
	v_add_u32_e32 v156, 0x18d40, v191
	v_add_u32_e32 v157, 0x18d80, v191
	v_add_u32_e32 v158, 0x18dc0, v191
	v_add_u32_e32 v143, 0x1ad00, v191
	v_add_u32_e32 v144, 0x1ad40, v191
	v_add_u32_e32 v145, 0x1ad80, v191
	v_add_u32_e32 v146, 0x1adc0, v191
	v_add_u32_e32 v147, 0x1ae00, v191
	v_add_u32_e32 v148, 0x1ae40, v191
	v_add_u32_e32 v149, 0x1ae80, v191
	v_add_u32_e32 v150, 0x1aec0, v191
	v_add_u32_e32 v135, 0x1ce00, v191
	v_add_u32_e32 v136, 0x1ce40, v191
	v_add_u32_e32 v137, 0x1ce80, v191
	v_add_u32_e32 v138, 0x1cec0, v191
	v_add_u32_e32 v139, 0x1cf00, v191
	v_add_u32_e32 v140, 0x1cf40, v191
	v_add_u32_e32 v141, 0x1cf80, v191
	v_add_u32_e32 v142, 0x1cfc0, v191
	v_add_u32_e32 v127, 0x1ef00, v191
	v_add_u32_e32 v132, 0x1ef40, v191
	v_add_u32_e32 v129, 0x1ef80, v191
	v_add_u32_e32 v253, 0x1efc0, v191
	v_add_u32_e32 v128, 0x1f000, v191
	v_add_u32_e32 v252, 0x1f040, v191
	v_add_u32_e32 v133, 0x1f080, v191
	v_add_u32_e32 v134, 0x1f0c0, v191
	s_addc_u32 s1, s1, 0
	ds_write_b128 v2, v[62:65]
	s_waitcnt lgkmcnt(0)
	s_barrier
	s_nop 0
	v_add_u32_e32 v2, s23, v1
	v_ashrrev_i32_e32 v3, 31, v2
	v_lshlrev_b32_e32 v4, 3, v192
	v_lshlrev_b64 v[2:3], 11, v[2:3]
	v_ashrrev_i32_e32 v5, 31, v4
	v_lshl_add_u64 v[2:3], s[50:51], 0, v[2:3]
	v_lshl_add_u64 v[2:3], v[4:5], 1, v[2:3]
	global_load_dwordx4 v[62:65], v[2:3], off
	global_load_dwordx4 v[66:69], v[2:3], off offset:64
	global_load_dwordx4 v[70:73], v[2:3], off offset:128
	global_load_dwordx4 v[74:77], v[2:3], off offset:192
	global_load_dwordx4 v[78:81], v[2:3], off offset:256
	global_load_dwordx4 v[82:85], v[2:3], off offset:320
	global_load_dwordx4 v[86:89], v[2:3], off offset:384
	global_load_dwordx4 v[90:93], v[2:3], off offset:448
	ds_read_b128 v[2:5], v191 offset:448
	ds_read_b128 v[6:9], v191 offset:384
	ds_read_b128 v[10:13], v191 offset:320
	ds_read_b128 v[14:17], v191 offset:256
	ds_read_b128 v[18:21], v191 offset:192
	ds_read_b128 v[22:25], v191 offset:128
	ds_read_b128 v[26:29], v191 offset:64
	ds_read_b128 v[30:33], v191
	ds_read_b128 v[34:37], v191 offset:8896
	ds_read_b128 v[38:41], v191 offset:8832
	ds_read_b128 v[42:45], v191 offset:8768
	ds_read_b128 v[46:49], v191 offset:8704
	ds_read_b128 v[50:53], v191 offset:8640
	ds_read_b128 v[54:57], v191 offset:8576
	ds_read_b128 v[58:61], v191 offset:8512
	ds_read_b128 v[94:97], v191 offset:8448
	s_waitcnt lgkmcnt(8)
	s_waitcnt vmcnt(7)
	v_mfma_f32_16x16x32_bf16 v[30:33], v[30:33], v[62:65], 0
	s_waitcnt vmcnt(6)
	v_mfma_f32_16x16x32_bf16 v[26:29], v[26:29], v[66:69], v[30:33]
	s_waitcnt vmcnt(5)
	v_mfma_f32_16x16x32_bf16 v[22:25], v[22:25], v[70:73], v[26:29]
	s_waitcnt vmcnt(4)
	v_mfma_f32_16x16x32_bf16 v[18:21], v[18:21], v[74:77], v[22:25]
	s_waitcnt vmcnt(3)
	v_mfma_f32_16x16x32_bf16 v[14:17], v[14:17], v[78:81], v[18:21]
	s_waitcnt vmcnt(2)
	v_mfma_f32_16x16x32_bf16 v[10:13], v[10:13], v[82:85], v[14:17]
	s_waitcnt vmcnt(1)
	v_mfma_f32_16x16x32_bf16 v[6:9], v[6:9], v[86:89], v[10:13]
	s_waitcnt vmcnt(0)
	v_mfma_f32_16x16x32_bf16 v[2:5], v[2:5], v[90:93], v[6:9]
	s_nop 3
	ds_read_b128 v[10:13], v191 offset:17344
	ds_read_b128 v[14:17], v191 offset:17280
	ds_read_b128 v[18:21], v191 offset:17216
	ds_read_b128 v[22:25], v191 offset:17152
	ds_read_b128 v[26:29], v191 offset:17088
	ds_read_b128 v[30:33], v191 offset:17024
	ds_read_b128 v[98:101], v191 offset:16960
	ds_read_b128 v[102:105], v191 offset:16896
	s_waitcnt lgkmcnt(8)
	s_nop 0
	v_mfma_f32_16x16x32_bf16 v[6:9], v[94:97], v[62:65], 0
	v_mfma_f32_16x16x32_bf16 v[6:9], v[58:61], v[66:69], v[6:9]
	v_mfma_f32_16x16x32_bf16 v[6:9], v[54:57], v[70:73], v[6:9]
	v_mfma_f32_16x16x32_bf16 v[6:9], v[50:53], v[74:77], v[6:9]
	v_mfma_f32_16x16x32_bf16 v[6:9], v[46:49], v[78:81], v[6:9]
	v_mfma_f32_16x16x32_bf16 v[6:9], v[42:45], v[82:85], v[6:9]
	v_mfma_f32_16x16x32_bf16 v[6:9], v[38:41], v[86:89], v[6:9]
	v_mfma_f32_16x16x32_bf16 v[6:9], v[34:37], v[90:93], v[6:9]
	ds_read_b128 v[34:37], v191 offset:25792
	ds_read_b128 v[38:41], v191 offset:25728
	ds_read_b128 v[42:45], v191 offset:25664
	ds_read_b128 v[46:49], v191 offset:25600
	ds_read_b128 v[50:53], v191 offset:25536
	ds_read_b128 v[54:57], v191 offset:25472
	ds_read_b128 v[58:61], v191 offset:25408
	ds_read_b128 v[94:97], v191 offset:25344
	s_waitcnt lgkmcnt(8)
; #define LAS __attribute__((address_space(3)))
; #define PIN8(a) asm volatile("" : "+v"(a[0]), "+v"(a[1]), "+v"(a[2]), "+v"(a[3]), "+v"(a[4]), "+v"(a[5]), "+v"(a[6]), "+v"(a[7]))
; __device__ __forceinline__ void xattn_unit(const Params& P, LAS unsigned char* lds, int unit, int tid, int lane, int wave) {
;     ...
;         f32x4 St[16];
;         bf16x8 fr[2][8];
; #pragma unroll
;         for (int s = 0; s < 8; ++s) fr[0][s] = *(const LAS bf16x8*)(arow + 64 * s);
; #pragma unroll
;         for (int kap = 0; kap < 16; ++kap) {
;             if (kap + 1 < 16) {
; #pragma unroll
;                 for (int s = 0; s < 8; ++s) fr[(kap + 1) & 1][s] = *(const LAS bf16x8*)(arow + (16 * (kap + 1)) * 528 + 64 * s);
;             }
;             __builtin_amdgcn_sched_barrier(0);
;             PIN8(fr[kap & 1]);
;             f32x4 acc = (f32x4){0.f, 0.f, 0.f, 0.f};
; #pragma unroll
;             for (int s = 0; s < 8; ++s) acc = __builtin_amdgcn_mfma_f32_16x16x32_bf16(fr[kap & 1][s], Bq[s], acc, 0, 0, 0);
;             St[kap] = acc;
;             __builtin_amdgcn_sched_barrier(0);
;         }
	s_nop 0
	v_mfma_f32_16x16x32_bf16 v[102:105], v[102:105], v[62:65], 0
	v_mfma_f32_16x16x32_bf16 v[98:101], v[98:101], v[66:69], v[102:105]
	v_mfma_f32_16x16x32_bf16 v[30:33], v[30:33], v[70:73], v[98:101]
	v_mfma_f32_16x16x32_bf16 v[26:29], v[26:29], v[74:77], v[30:33]
	v_mfma_f32_16x16x32_bf16 v[22:25], v[22:25], v[78:81], v[26:29]
	v_mfma_f32_16x16x32_bf16 v[18:21], v[18:21], v[82:85], v[22:25]
	v_mfma_f32_16x16x32_bf16 v[14:17], v[14:17], v[86:89], v[18:21]
	v_mfma_f32_16x16x32_bf16 v[10:13], v[10:13], v[90:93], v[14:17]
	s_nop 5
	ds_read_b128 v[18:21], v191 offset:34240
	ds_read_b128 v[22:25], v191 offset:34176
	ds_read_b128 v[26:29], v191 offset:34112
	ds_read_b128 v[30:33], v191 offset:34048
	ds_read_b128 v[98:101], v191 offset:33984
	ds_read_b128 v[102:105], v191 offset:33920
	ds_read_b128 v[106:109], v191 offset:33856
	ds_read_b128 v[110:113], v191 offset:33792
	s_waitcnt lgkmcnt(8)
	s_nop 0
	v_mfma_f32_16x16x32_bf16 v[14:17], v[94:97], v[62:65], 0
	v_mfma_f32_16x16x32_bf16 v[14:17], v[58:61], v[66:69], v[14:17]
	v_mfma_f32_16x16x32_bf16 v[14:17], v[54:57], v[70:73], v[14:17]
	v_mfma_f32_16x16x32_bf16 v[14:17], v[50:53], v[74:77], v[14:17]
	v_mfma_f32_16x16x32_bf16 v[14:17], v[46:49], v[78:81], v[14:17]
	v_mfma_f32_16x16x32_bf16 v[14:17], v[42:45], v[82:85], v[14:17]
	v_mfma_f32_16x16x32_bf16 v[14:17], v[38:41], v[86:89], v[14:17]
	v_mfma_f32_16x16x32_bf16 v[14:17], v[34:37], v[90:93], v[14:17]
	ds_read_b128 v[34:37], v191 offset:42688
	ds_read_b128 v[38:41], v191 offset:42624
	ds_read_b128 v[42:45], v191 offset:42560
	ds_read_b128 v[46:49], v191 offset:42496
	ds_read_b128 v[50:53], v191 offset:42432
	ds_read_b128 v[54:57], v191 offset:42368
	ds_read_b128 v[58:61], v191 offset:42304
	ds_read_b128 v[94:97], v191 offset:42240
	s_waitcnt lgkmcnt(8)
	s_nop 0
	v_mfma_f32_16x16x32_bf16 v[110:113], v[110:113], v[62:65], 0
	v_mfma_f32_16x16x32_bf16 v[106:109], v[106:109], v[66:69], v[110:113]
	v_mfma_f32_16x16x32_bf16 v[102:105], v[102:105], v[70:73], v[106:109]
	v_mfma_f32_16x16x32_bf16 v[98:101], v[98:101], v[74:77], v[102:105]
	v_mfma_f32_16x16x32_bf16 v[30:33], v[30:33], v[78:81], v[98:101]
	v_mfma_f32_16x16x32_bf16 v[26:29], v[26:29], v[82:85], v[30:33]
	v_mfma_f32_16x16x32_bf16 v[22:25], v[22:25], v[86:89], v[26:29]
	v_mfma_f32_16x16x32_bf16 v[18:21], v[18:21], v[90:93], v[22:25]
	s_nop 5
	ds_read_b128 v[26:29], v191 offset:51136
	ds_read_b128 v[30:33], v191 offset:51072
	ds_read_b128 v[98:101], v191 offset:51008
	ds_read_b128 v[102:105], v191 offset:50944
	ds_read_b128 v[106:109], v191 offset:50880
	ds_read_b128 v[110:113], v191 offset:50816
	ds_read_b128 v[114:117], v191 offset:50752
	ds_read_b128 v[118:121], v191 offset:50688
	s_waitcnt lgkmcnt(8)
	s_nop 0
	v_mfma_f32_16x16x32_bf16 v[22:25], v[94:97], v[62:65], 0
	v_mfma_f32_16x16x32_bf16 v[22:25], v[58:61], v[66:69], v[22:25]
	v_mfma_f32_16x16x32_bf16 v[22:25], v[54:57], v[70:73], v[22:25]
	v_mfma_f32_16x16x32_bf16 v[22:25], v[50:53], v[74:77], v[22:25]
	v_mfma_f32_16x16x32_bf16 v[22:25], v[46:49], v[78:81], v[22:25]
	v_mfma_f32_16x16x32_bf16 v[22:25], v[42:45], v[82:85], v[22:25]
	v_mfma_f32_16x16x32_bf16 v[22:25], v[38:41], v[86:89], v[22:25]
	v_mfma_f32_16x16x32_bf16 v[22:25], v[34:37], v[90:93], v[22:25]
	ds_read_b128 v[34:37], v191 offset:59584
	ds_read_b128 v[38:41], v191 offset:59520
	ds_read_b128 v[42:45], v191 offset:59456
	ds_read_b128 v[46:49], v191 offset:59392
	ds_read_b128 v[50:53], v191 offset:59328
	ds_read_b128 v[54:57], v191 offset:59264
	ds_read_b128 v[58:61], v191 offset:59200
	ds_read_b128 v[94:97], v191 offset:59136
	s_waitcnt lgkmcnt(8)
	s_nop 0
	v_mfma_f32_16x16x32_bf16 v[118:121], v[118:121], v[62:65], 0
	v_mfma_f32_16x16x32_bf16 v[114:117], v[114:117], v[66:69], v[118:121]
	v_mfma_f32_16x16x32_bf16 v[110:113], v[110:113], v[70:73], v[114:117]
	v_mfma_f32_16x16x32_bf16 v[106:109], v[106:109], v[74:77], v[110:113]
	v_mfma_f32_16x16x32_bf16 v[102:105], v[102:105], v[78:81], v[106:109]
	v_mfma_f32_16x16x32_bf16 v[98:101], v[98:101], v[82:85], v[102:105]
	v_mfma_f32_16x16x32_bf16 v[30:33], v[30:33], v[86:89], v[98:101]
	v_mfma_f32_16x16x32_bf16 v[26:29], v[26:29], v[90:93], v[30:33]
	s_nop 5
	ds_read_b128 v[98:101], v190
	ds_read_b128 v[102:105], v189
	ds_read_b128 v[106:109], v188
	ds_read_b128 v[110:113], v187
	ds_read_b128 v[114:117], v186
	ds_read_b128 v[118:121], v185
	ds_read_b128 v[122:125], v184
	ds_read_b128 v[194:197], v183
	s_waitcnt lgkmcnt(8)
	s_nop 0
	v_mfma_f32_16x16x32_bf16 v[30:33], v[94:97], v[62:65], 0
	v_mfma_f32_16x16x32_bf16 v[30:33], v[58:61], v[66:69], v[30:33]
	v_mfma_f32_16x16x32_bf16 v[30:33], v[54:57], v[70:73], v[30:33]
	v_mfma_f32_16x16x32_bf16 v[30:33], v[50:53], v[74:77], v[30:33]
	v_mfma_f32_16x16x32_bf16 v[30:33], v[46:49], v[78:81], v[30:33]
	v_mfma_f32_16x16x32_bf16 v[30:33], v[42:45], v[82:85], v[30:33]
	v_mfma_f32_16x16x32_bf16 v[30:33], v[38:41], v[86:89], v[30:33]
	v_mfma_f32_16x16x32_bf16 v[30:33], v[34:37], v[90:93], v[30:33]
	ds_read_b128 v[38:41], v182
	ds_read_b128 v[42:45], v181
	ds_read_b128 v[46:49], v180
	ds_read_b128 v[50:53], v179
	ds_read_b128 v[54:57], v178
	ds_read_b128 v[58:61], v177
	ds_read_b128 v[94:97], v176
	ds_read_b128 v[198:201], v175
	s_waitcnt lgkmcnt(8)
	s_nop 0
	v_mfma_f32_16x16x32_bf16 v[34:37], v[194:197], v[62:65], 0
	v_mfma_f32_16x16x32_bf16 v[34:37], v[122:125], v[66:69], v[34:37]
	v_mfma_f32_16x16x32_bf16 v[34:37], v[118:121], v[70:73], v[34:37]
	v_mfma_f32_16x16x32_bf16 v[34:37], v[114:117], v[74:77], v[34:37]
	v_mfma_f32_16x16x32_bf16 v[34:37], v[110:113], v[78:81], v[34:37]
	v_mfma_f32_16x16x32_bf16 v[34:37], v[106:109], v[82:85], v[34:37]
	v_mfma_f32_16x16x32_bf16 v[34:37], v[102:105], v[86:89], v[34:37]
	v_mfma_f32_16x16x32_bf16 v[34:37], v[98:101], v[90:93], v[34:37]
	ds_read_b128 v[98:101], v174
	ds_read_b128 v[102:105], v173
	ds_read_b128 v[106:109], v172
	ds_read_b128 v[110:113], v171
	ds_read_b128 v[114:117], v170
	ds_read_b128 v[118:121], v169
	ds_read_b128 v[122:125], v168
	ds_read_b128 v[194:197], v167
	s_waitcnt lgkmcnt(8)
; #define LAS __attribute__((address_space(3)))
; #define PIN8(a) asm volatile("" : "+v"(a[0]), "+v"(a[1]), "+v"(a[2]), "+v"(a[3]), "+v"(a[4]), "+v"(a[5]), "+v"(a[6]), "+v"(a[7]))
; __device__ __forceinline__ void xattn_unit(const Params& P, LAS unsigned char* lds, int unit, int tid, int lane, int wave) {
;     ...
;         f32x4 St[16];
;         bf16x8 fr[2][8];
; #pragma unroll
;         for (int s = 0; s < 8; ++s) fr[0][s] = *(const LAS bf16x8*)(arow + 64 * s);
; #pragma unroll
;         for (int kap = 0; kap < 16; ++kap) {
;             if (kap + 1 < 16) {
; #pragma unroll
;                 for (int s = 0; s < 8; ++s) fr[(kap + 1) & 1][s] = *(const LAS bf16x8*)(arow + (16 * (kap + 1)) * 528 + 64 * s);
;             }
;             __builtin_amdgcn_sched_barrier(0);
;             PIN8(fr[kap & 1]);
;             f32x4 acc = (f32x4){0.f, 0.f, 0.f, 0.f};
; #pragma unroll
;             for (int s = 0; s < 8; ++s) acc = __builtin_amdgcn_mfma_f32_16x16x32_bf16(fr[kap & 1][s], Bq[s], acc, 0, 0, 0);
;             St[kap] = acc;
;             __builtin_amdgcn_sched_barrier(0);
;         }
	s_nop 0
	v_mfma_f32_16x16x32_bf16 v[198:201], v[198:201], v[62:65], 0
	v_mfma_f32_16x16x32_bf16 v[94:97], v[94:97], v[66:69], v[198:201]
	v_mfma_f32_16x16x32_bf16 v[58:61], v[58:61], v[70:73], v[94:97]
	v_mfma_f32_16x16x32_bf16 v[54:57], v[54:57], v[74:77], v[58:61]
	v_mfma_f32_16x16x32_bf16 v[50:53], v[50:53], v[78:81], v[54:57]
	v_mfma_f32_16x16x32_bf16 v[46:49], v[46:49], v[82:85], v[50:53]
	v_mfma_f32_16x16x32_bf16 v[42:45], v[42:45], v[86:89], v[46:49]
	v_mfma_f32_16x16x32_bf16 v[38:41], v[38:41], v[90:93], v[42:45]
	s_nop 5
	ds_read_b128 v[46:49], v166
	ds_read_b128 v[50:53], v165
	ds_read_b128 v[54:57], v164
	ds_read_b128 v[58:61], v163
	ds_read_b128 v[94:97], v162
	ds_read_b128 v[198:201], v161
	ds_read_b128 v[202:205], v160
	ds_read_b128 v[206:209], v159
	s_waitcnt lgkmcnt(8)
	s_nop 0
	v_mfma_f32_16x16x32_bf16 v[42:45], v[194:197], v[62:65], 0
	v_mfma_f32_16x16x32_bf16 v[42:45], v[122:125], v[66:69], v[42:45]
	v_mfma_f32_16x16x32_bf16 v[42:45], v[118:121], v[70:73], v[42:45]
	v_mfma_f32_16x16x32_bf16 v[42:45], v[114:117], v[74:77], v[42:45]
	v_mfma_f32_16x16x32_bf16 v[42:45], v[110:113], v[78:81], v[42:45]
	v_mfma_f32_16x16x32_bf16 v[42:45], v[106:109], v[82:85], v[42:45]
	v_mfma_f32_16x16x32_bf16 v[42:45], v[102:105], v[86:89], v[42:45]
	v_mfma_f32_16x16x32_bf16 v[42:45], v[98:101], v[90:93], v[42:45]
	ds_read_b128 v[98:101], v158
	ds_read_b128 v[102:105], v157
	ds_read_b128 v[106:109], v156
	ds_read_b128 v[110:113], v155
	ds_read_b128 v[114:117], v154
	ds_read_b128 v[118:121], v153
	ds_read_b128 v[122:125], v152
	ds_read_b128 v[194:197], v151
	s_waitcnt lgkmcnt(8)
	s_nop 0
	v_mfma_f32_16x16x32_bf16 v[206:209], v[206:209], v[62:65], 0
	v_mfma_f32_16x16x32_bf16 v[202:205], v[202:205], v[66:69], v[206:209]
	v_mfma_f32_16x16x32_bf16 v[198:201], v[198:201], v[70:73], v[202:205]
	v_mfma_f32_16x16x32_bf16 v[94:97], v[94:97], v[74:77], v[198:201]
	v_mfma_f32_16x16x32_bf16 v[58:61], v[58:61], v[78:81], v[94:97]
	v_mfma_f32_16x16x32_bf16 v[54:57], v[54:57], v[82:85], v[58:61]
	v_mfma_f32_16x16x32_bf16 v[50:53], v[50:53], v[86:89], v[54:57]
	v_mfma_f32_16x16x32_bf16 v[46:49], v[46:49], v[90:93], v[50:53]
	s_nop 5
	ds_read_b128 v[54:57], v150
	ds_read_b128 v[58:61], v149
	ds_read_b128 v[94:97], v148
	ds_read_b128 v[198:201], v147
	ds_read_b128 v[202:205], v146
	ds_read_b128 v[206:209], v145
	ds_read_b128 v[210:213], v144
	ds_read_b128 v[214:217], v143
	s_waitcnt lgkmcnt(8)
	s_nop 0
	v_mfma_f32_16x16x32_bf16 v[50:53], v[194:197], v[62:65], 0
	v_mfma_f32_16x16x32_bf16 v[50:53], v[122:125], v[66:69], v[50:53]
	v_mfma_f32_16x16x32_bf16 v[50:53], v[118:121], v[70:73], v[50:53]
	v_mfma_f32_16x16x32_bf16 v[50:53], v[114:117], v[74:77], v[50:53]
	v_mfma_f32_16x16x32_bf16 v[50:53], v[110:113], v[78:81], v[50:53]
	v_mfma_f32_16x16x32_bf16 v[50:53], v[106:109], v[82:85], v[50:53]
	v_mfma_f32_16x16x32_bf16 v[50:53], v[102:105], v[86:89], v[50:53]
	v_mfma_f32_16x16x32_bf16 v[50:53], v[98:101], v[90:93], v[50:53]
	ds_read_b128 v[98:101], v142
	ds_read_b128 v[102:105], v141
	ds_read_b128 v[106:109], v140
	ds_read_b128 v[110:113], v139
	ds_read_b128 v[114:117], v138
	ds_read_b128 v[118:121], v137
	ds_read_b128 v[122:125], v136
	ds_read_b128 v[194:197], v135
	s_waitcnt lgkmcnt(8)
	s_nop 0
	v_mfma_f32_16x16x32_bf16 v[214:217], v[214:217], v[62:65], 0
	v_mfma_f32_16x16x32_bf16 v[210:213], v[210:213], v[66:69], v[214:217]
	v_mfma_f32_16x16x32_bf16 v[206:209], v[206:209], v[70:73], v[210:213]
	v_mfma_f32_16x16x32_bf16 v[202:205], v[202:205], v[74:77], v[206:209]
	v_mfma_f32_16x16x32_bf16 v[198:201], v[198:201], v[78:81], v[202:205]
	v_mfma_f32_16x16x32_bf16 v[94:97], v[94:97], v[82:85], v[198:201]
	v_mfma_f32_16x16x32_bf16 v[58:61], v[58:61], v[86:89], v[94:97]
	v_mfma_f32_16x16x32_bf16 v[54:57], v[54:57], v[90:93], v[58:61]
	s_nop 5
	ds_read_b128 v[94:97], v134
	ds_read_b128 v[198:201], v133
	ds_read_b128 v[202:205], v252
	ds_read_b128 v[206:209], v128
	ds_read_b128 v[210:213], v253
	ds_read_b128 v[214:217], v129
	ds_read_b128 v[218:221], v132
	ds_read_b128 v[222:225], v127
	s_waitcnt lgkmcnt(8)
	s_nop 0
	v_mfma_f32_16x16x32_bf16 v[58:61], v[194:197], v[62:65], 0
	v_mfma_f32_16x16x32_bf16 v[58:61], v[122:125], v[66:69], v[58:61]
	v_mfma_f32_16x16x32_bf16 v[58:61], v[118:121], v[70:73], v[58:61]
	v_mfma_f32_16x16x32_bf16 v[58:61], v[114:117], v[74:77], v[58:61]
	v_mfma_f32_16x16x32_bf16 v[58:61], v[110:113], v[78:81], v[58:61]
	v_mfma_f32_16x16x32_bf16 v[58:61], v[106:109], v[82:85], v[58:61]
	v_mfma_f32_16x16x32_bf16 v[58:61], v[102:105], v[86:89], v[58:61]
	v_mfma_f32_16x16x32_bf16 v[58:61], v[98:101], v[90:93], v[58:61]
	s_waitcnt lgkmcnt(0)
; __device__ __forceinline__ void xattn_unit(const Params& P, LAS unsigned char* lds, int unit, int tid, int lane, int wave) {
;     ...
;             for (int s = 0; s < 8; ++s) acc = __builtin_amdgcn_mfma_f32_16x16x32_bf16(fr[kap & 1][s], Bq[s], acc, 0, 0, 0);
;             St[kap] = acc;
;             __builtin_amdgcn_sched_barrier(0);
;         }
;         float mx = -3.0e38f;
; #pragma unroll
;         for (int kap = 0; kap < 16; ++kap) mx = fmaxf(fmaxf(fmaxf(St[kap].x, St[kap].y), fmaxf(St[kap].z, St[kap].w)), mx);
;         mx = fmaxf(mx, __shfl_xor(mx, 16)); mx = fmaxf(mx, __shfl_xor(mx, 32));
	s_nop 0
	v_mfma_f32_16x16x32_bf16 v[62:65], v[222:225], v[62:65], 0
	v_mfma_f32_16x16x32_bf16 v[62:65], v[218:221], v[66:69], v[62:65]
	v_mfma_f32_16x16x32_bf16 v[62:65], v[214:217], v[70:73], v[62:65]
	v_mfma_f32_16x16x32_bf16 v[62:65], v[210:213], v[74:77], v[62:65]
	v_mfma_f32_16x16x32_bf16 v[62:65], v[206:209], v[78:81], v[62:65]
	v_mfma_f32_16x16x32_bf16 v[62:65], v[202:205], v[82:85], v[62:65]
	v_mfma_f32_16x16x32_bf16 v[62:65], v[198:201], v[86:89], v[62:65]
	v_mfma_f32_16x16x32_bf16 v[62:65], v[94:97], v[90:93], v[62:65]
	v_max_f32_e32 v66, v3, v3
	v_max_f32_e32 v67, v2, v2
	v_max_f32_e32 v66, v67, v66
	v_max_f32_e32 v67, v5, v5
	v_max_f32_e32 v68, v4, v4
	v_max_f32_e32 v67, v68, v67
	s_mov_b32 s29, 0xff61b1e6
	v_max3_f32 v66, v66, v67, s29
	v_max_f32_e32 v67, v7, v7
	v_max_f32_e32 v68, v6, v6
	v_max_f32_e32 v67, v68, v67
	v_max_f32_e32 v68, v9, v9
	v_max_f32_e32 v69, v8, v8
	v_max_f32_e32 v68, v69, v68
	v_max3_f32 v66, v67, v68, v66
	v_max_f32_e32 v67, v11, v11
	v_max_f32_e32 v68, v10, v10
	v_max_f32_e32 v67, v68, v67
	v_max_f32_e32 v68, v13, v13
	v_max_f32_e32 v69, v12, v12
	v_max_f32_e32 v68, v69, v68
	v_max3_f32 v66, v67, v68, v66
	v_max_f32_e32 v67, v15, v15
	v_max_f32_e32 v68, v14, v14
	v_max_f32_e32 v67, v68, v67
	v_max_f32_e32 v68, v17, v17
	v_max_f32_e32 v69, v16, v16
	v_max_f32_e32 v68, v69, v68
	v_max3_f32 v66, v67, v68, v66
	v_max_f32_e32 v67, v19, v19
	v_max_f32_e32 v68, v18, v18
	v_max_f32_e32 v67, v68, v67
	v_max_f32_e32 v68, v21, v21
	v_max_f32_e32 v69, v20, v20
	v_max_f32_e32 v68, v69, v68
	v_max3_f32 v66, v67, v68, v66
	v_max_f32_e32 v67, v23, v23
	v_max_f32_e32 v68, v22, v22
	v_max_f32_e32 v67, v68, v67
	v_max_f32_e32 v68, v25, v25
	v_max_f32_e32 v69, v24, v24
	v_max_f32_e32 v68, v69, v68
	v_max3_f32 v66, v67, v68, v66
	v_max_f32_e32 v67, v27, v27
	v_max_f32_e32 v68, v26, v26
	v_max_f32_e32 v67, v68, v67
	v_max_f32_e32 v68, v29, v29
	v_max_f32_e32 v69, v28, v28
	v_max_f32_e32 v68, v69, v68
	v_max3_f32 v66, v67, v68, v66
	v_max_f32_e32 v67, v31, v31
	v_max_f32_e32 v68, v30, v30
	v_max_f32_e32 v67, v68, v67
	v_max_f32_e32 v68, v33, v33
	v_max_f32_e32 v69, v32, v32
	v_max_f32_e32 v68, v69, v68
	v_max3_f32 v66, v67, v68, v66
	v_max_f32_e32 v67, v35, v35
	v_max_f32_e32 v68, v34, v34
	v_max_f32_e32 v67, v68, v67
	v_max_f32_e32 v68, v37, v37
	v_max_f32_e32 v69, v36, v36
	v_max_f32_e32 v68, v69, v68
	v_max3_f32 v66, v67, v68, v66
	v_max_f32_e32 v67, v39, v39
	v_max_f32_e32 v68, v38, v38
	v_max_f32_e32 v67, v68, v67
	v_max_f32_e32 v68, v41, v41
	v_max_f32_e32 v69, v40, v40
	v_max_f32_e32 v68, v69, v68
	v_max3_f32 v66, v67, v68, v66
	v_max_f32_e32 v67, v43, v43
	v_max_f32_e32 v68, v42, v42
	v_max_f32_e32 v67, v68, v67
	v_max_f32_e32 v68, v45, v45
	v_max_f32_e32 v69, v44, v44
	v_max_f32_e32 v68, v69, v68
	v_max3_f32 v66, v67, v68, v66
	v_max_f32_e32 v67, v47, v47
	v_max_f32_e32 v68, v46, v46
	v_max_f32_e32 v67, v68, v67
	v_max_f32_e32 v68, v49, v49
	v_max_f32_e32 v69, v48, v48
	v_max_f32_e32 v68, v69, v68
	v_max3_f32 v66, v67, v68, v66
	v_max_f32_e32 v67, v51, v51
	v_max_f32_e32 v68, v50, v50
	v_max_f32_e32 v67, v68, v67
	v_max_f32_e32 v68, v53, v53
	v_max_f32_e32 v69, v52, v52
	v_max_f32_e32 v68, v69, v68
	v_max3_f32 v66, v67, v68, v66
	v_max_f32_e32 v67, v55, v55
	v_max_f32_e32 v68, v54, v54
	v_max_f32_e32 v67, v68, v67
	v_max_f32_e32 v68, v57, v57
	v_max_f32_e32 v69, v56, v56
	v_max_f32_e32 v68, v69, v68
	v_max3_f32 v66, v67, v68, v66
	v_max_f32_e32 v67, v59, v59
	v_max_f32_e32 v68, v58, v58
	v_max_f32_e32 v67, v68, v67
	v_max_f32_e32 v68, v61, v61
	v_max_f32_e32 v69, v60, v60
	v_max_f32_e32 v68, v69, v68
	v_max3_f32 v66, v67, v68, v66
	v_max_f32_e32 v67, v63, v63
	v_max_f32_e32 v68, v62, v62
	v_max_f32_e32 v67, v68, v67
	v_max_f32_e32 v68, v65, v65
	v_max_f32_e32 v69, v64, v64
	v_max_f32_e32 v68, v69, v68
	v_max3_f32 v66, v67, v68, v66
	v_mbcnt_lo_u32_b32 v67, -1, 0
	v_mbcnt_hi_u32_b32 v67, -1, v67
	v_and_b32_e32 v69, 64, v67
	v_xor_b32_e32 v68, 16, v67
	v_add_u32_e32 v69, 64, v69
	v_cmp_lt_i32_e32 vcc, v68, v69
	s_movk_i32 s22, 0x7fff
	s_mov_b32 s28, 0xffff0000
	v_cndmask_b32_e32 v68, v67, v68, vcc
	v_lshlrev_b32_e32 v193, 2, v68
	ds_bpermute_b32 v68, v193, v66
	s_waitcnt lgkmcnt(0)
	v_max_f32_e32 v68, v68, v68
	v_max_f32_e32 v66, v66, v68
	v_xor_b32_e32 v68, 32, v67
	v_cmp_lt_i32_e32 vcc, v68, v69
	s_nop 1
	v_cndmask_b32_e32 v67, v67, v68, vcc
	v_lshlrev_b32_e32 v194, 2, v67
	ds_bpermute_b32 v67, v194, v66
	s_waitcnt lgkmcnt(0)
; __device__ __forceinline__ void xattn_unit(const Params& P, LAS unsigned char* lds, int unit, int tid, int lane, int wave) {
;     ...
;         float l = 0.f;
; #pragma unroll
;         for (int kap = 0; kap < 16; ++kap) { St[kap].x = __expf(St[kap].x - mx); St[kap].y = __expf(St[kap].y - mx); St[kap].z = __expf(St[kap].z - mx); St[kap].w = __expf(St[kap].w - mx);
;             l += (St[kap].x + St[kap].y) + (St[kap].z + St[kap].w); }
	v_max_f32_e32 v67, v67, v67
	v_max_f32_e32 v78, v66, v67
	v_sub_f32_e32 v3, v3, v78
	v_mul_f32_e32 v3, 0x3fb8aa3b, v3
	v_sub_f32_e32 v2, v2, v78
	v_exp_f32_e32 v66, v3
	v_sub_f32_e32 v3, v4, v78
	v_sub_f32_e32 v4, v5, v78
	v_sub_f32_e32 v5, v7, v78
	v_mul_f32_e32 v2, 0x3fb8aa3b, v2
	v_mul_f32_e32 v3, 0x3fb8aa3b, v3
	v_mul_f32_e32 v4, 0x3fb8aa3b, v4
	v_mul_f32_e32 v5, 0x3fb8aa3b, v5
	v_exp_f32_e32 v2, v2
	v_exp_f32_e32 v3, v3
	v_exp_f32_e32 v67, v4
	v_sub_f32_e32 v4, v6, v78
	v_exp_f32_e32 v68, v5
	v_sub_f32_e32 v5, v8, v78
	v_sub_f32_e32 v6, v9, v78
	v_mul_f32_e32 v4, 0x3fb8aa3b, v4
	v_mul_f32_e32 v5, 0x3fb8aa3b, v5
	v_mul_f32_e32 v6, 0x3fb8aa3b, v6
	v_exp_f32_e32 v4, v4
	v_exp_f32_e32 v5, v5
	v_exp_f32_e32 v69, v6
	v_pk_add_f32 v[6:7], v[2:3], v[66:67]
	v_sub_f32_e32 v8, v17, v78
	v_add_f32_e32 v6, v6, v7
	v_add_f32_e32 v9, 0, v6
	v_pk_add_f32 v[6:7], v[4:5], v[68:69]
	v_mul_f32_e32 v8, 0x3fb8aa3b, v8
	v_pk_add_f32 v[6:7], v[6:7], v[6:7] op_sel_hi:[0,1]
	v_sub_f32_e32 v6, v10, v78
	v_mul_f32_e32 v6, 0x3fb8aa3b, v6
	v_exp_f32_e32 v79, v6
	v_sub_f32_e32 v6, v11, v78
	v_mul_f32_e32 v6, 0x3fb8aa3b, v6
	v_exp_f32_e32 v80, v6
	v_sub_f32_e32 v6, v12, v78
	v_mul_f32_e32 v6, 0x3fb8aa3b, v6
	v_exp_f32_e32 v81, v6
	v_sub_f32_e32 v6, v13, v78
	v_mul_f32_e32 v6, 0x3fb8aa3b, v6
	v_exp_f32_e32 v82, v6
	v_sub_f32_e32 v6, v14, v78
	v_mul_f32_e32 v6, 0x3fb8aa3b, v6
	v_exp_f32_e32 v12, v6
	v_sub_f32_e32 v6, v15, v78
	v_mul_f32_e32 v6, 0x3fb8aa3b, v6
	v_exp_f32_e32 v72, v6
	v_sub_f32_e32 v6, v16, v78
	v_mul_f32_e32 v6, 0x3fb8aa3b, v6
	v_exp_f32_e32 v6, v6
	v_exp_f32_e32 v8, v8
	v_add_f32_e32 v13, v79, v80
	v_add_f32_e32 v73, v81, v82
	v_pk_add_f32 v[10:11], v[12:13], v[72:73]
	v_pk_add_f32 v[14:15], v[6:7], v[8:9]
	v_sub_f32_e32 v7, v18, v78
	v_pk_add_f32 v[10:11], v[10:11], v[14:15]
	v_mul_f32_e32 v7, 0x3fb8aa3b, v7
	v_pk_add_f32 v[14:15], v[10:11], v[10:11] op_sel_hi:[0,1]
	v_exp_f32_e32 v10, v7
	v_sub_f32_e32 v7, v19, v78
	v_mul_f32_e32 v7, 0x3fb8aa3b, v7
	v_exp_f32_e32 v70, v7
	v_sub_f32_e32 v7, v20, v78
	v_mul_f32_e32 v7, 0x3fb8aa3b, v7
	v_exp_f32_e32 v11, v7
	v_sub_f32_e32 v7, v21, v78
	v_mul_f32_e32 v7, 0x3fb8aa3b, v7
	v_exp_f32_e32 v71, v7
	v_sub_f32_e32 v7, v22, v78
	v_mul_f32_e32 v7, 0x3fb8aa3b, v7
	v_exp_f32_e32 v13, v7
	v_sub_f32_e32 v7, v23, v78
	v_mul_f32_e32 v7, 0x3fb8aa3b, v7
	v_exp_f32_e32 v73, v7
	v_sub_f32_e32 v7, v24, v78
	v_mul_f32_e32 v7, 0x3fb8aa3b, v7
	v_exp_f32_e32 v83, v7
	v_sub_f32_e32 v7, v25, v78
	v_mul_f32_e32 v7, 0x3fb8aa3b, v7
	v_exp_f32_e32 v84, v7
	v_sub_f32_e32 v7, v26, v78
	v_pk_add_f32 v[16:17], v[10:11], v[70:71]
	v_mul_f32_e32 v7, 0x3fb8aa3b, v7
	v_pk_add_f32 v[18:19], v[16:17], v[16:17] op_sel_hi:[0,1]
	v_exp_f32_e32 v16, v7
	v_sub_f32_e32 v7, v27, v78
	v_mul_f32_e32 v7, 0x3fb8aa3b, v7
	v_exp_f32_e32 v20, v7
	v_sub_f32_e32 v7, v28, v78
	v_mul_f32_e32 v7, 0x3fb8aa3b, v7
	v_exp_f32_e32 v18, v7
	v_sub_f32_e32 v7, v29, v78
	v_mul_f32_e32 v7, 0x3fb8aa3b, v7
	v_exp_f32_e32 v14, v7
	v_sub_f32_e32 v7, v30, v78
	v_mul_f32_e32 v7, 0x3fb8aa3b, v7
	v_exp_f32_e32 v28, v7
	v_sub_f32_e32 v7, v31, v78
	v_mul_f32_e32 v7, 0x3fb8aa3b, v7
	v_exp_f32_e32 v74, v7
	v_sub_f32_e32 v7, v32, v78
	v_mul_f32_e32 v7, 0x3fb8aa3b, v7
	v_exp_f32_e32 v29, v7
	v_sub_f32_e32 v7, v33, v78
	v_mul_f32_e32 v7, 0x3fb8aa3b, v7
	v_exp_f32_e32 v75, v7
	v_sub_f32_e32 v7, v34, v78
	v_mul_f32_e32 v7, 0x3fb8aa3b, v7
	v_pk_add_f32 v[24:25], v[18:19], v[14:15]
	v_exp_f32_e32 v19, v7
	v_sub_f32_e32 v7, v35, v78
	v_add_f32_e32 v17, v13, v73
	v_add_f32_e32 v21, v83, v84
	v_mul_f32_e32 v7, 0x3fb8aa3b, v7
	v_pk_add_f32 v[22:23], v[16:17], v[20:21]
	v_exp_f32_e32 v21, v7
	v_sub_f32_e32 v7, v36, v78
	v_mul_f32_e32 v7, 0x3fb8aa3b, v7
	v_exp_f32_e32 v85, v7
	v_sub_f32_e32 v7, v37, v78
	v_mul_f32_e32 v7, 0x3fb8aa3b, v7
	v_exp_f32_e32 v86, v7
	v_sub_f32_e32 v7, v38, v78
	v_mul_f32_e32 v7, 0x3fb8aa3b, v7
	v_exp_f32_e32 v36, v7
	v_sub_f32_e32 v7, v39, v78
	v_pk_add_f32 v[22:23], v[22:23], v[24:25]
	v_mul_f32_e32 v7, 0x3fb8aa3b, v7
	v_pk_add_f32 v[24:25], v[22:23], v[22:23] op_sel_hi:[0,1]
	v_pk_add_f32 v[22:23], v[28:29], v[74:75]
	v_exp_f32_e32 v76, v7
	v_sub_f32_e32 v7, v40, v78
	v_pk_add_f32 v[22:23], v[22:23], v[22:23] op_sel_hi:[0,1]
	v_mul_f32_e32 v7, 0x3fb8aa3b, v7
	v_exp_f32_e32 v22, v7
	v_sub_f32_e32 v7, v41, v78
	v_mul_f32_e32 v7, 0x3fb8aa3b, v7
	v_exp_f32_e32 v24, v7
	v_add_f32_e32 v37, v19, v21
	v_add_f32_e32 v77, v85, v86
	v_sub_f32_e32 v7, v42, v78
	v_pk_add_f32 v[26:27], v[36:37], v[76:77]
	v_pk_add_f32 v[30:31], v[22:23], v[24:25]
	v_mul_f32_e32 v7, 0x3fb8aa3b, v7
	v_pk_add_f32 v[26:27], v[26:27], v[30:31]
	v_exp_f32_e32 v30, v7
	v_sub_f32_e32 v7, v43, v78
	v_mul_f32_e32 v7, 0x3fb8aa3b, v7
	v_exp_f32_e32 v40, v7
	v_sub_f32_e32 v7, v44, v78
	v_mul_f32_e32 v7, 0x3fb8aa3b, v7
	v_exp_f32_e32 v31, v7
	v_sub_f32_e32 v7, v45, v78
	v_mul_f32_e32 v7, 0x3fb8aa3b, v7
	v_exp_f32_e32 v41, v7
	v_sub_f32_e32 v7, v46, v78
	v_mul_f32_e32 v7, 0x3fb8aa3b, v7
	v_exp_f32_e32 v23, v7
	v_sub_f32_e32 v7, v47, v78
	v_mul_f32_e32 v7, 0x3fb8aa3b, v7
	v_exp_f32_e32 v25, v7
	v_sub_f32_e32 v7, v48, v78
	v_mul_f32_e32 v7, 0x3fb8aa3b, v7
	v_exp_f32_e32 v37, v7
	v_sub_f32_e32 v7, v49, v78
	v_mul_f32_e32 v7, 0x3fb8aa3b, v7
	v_exp_f32_e32 v77, v7
	v_sub_f32_e32 v7, v50, v78
	v_pk_add_f32 v[32:33], v[30:31], v[40:41]
	v_mul_f32_e32 v7, 0x3fb8aa3b, v7
	v_pk_add_f32 v[34:35], v[32:33], v[32:33] op_sel_hi:[0,1]
	v_exp_f32_e32 v32, v7
	v_sub_f32_e32 v7, v51, v78
	v_mul_f32_e32 v7, 0x3fb8aa3b, v7
	v_exp_f32_e32 v38, v7
	v_sub_f32_e32 v7, v52, v78
	v_mul_f32_e32 v7, 0x3fb8aa3b, v7
	v_exp_f32_e32 v34, v7
	v_sub_f32_e32 v7, v53, v78
	v_pk_add_f32 v[26:27], v[26:27], v[26:27] op_sel_hi:[0,1]
; __device__ __forceinline__ unsigned pk2(float lo, float hi) { return f2bf(lo) | (f2bf(hi) << 16); }
; __device__ __forceinline__ bf16x8 pack_b(const f32x4 a, const f32x4 b) {
;     v4u r; r.x = pk2(a.x, a.y); r.y = pk2(a.z, a.w); r.z = pk2(b.x, b.y); r.w = pk2(b.z, b.w);
;     return __builtin_bit_cast(bf16x8, r);
; }
; __device__ __forceinline__ void xattn_unit(const Params& P, LAS unsigned char* lds, int unit, int tid, int lane, int wave) {
;     ...
;         l += __shfl_xor(l, 16); l += __shfl_xor(l, 32);
;         inv[ps] = 1.0f / l;
; #pragma unroll
;         for (int s = 0; s < 8; ++s) Bp[ps][s] = pack_b(St[2 * s], St[2 * s + 1]);
	v_mul_f32_e32 v7, 0x3fb8aa3b, v7
	v_exp_f32_e32 v26, v7
	v_sub_f32_e32 v7, v54, v78
	v_mul_f32_e32 v7, 0x3fb8aa3b, v7
	v_exp_f32_e32 v46, v7
	v_sub_f32_e32 v7, v55, v78
	v_mul_f32_e32 v7, 0x3fb8aa3b, v7
	v_exp_f32_e32 v48, v7
	v_sub_f32_e32 v7, v56, v78
	v_mul_f32_e32 v7, 0x3fb8aa3b, v7
	v_exp_f32_e32 v47, v7
	v_sub_f32_e32 v7, v57, v78
	v_mul_f32_e32 v7, 0x3fb8aa3b, v7
	v_exp_f32_e32 v49, v7
	v_sub_f32_e32 v7, v58, v78
	v_add_f32_e32 v33, v23, v25
	v_add_f32_e32 v39, v37, v77
	v_mul_f32_e32 v7, 0x3fb8aa3b, v7
	v_pk_add_f32 v[42:43], v[32:33], v[38:39]
	v_exp_f32_e32 v33, v7
	v_sub_f32_e32 v7, v59, v78
	v_mul_f32_e32 v7, 0x3fb8aa3b, v7
	v_pk_add_f32 v[44:45], v[34:35], v[26:27]
	v_exp_f32_e32 v35, v7
	v_sub_f32_e32 v7, v60, v78
	v_mul_f32_e32 v7, 0x3fb8aa3b, v7
	v_exp_f32_e32 v39, v7
	v_sub_f32_e32 v7, v61, v78
	v_mul_f32_e32 v7, 0x3fb8aa3b, v7
	v_exp_f32_e32 v58, v7
	v_sub_f32_e32 v7, v62, v78
	v_mul_f32_e32 v7, 0x3fb8aa3b, v7
	v_exp_f32_e32 v50, v7
	v_sub_f32_e32 v7, v63, v78
	v_pk_add_f32 v[42:43], v[42:43], v[44:45]
	v_mul_f32_e32 v7, 0x3fb8aa3b, v7
	v_pk_add_f32 v[44:45], v[42:43], v[42:43] op_sel_hi:[0,1]
	v_pk_add_f32 v[42:43], v[46:47], v[48:49]
	v_exp_f32_e32 v52, v7
	v_sub_f32_e32 v7, v64, v78
	v_pk_add_f32 v[42:43], v[42:43], v[42:43] op_sel_hi:[0,1]
	v_mul_f32_e32 v7, 0x3fb8aa3b, v7
	v_exp_f32_e32 v42, v7
	v_sub_f32_e32 v7, v65, v78
	v_mul_f32_e32 v7, 0x3fb8aa3b, v7
	v_exp_f32_e32 v44, v7
	v_add_f32_e32 v51, v33, v35
	v_add_f32_e32 v53, v39, v58
	v_pk_add_f32 v[54:55], v[50:51], v[52:53]
	v_pk_add_f32 v[56:57], v[42:43], v[44:45]
	v_bfe_u32 v45, v4, 16, 1
	v_pk_add_f32 v[54:55], v[54:55], v[56:57]
	v_bfe_u32 v51, v5, 16, 1
	v_add_f32_e32 v7, v54, v55
	ds_bpermute_b32 v9, v193, v7
	v_add3_u32 v5, v5, v51, s22
	v_add3_u32 v4, v4, v45, s22
	v_lshrrev_b32_e32 v4, 16, v4
	v_lshrrev_b32_e32 v5, 16, v5
	s_waitcnt lgkmcnt(0)
	v_add_f32_e32 v7, v7, v9
	ds_bpermute_b32 v9, v194, v7
	v_bfe_u32 v45, v12, 16, 1
	v_bfe_u32 v51, v13, 16, 1
	v_bfe_u32 v53, v83, 16, 1
	v_add3_u32 v53, v83, v53, s22
	s_waitcnt lgkmcnt(0)
	v_add_f32_e32 v7, v7, v9
	v_div_scale_f32 v9, s[30:31], v7, v7, 1.0
	v_rcp_f32_e32 v15, v9
	v_add3_u32 v13, v13, v51, s22
	v_bfe_u32 v51, v29, 16, 1
	v_fma_f32 v17, -v9, v15, 1.0
	v_fmac_f32_e32 v15, v17, v15
	v_div_scale_f32 v17, vcc, 1.0, v7, 1.0
	v_mul_f32_e32 v27, v17, v15
	v_fma_f32 v43, -v9, v27, v17
	v_fmac_f32_e32 v27, v43, v15
	v_fma_f32 v9, -v9, v27, v17
	v_div_fmas_f32 v9, v9, v15, v27
	v_div_fixup_f32 v126, v9, v7, 1.0
	v_bfe_u32 v7, v69, 16, 1
	v_bfe_u32 v9, v68, 16, 1
	v_add3_u32 v9, v68, v9, s22
	v_add3_u32 v7, v69, v7, s22
	v_bfe_u32 v43, v3, 16, 1
	v_bfe_u32 v15, v67, 16, 1
	v_add3_u32 v3, v3, v43, s22
	v_and_or_b32 v5, v7, s28, v5
	v_and_or_b32 v4, v9, s28, v4
	v_bfe_u32 v7, v8, 16, 1
	v_bfe_u32 v9, v72, 16, 1
	v_add3_u32 v15, v67, v15, s22
	v_bfe_u32 v27, v2, 16, 1
	v_lshrrev_b32_e32 v3, 16, v3
	v_add3_u32 v7, v8, v7, s22
	v_add3_u32 v8, v72, v9, s22
	v_bfe_u32 v9, v6, 16, 1
	v_bfe_u32 v43, v81, 16, 1
	v_bfe_u32 v17, v66, 16, 1
	v_add3_u32 v2, v2, v27, s22
	v_and_or_b32 v3, v15, s28, v3
	v_bfe_u32 v15, v82, 16, 1
	v_add3_u32 v6, v6, v9, s22
	v_add3_u32 v9, v12, v45, s22
	v_add3_u32 v12, v81, v43, s22
	v_add3_u32 v17, v66, v17, s22
	v_lshrrev_b32_e32 v2, 16, v2
	v_add3_u32 v15, v82, v15, s22
	v_bfe_u32 v27, v79, 16, 1
	v_lshrrev_b32_e32 v6, 16, v6
	v_lshrrev_b32_e32 v12, 16, v12
	v_lshrrev_b32_e32 v43, 16, v9
	v_and_or_b32 v2, v17, s28, v2
	v_bfe_u32 v17, v80, 16, 1
	v_add3_u32 v27, v79, v27, s22
	v_and_or_b32 v9, v7, s28, v6
	v_and_or_b32 v8, v8, s28, v43
	v_and_or_b32 v7, v15, s28, v12
	v_bfe_u32 v12, v84, 16, 1
	v_bfe_u32 v15, v73, 16, 1
	v_bfe_u32 v43, v10, 16, 1
	v_add3_u32 v17, v80, v17, s22
	v_lshrrev_b32_e32 v27, 16, v27
	v_add3_u32 v15, v73, v15, s22
	v_add3_u32 v12, v84, v12, s22
	v_bfe_u32 v45, v11, 16, 1
	v_add3_u32 v10, v10, v43, s22
	v_lshrrev_b32_e32 v43, 16, v13
	v_lshrrev_b32_e32 v13, 16, v53
	v_and_or_b32 v6, v17, s28, v27
	v_bfe_u32 v17, v71, 16, 1
	v_add3_u32 v11, v11, v45, s22
	v_and_or_b32 v13, v12, s28, v13
	v_and_or_b32 v12, v15, s28, v43
	v_bfe_u32 v15, v14, 16, 1
	v_add3_u32 v17, v71, v17, s22
	v_lshrrev_b32_e32 v11, 16, v11
	v_bfe_u32 v43, v20, 16, 1
	v_add3_u32 v14, v14, v15, s22
	v_bfe_u32 v15, v18, 16, 1
	v_bfe_u32 v27, v70, 16, 1
	v_and_or_b32 v11, v17, s28, v11
	v_bfe_u32 v17, v75, 16, 1
	v_add3_u32 v20, v20, v43, s22
	v_bfe_u32 v43, v16, 16, 1
	v_bfe_u32 v45, v28, 16, 1
	v_add3_u32 v15, v18, v15, s22
	v_add3_u32 v18, v29, v51, s22
	v_add3_u32 v27, v70, v27, s22
	v_lshrrev_b32_e32 v10, 16, v10
	v_add3_u32 v17, v75, v17, s22
	v_add3_u32 v28, v28, v45, s22
	v_add3_u32 v16, v16, v43, s22
	v_lshrrev_b32_e32 v18, 16, v18
	v_and_or_b32 v10, v27, s28, v10
	v_bfe_u32 v27, v74, 16, 1
	v_lshrrev_b32_e32 v15, 16, v15
	v_lshrrev_b32_e32 v29, 16, v16
	v_lshrrev_b32_e32 v16, 16, v28
	v_and_or_b32 v17, v17, s28, v18
	v_bfe_u32 v18, v24, 16, 1
	v_bfe_u32 v28, v21, 16, 1
	v_add3_u32 v27, v74, v27, s22
	v_and_or_b32 v15, v14, s28, v15
	v_and_or_b32 v14, v20, s28, v29
	v_add3_u32 v18, v24, v18, s22
	v_add3_u32 v24, v21, v28, s22
	v_bfe_u32 v21, v22, 16, 1
	v_bfe_u32 v28, v19, 16, 1
	v_bfe_u32 v29, v85, 16, 1
	v_and_or_b32 v16, v27, s28, v16
	v_bfe_u32 v27, v86, 16, 1
	v_bfe_u32 v43, v36, 16, 1
	v_add3_u32 v21, v22, v21, s22
	v_add3_u32 v29, v85, v29, s22
	v_add3_u32 v19, v19, v28, s22
	v_add3_u32 v27, v86, v27, s22
	v_add3_u32 v22, v36, v43, s22
	v_lshrrev_b32_e32 v21, 16, v21
	v_lshrrev_b32_e32 v28, 16, v19
	v_lshrrev_b32_e32 v19, 16, v29
	v_bfe_u32 v29, v31, 16, 1
	v_bfe_u32 v36, v23, 16, 1
	v_bfe_u32 v20, v76, 16, 1
	v_and_or_b32 v21, v18, s28, v21
	v_and_or_b32 v19, v27, s28, v19
; #define LAS __attribute__((address_space(3)))
; #define PIN8(a) asm volatile("" : "+v"(a[0]), "+v"(a[1]), "+v"(a[2]), "+v"(a[3]), "+v"(a[4]), "+v"(a[5]), "+v"(a[6]), "+v"(a[7]))
; __device__ __forceinline__ void xattn_unit(const Params& P, LAS unsigned char* lds, int unit, int tid, int lane, int wave) {
;     ...
;     for (int ps = 0; ps < XA_NPS; ++ps) {
;         __builtin_amdgcn_sched_barrier(0); asm volatile("" : "+v"(col), "+v"(g) :: "memory");
;         const bf16* Q = (const bf16*)(ws + WS_Q) + (size_t)(tw + 128 * ps + col) * 1024 + h * 256 + 8 * g;
;         bf16x8 Bq[8];
; #pragma unroll
;         for (int s = 0; s < 8; ++s) Bq[s] = *(const bf16x8*)(Q + 32 * s);
;         f32x4 St[16];
;         bf16x8 fr[2][8];
; #pragma unroll
;         for (int s = 0; s < 8; ++s) fr[0][s] = *(const LAS bf16x8*)(arow + 64 * s);
; #pragma unroll
;         for (int kap = 0; kap < 16; ++kap) {
;             if (kap + 1 < 16) {
; #pragma unroll
;                 for (int s = 0; s < 8; ++s) fr[(kap + 1) & 1][s] = *(const LAS bf16x8*)(arow + (16 * (kap + 1)) * 528 + 64 * s);
;             }
;             __builtin_amdgcn_sched_barrier(0);
;             PIN8(fr[kap & 1]);
;             f32x4 acc = (f32x4){0.f, 0.f, 0.f, 0.f};
; #pragma unroll
;             for (int s = 0; s < 8; ++s) acc = __builtin_amdgcn_mfma_f32_16x16x32_bf16(fr[kap & 1][s], Bq[s], acc, 0, 0, 0);
;     ...
;         inv[ps] = 1.0f / l;
; #pragma unroll
;         for (int s = 0; s < 8; ++s) Bp[ps][s] = pack_b(St[2 * s], St[2 * s + 1]);
	v_and_or_b32 v18, v24, s28, v28
	v_bfe_u32 v24, v25, 16, 1
	v_bfe_u32 v27, v41, 16, 1
	v_bfe_u32 v28, v40, 16, 1
	v_add3_u32 v23, v23, v36, s22
	v_add3_u32 v29, v31, v29, s22
	v_add3_u32 v20, v76, v20, s22
	v_lshrrev_b32_e32 v22, 16, v22
	v_add3_u32 v28, v40, v28, s22
	v_add3_u32 v27, v41, v27, s22
	v_add3_u32 v24, v25, v24, s22
	v_bfe_u32 v25, v30, 16, 1
	v_bfe_u32 v40, v37, 16, 1
	v_lshrrev_b32_e32 v29, 16, v29
	v_lshrrev_b32_e32 v23, 16, v23
	v_and_or_b32 v20, v20, s28, v22
	v_bfe_u32 v22, v77, 16, 1
	v_add3_u32 v37, v37, v40, s22
	v_add3_u32 v25, v30, v25, s22
	v_and_or_b32 v24, v24, s28, v23
	v_and_or_b32 v23, v27, s28, v29
	v_bfe_u32 v27, v26, 16, 1
	v_bfe_u32 v29, v48, 16, 1
	v_add3_u32 v22, v77, v22, s22
	v_lshrrev_b32_e32 v30, 16, v25
	v_lshrrev_b32_e32 v25, 16, v37
	v_add3_u32 v26, v26, v27, s22
	v_add3_u32 v31, v48, v29, s22
	v_bfe_u32 v27, v34, 16, 1
	v_bfe_u32 v29, v32, 16, 1
	v_and_or_b32 v25, v22, s28, v25
	v_and_or_b32 v22, v28, s28, v30
	v_bfe_u32 v30, v38, 16, 1
	v_bfe_u32 v36, v46, 16, 1
	v_bfe_u32 v37, v47, 16, 1
	v_add3_u32 v27, v34, v27, s22
	v_add3_u32 v29, v32, v29, s22
	v_bfe_u32 v28, v49, 16, 1
	v_add3_u32 v30, v38, v30, s22
	v_add3_u32 v34, v47, v37, s22
	v_add3_u32 v36, v46, v36, s22
	v_lshrrev_b32_e32 v27, 16, v27
	v_lshrrev_b32_e32 v32, 16, v29
	v_add3_u32 v28, v49, v28, s22
	v_lshrrev_b32_e32 v36, 16, v36
	v_lshrrev_b32_e32 v29, 16, v34
	v_and_or_b32 v27, v26, s28, v27
	v_and_or_b32 v26, v30, s28, v32
	v_bfe_u32 v32, v58, 16, 1
	v_bfe_u32 v34, v35, 16, 1
	v_and_or_b32 v29, v28, s28, v29
	v_and_or_b32 v28, v31, s28, v36
	v_add3_u32 v34, v35, v34, s22
	v_add3_u32 v35, v58, v32, s22
	v_bfe_u32 v32, v42, 16, 1
	v_bfe_u32 v36, v33, 16, 1
	v_bfe_u32 v37, v39, 16, 1
	v_bfe_u32 v38, v50, 16, 1
	v_bfe_u32 v30, v44, 16, 1
	v_bfe_u32 v31, v52, 16, 1
	v_add3_u32 v32, v42, v32, s22
	v_add3_u32 v38, v50, v38, s22
	v_add3_u32 v37, v39, v37, s22
	v_add3_u32 v33, v33, v36, s22
	v_add3_u32 v30, v44, v30, s22
	v_add3_u32 v31, v52, v31, s22
	v_lshrrev_b32_e32 v32, 16, v32
	v_lshrrev_b32_e32 v36, 16, v33
	v_lshrrev_b32_e32 v37, 16, v37
	v_lshrrev_b32_e32 v38, 16, v38
	v_and_or_b32 v33, v30, s28, v32
	v_and_or_b32 v32, v31, s28, v38
	v_and_or_b32 v31, v35, s28, v37
	v_and_or_b32 v30, v34, s28, v36
	s_nop 0
	v_add_u32_e32 v34, s3, v1
	v_ashrrev_i32_e32 v35, 31, v34
	v_lshlrev_b32_e32 v36, 3, v192
	v_lshlrev_b64 v[34:35], 11, v[34:35]
	v_ashrrev_i32_e32 v37, 31, v36
	v_lshl_add_u64 v[34:35], s[50:51], 0, v[34:35]
	v_lshl_add_u64 v[34:35], v[36:37], 1, v[34:35]
	global_load_dwordx4 v[90:93], v[34:35], off
	global_load_dwordx4 v[94:97], v[34:35], off offset:64
	global_load_dwordx4 v[98:101], v[34:35], off offset:128
	global_load_dwordx4 v[102:105], v[34:35], off offset:192
	global_load_dwordx4 v[106:109], v[34:35], off offset:256
	global_load_dwordx4 v[110:113], v[34:35], off offset:320
	global_load_dwordx4 v[114:117], v[34:35], off offset:384
	global_load_dwordx4 v[118:121], v[34:35], off offset:448
	ds_read_b128 v[34:37], v191 offset:448
	ds_read_b128 v[38:41], v191 offset:384
	ds_read_b128 v[42:45], v191 offset:320
	ds_read_b128 v[46:49], v191 offset:256
	ds_read_b128 v[50:53], v191 offset:192
	ds_read_b128 v[54:57], v191 offset:128
	ds_read_b128 v[58:61], v191 offset:64
	ds_read_b128 v[62:65], v191
	ds_read_b128 v[66:69], v191 offset:8896
	ds_read_b128 v[70:73], v191 offset:8832
	ds_read_b128 v[74:77], v191 offset:8768
	ds_read_b128 v[78:81], v191 offset:8704
	ds_read_b128 v[82:85], v191 offset:8640
	ds_read_b128 v[86:89], v191 offset:8576
	ds_read_b128 v[122:125], v191 offset:8512
	ds_read_b128 v[196:199], v191 offset:8448
	s_waitcnt lgkmcnt(8)
	s_waitcnt vmcnt(7)
	v_mfma_f32_16x16x32_bf16 v[62:65], v[62:65], v[90:93], 0
	s_waitcnt vmcnt(6)
	v_mfma_f32_16x16x32_bf16 v[58:61], v[58:61], v[94:97], v[62:65]
	s_waitcnt vmcnt(5)
	v_mfma_f32_16x16x32_bf16 v[54:57], v[54:57], v[98:101], v[58:61]
	s_waitcnt vmcnt(4)
	v_mfma_f32_16x16x32_bf16 v[50:53], v[50:53], v[102:105], v[54:57]
	s_waitcnt vmcnt(3)
	v_mfma_f32_16x16x32_bf16 v[46:49], v[46:49], v[106:109], v[50:53]
	s_waitcnt vmcnt(2)
	v_mfma_f32_16x16x32_bf16 v[42:45], v[42:45], v[110:113], v[46:49]
	s_waitcnt vmcnt(1)
	v_mfma_f32_16x16x32_bf16 v[38:41], v[38:41], v[114:117], v[42:45]
	s_waitcnt vmcnt(0)
	v_mfma_f32_16x16x32_bf16 v[34:37], v[34:37], v[118:121], v[38:41]
	s_nop 3
	ds_read_b128 v[42:45], v191 offset:17344
	ds_read_b128 v[46:49], v191 offset:17280
	ds_read_b128 v[50:53], v191 offset:17216
	ds_read_b128 v[54:57], v191 offset:17152
	ds_read_b128 v[58:61], v191 offset:17088
	ds_read_b128 v[62:65], v191 offset:17024
	ds_read_b128 v[200:203], v191 offset:16960
	ds_read_b128 v[204:207], v191 offset:16896
	s_waitcnt lgkmcnt(8)
	s_nop 0
	v_mfma_f32_16x16x32_bf16 v[38:41], v[196:199], v[90:93], 0
	v_mfma_f32_16x16x32_bf16 v[38:41], v[122:125], v[94:97], v[38:41]
	v_mfma_f32_16x16x32_bf16 v[38:41], v[86:89], v[98:101], v[38:41]
	v_mfma_f32_16x16x32_bf16 v[38:41], v[82:85], v[102:105], v[38:41]
	v_mfma_f32_16x16x32_bf16 v[38:41], v[78:81], v[106:109], v[38:41]
	v_mfma_f32_16x16x32_bf16 v[38:41], v[74:77], v[110:113], v[38:41]
	v_mfma_f32_16x16x32_bf16 v[38:41], v[70:73], v[114:117], v[38:41]
	v_mfma_f32_16x16x32_bf16 v[38:41], v[66:69], v[118:121], v[38:41]
	ds_read_b128 v[66:69], v191 offset:25792
	ds_read_b128 v[70:73], v191 offset:25728
	ds_read_b128 v[74:77], v191 offset:25664
	ds_read_b128 v[78:81], v191 offset:25600
	ds_read_b128 v[82:85], v191 offset:25536
	ds_read_b128 v[86:89], v191 offset:25472
	ds_read_b128 v[122:125], v191 offset:25408
	ds_read_b128 v[196:199], v191 offset:25344
	s_waitcnt lgkmcnt(8)
; #define LAS __attribute__((address_space(3)))
; #define PIN8(a) asm volatile("" : "+v"(a[0]), "+v"(a[1]), "+v"(a[2]), "+v"(a[3]), "+v"(a[4]), "+v"(a[5]), "+v"(a[6]), "+v"(a[7]))
; __device__ __forceinline__ void xattn_unit(const Params& P, LAS unsigned char* lds, int unit, int tid, int lane, int wave) {
;     ...
; #pragma unroll
;         for (int kap = 0; kap < 16; ++kap) {
;             if (kap + 1 < 16) {
; #pragma unroll
;                 for (int s = 0; s < 8; ++s) fr[(kap + 1) & 1][s] = *(const LAS bf16x8*)(arow + (16 * (kap + 1)) * 528 + 64 * s);
;             }
;             __builtin_amdgcn_sched_barrier(0);
;             PIN8(fr[kap & 1]);
;             f32x4 acc = (f32x4){0.f, 0.f, 0.f, 0.f};
; #pragma unroll
;             for (int s = 0; s < 8; ++s) acc = __builtin_amdgcn_mfma_f32_16x16x32_bf16(fr[kap & 1][s], Bq[s], acc, 0, 0, 0);
;             St[kap] = acc;
;             __builtin_amdgcn_sched_barrier(0);
;         }
	s_nop 0
	v_mfma_f32_16x16x32_bf16 v[204:207], v[204:207], v[90:93], 0
	v_mfma_f32_16x16x32_bf16 v[200:203], v[200:203], v[94:97], v[204:207]
	v_mfma_f32_16x16x32_bf16 v[62:65], v[62:65], v[98:101], v[200:203]
	v_mfma_f32_16x16x32_bf16 v[58:61], v[58:61], v[102:105], v[62:65]
	v_mfma_f32_16x16x32_bf16 v[54:57], v[54:57], v[106:109], v[58:61]
	v_mfma_f32_16x16x32_bf16 v[50:53], v[50:53], v[110:113], v[54:57]
	v_mfma_f32_16x16x32_bf16 v[46:49], v[46:49], v[114:117], v[50:53]
	v_mfma_f32_16x16x32_bf16 v[42:45], v[42:45], v[118:121], v[46:49]
	s_nop 5
	ds_read_b128 v[50:53], v191 offset:34240
	ds_read_b128 v[54:57], v191 offset:34176
	ds_read_b128 v[58:61], v191 offset:34112
	ds_read_b128 v[62:65], v191 offset:34048
	ds_read_b128 v[200:203], v191 offset:33984
	ds_read_b128 v[204:207], v191 offset:33920
	ds_read_b128 v[208:211], v191 offset:33856
	ds_read_b128 v[212:215], v191 offset:33792
	s_waitcnt lgkmcnt(8)
	s_nop 0
	v_mfma_f32_16x16x32_bf16 v[46:49], v[196:199], v[90:93], 0
	v_mfma_f32_16x16x32_bf16 v[46:49], v[122:125], v[94:97], v[46:49]
	v_mfma_f32_16x16x32_bf16 v[46:49], v[86:89], v[98:101], v[46:49]
	v_mfma_f32_16x16x32_bf16 v[46:49], v[82:85], v[102:105], v[46:49]
	v_mfma_f32_16x16x32_bf16 v[46:49], v[78:81], v[106:109], v[46:49]
	v_mfma_f32_16x16x32_bf16 v[46:49], v[74:77], v[110:113], v[46:49]
	v_mfma_f32_16x16x32_bf16 v[46:49], v[70:73], v[114:117], v[46:49]
	v_mfma_f32_16x16x32_bf16 v[46:49], v[66:69], v[118:121], v[46:49]
	ds_read_b128 v[66:69], v191 offset:42688
	ds_read_b128 v[70:73], v191 offset:42624
	ds_read_b128 v[74:77], v191 offset:42560
	ds_read_b128 v[78:81], v191 offset:42496
	ds_read_b128 v[82:85], v191 offset:42432
	ds_read_b128 v[86:89], v191 offset:42368
	ds_read_b128 v[122:125], v191 offset:42304
	ds_read_b128 v[196:199], v191 offset:42240
	s_waitcnt lgkmcnt(8)
	s_nop 0
	v_mfma_f32_16x16x32_bf16 v[212:215], v[212:215], v[90:93], 0
	v_mfma_f32_16x16x32_bf16 v[208:211], v[208:211], v[94:97], v[212:215]
	v_mfma_f32_16x16x32_bf16 v[204:207], v[204:207], v[98:101], v[208:211]
	v_mfma_f32_16x16x32_bf16 v[200:203], v[200:203], v[102:105], v[204:207]
	v_mfma_f32_16x16x32_bf16 v[62:65], v[62:65], v[106:109], v[200:203]
	v_mfma_f32_16x16x32_bf16 v[58:61], v[58:61], v[110:113], v[62:65]
	v_mfma_f32_16x16x32_bf16 v[54:57], v[54:57], v[114:117], v[58:61]
	v_mfma_f32_16x16x32_bf16 v[50:53], v[50:53], v[118:121], v[54:57]
	s_nop 5
	ds_read_b128 v[58:61], v191 offset:51136
	ds_read_b128 v[62:65], v191 offset:51072
	ds_read_b128 v[200:203], v191 offset:51008
	ds_read_b128 v[204:207], v191 offset:50944
	ds_read_b128 v[208:211], v191 offset:50880
	ds_read_b128 v[212:215], v191 offset:50816
	ds_read_b128 v[216:219], v191 offset:50752
	ds_read_b128 v[220:223], v191 offset:50688
	s_waitcnt lgkmcnt(8)
	s_nop 0
	v_mfma_f32_16x16x32_bf16 v[54:57], v[196:199], v[90:93], 0
	v_mfma_f32_16x16x32_bf16 v[54:57], v[122:125], v[94:97], v[54:57]
	v_mfma_f32_16x16x32_bf16 v[54:57], v[86:89], v[98:101], v[54:57]
	v_mfma_f32_16x16x32_bf16 v[54:57], v[82:85], v[102:105], v[54:57]
	v_mfma_f32_16x16x32_bf16 v[54:57], v[78:81], v[106:109], v[54:57]
	v_mfma_f32_16x16x32_bf16 v[54:57], v[74:77], v[110:113], v[54:57]
	v_mfma_f32_16x16x32_bf16 v[54:57], v[70:73], v[114:117], v[54:57]
	v_mfma_f32_16x16x32_bf16 v[54:57], v[66:69], v[118:121], v[54:57]
	ds_read_b128 v[66:69], v191 offset:59584
	ds_read_b128 v[70:73], v191 offset:59520
	ds_read_b128 v[74:77], v191 offset:59456
	ds_read_b128 v[78:81], v191 offset:59392
	ds_read_b128 v[82:85], v191 offset:59328
	ds_read_b128 v[86:89], v191 offset:59264
	ds_read_b128 v[122:125], v191 offset:59200
	ds_read_b128 v[196:199], v191 offset:59136
	s_waitcnt lgkmcnt(8)
	s_nop 0
	v_mfma_f32_16x16x32_bf16 v[220:223], v[220:223], v[90:93], 0
	v_mfma_f32_16x16x32_bf16 v[216:219], v[216:219], v[94:97], v[220:223]
	v_mfma_f32_16x16x32_bf16 v[212:215], v[212:215], v[98:101], v[216:219]
	v_mfma_f32_16x16x32_bf16 v[208:211], v[208:211], v[102:105], v[212:215]
	v_mfma_f32_16x16x32_bf16 v[204:207], v[204:207], v[106:109], v[208:211]
	v_mfma_f32_16x16x32_bf16 v[200:203], v[200:203], v[110:113], v[204:207]
	v_mfma_f32_16x16x32_bf16 v[62:65], v[62:65], v[114:117], v[200:203]
	v_mfma_f32_16x16x32_bf16 v[58:61], v[58:61], v[118:121], v[62:65]
	s_nop 5
	ds_read_b128 v[200:203], v190
	ds_read_b128 v[204:207], v189
	ds_read_b128 v[208:211], v188
	ds_read_b128 v[212:215], v187
	ds_read_b128 v[216:219], v186
	ds_read_b128 v[220:223], v185
	ds_read_b128 v[224:227], v184
	ds_read_b128 v[228:231], v183
	s_waitcnt lgkmcnt(8)
	s_nop 0
	v_mfma_f32_16x16x32_bf16 v[62:65], v[196:199], v[90:93], 0
	v_mfma_f32_16x16x32_bf16 v[62:65], v[122:125], v[94:97], v[62:65]
	v_mfma_f32_16x16x32_bf16 v[62:65], v[86:89], v[98:101], v[62:65]
	v_mfma_f32_16x16x32_bf16 v[62:65], v[82:85], v[102:105], v[62:65]
	v_mfma_f32_16x16x32_bf16 v[62:65], v[78:81], v[106:109], v[62:65]
	v_mfma_f32_16x16x32_bf16 v[62:65], v[74:77], v[110:113], v[62:65]
	v_mfma_f32_16x16x32_bf16 v[62:65], v[70:73], v[114:117], v[62:65]
	v_mfma_f32_16x16x32_bf16 v[62:65], v[66:69], v[118:121], v[62:65]
	ds_read_b128 v[70:73], v182
	ds_read_b128 v[74:77], v181
	ds_read_b128 v[78:81], v180
	ds_read_b128 v[82:85], v179
	ds_read_b128 v[86:89], v178
	ds_read_b128 v[122:125], v177
	ds_read_b128 v[196:199], v176
	ds_read_b128 v[232:235], v175
	s_waitcnt lgkmcnt(8)
; #define LAS __attribute__((address_space(3)))
; #define PIN8(a) asm volatile("" : "+v"(a[0]), "+v"(a[1]), "+v"(a[2]), "+v"(a[3]), "+v"(a[4]), "+v"(a[5]), "+v"(a[6]), "+v"(a[7]))
; __device__ __forceinline__ void xattn_unit(const Params& P, LAS unsigned char* lds, int unit, int tid, int lane, int wave) {
;     ...
;         for (int s = 0; s < 8; ++s) fr[0][s] = *(const LAS bf16x8*)(arow + 64 * s);
; #pragma unroll
;         for (int kap = 0; kap < 16; ++kap) {
;             if (kap + 1 < 16) {
; #pragma unroll
;                 for (int s = 0; s < 8; ++s) fr[(kap + 1) & 1][s] = *(const LAS bf16x8*)(arow + (16 * (kap + 1)) * 528 + 64 * s);
;             }
;             __builtin_amdgcn_sched_barrier(0);
;             PIN8(fr[kap & 1]);
;             f32x4 acc = (f32x4){0.f, 0.f, 0.f, 0.f};
; #pragma unroll
;             for (int s = 0; s < 8; ++s) acc = __builtin_amdgcn_mfma_f32_16x16x32_bf16(fr[kap & 1][s], Bq[s], acc, 0, 0, 0);
;             St[kap] = acc;
;             __builtin_amdgcn_sched_barrier(0);
;         }
	s_nop 0
	v_mfma_f32_16x16x32_bf16 v[66:69], v[228:231], v[90:93], 0
	v_mfma_f32_16x16x32_bf16 v[66:69], v[224:227], v[94:97], v[66:69]
	v_mfma_f32_16x16x32_bf16 v[66:69], v[220:223], v[98:101], v[66:69]
	v_mfma_f32_16x16x32_bf16 v[66:69], v[216:219], v[102:105], v[66:69]
	v_mfma_f32_16x16x32_bf16 v[66:69], v[212:215], v[106:109], v[66:69]
	v_mfma_f32_16x16x32_bf16 v[66:69], v[208:211], v[110:113], v[66:69]
	v_mfma_f32_16x16x32_bf16 v[66:69], v[204:207], v[114:117], v[66:69]
	v_mfma_f32_16x16x32_bf16 v[66:69], v[200:203], v[118:121], v[66:69]
	ds_read_b128 v[200:203], v174
	ds_read_b128 v[204:207], v173
	ds_read_b128 v[208:211], v172
	ds_read_b128 v[212:215], v171
	ds_read_b128 v[216:219], v170
	ds_read_b128 v[220:223], v169
	ds_read_b128 v[224:227], v168
	ds_read_b128 v[228:231], v167
	s_waitcnt lgkmcnt(8)
	s_nop 0
	v_mfma_f32_16x16x32_bf16 v[232:235], v[232:235], v[90:93], 0
	v_mfma_f32_16x16x32_bf16 v[196:199], v[196:199], v[94:97], v[232:235]
	v_mfma_f32_16x16x32_bf16 v[122:125], v[122:125], v[98:101], v[196:199]
	v_mfma_f32_16x16x32_bf16 v[86:89], v[86:89], v[102:105], v[122:125]
	v_mfma_f32_16x16x32_bf16 v[82:85], v[82:85], v[106:109], v[86:89]
	v_mfma_f32_16x16x32_bf16 v[78:81], v[78:81], v[110:113], v[82:85]
	v_mfma_f32_16x16x32_bf16 v[74:77], v[74:77], v[114:117], v[78:81]
	v_mfma_f32_16x16x32_bf16 v[70:73], v[70:73], v[118:121], v[74:77]
	s_nop 5
	ds_read_b128 v[78:81], v166
	ds_read_b128 v[82:85], v165
	ds_read_b128 v[86:89], v164
	ds_read_b128 v[122:125], v163
	ds_read_b128 v[196:199], v162
	ds_read_b128 v[232:235], v161
	ds_read_b128 v[236:239], v160
	ds_read_b128 v[240:243], v159
	s_waitcnt lgkmcnt(8)
	s_nop 0
	v_mfma_f32_16x16x32_bf16 v[74:77], v[228:231], v[90:93], 0
	v_mfma_f32_16x16x32_bf16 v[74:77], v[224:227], v[94:97], v[74:77]
	v_mfma_f32_16x16x32_bf16 v[74:77], v[220:223], v[98:101], v[74:77]
	v_mfma_f32_16x16x32_bf16 v[74:77], v[216:219], v[102:105], v[74:77]
	v_mfma_f32_16x16x32_bf16 v[74:77], v[212:215], v[106:109], v[74:77]
	v_mfma_f32_16x16x32_bf16 v[74:77], v[208:211], v[110:113], v[74:77]
	v_mfma_f32_16x16x32_bf16 v[74:77], v[204:207], v[114:117], v[74:77]
	v_mfma_f32_16x16x32_bf16 v[74:77], v[200:203], v[118:121], v[74:77]
	ds_read_b128 v[200:203], v158
	ds_read_b128 v[204:207], v157
	ds_read_b128 v[208:211], v156
	ds_read_b128 v[212:215], v155
	ds_read_b128 v[216:219], v154
	ds_read_b128 v[220:223], v153
	ds_read_b128 v[224:227], v152
	ds_read_b128 v[228:231], v151
	s_waitcnt lgkmcnt(8)
	s_nop 0
	v_mfma_f32_16x16x32_bf16 v[240:243], v[240:243], v[90:93], 0
	v_mfma_f32_16x16x32_bf16 v[236:239], v[236:239], v[94:97], v[240:243]
	v_mfma_f32_16x16x32_bf16 v[232:235], v[232:235], v[98:101], v[236:239]
	v_mfma_f32_16x16x32_bf16 v[196:199], v[196:199], v[102:105], v[232:235]
	v_mfma_f32_16x16x32_bf16 v[122:125], v[122:125], v[106:109], v[196:199]
	v_mfma_f32_16x16x32_bf16 v[86:89], v[86:89], v[110:113], v[122:125]
	v_mfma_f32_16x16x32_bf16 v[82:85], v[82:85], v[114:117], v[86:89]
	v_mfma_f32_16x16x32_bf16 v[78:81], v[78:81], v[118:121], v[82:85]
	s_nop 5
	ds_read_b128 v[86:89], v150
	ds_read_b128 v[122:125], v149
	ds_read_b128 v[196:199], v148
	ds_read_b128 v[232:235], v147
	ds_read_b128 v[236:239], v146
	ds_read_b128 v[240:243], v145
	ds_read_b128 v[244:247], v144
	ds_read_b128 v[248:251], v143
	s_waitcnt lgkmcnt(8)
	s_nop 0
	v_mfma_f32_16x16x32_bf16 v[82:85], v[228:231], v[90:93], 0
	v_mfma_f32_16x16x32_bf16 v[82:85], v[224:227], v[94:97], v[82:85]
	v_mfma_f32_16x16x32_bf16 v[82:85], v[220:223], v[98:101], v[82:85]
	v_mfma_f32_16x16x32_bf16 v[82:85], v[216:219], v[102:105], v[82:85]
	v_mfma_f32_16x16x32_bf16 v[82:85], v[212:215], v[106:109], v[82:85]
	v_mfma_f32_16x16x32_bf16 v[82:85], v[208:211], v[110:113], v[82:85]
	v_mfma_f32_16x16x32_bf16 v[82:85], v[204:207], v[114:117], v[82:85]
	v_mfma_f32_16x16x32_bf16 v[82:85], v[200:203], v[118:121], v[82:85]
	ds_read_b128 v[200:203], v142
	ds_read_b128 v[204:207], v141
	ds_read_b128 v[208:211], v140
	ds_read_b128 v[212:215], v139
	ds_read_b128 v[216:219], v138
	ds_read_b128 v[220:223], v137
	ds_read_b128 v[224:227], v136
	ds_read_b128 v[228:231], v135
	s_waitcnt lgkmcnt(8)
	s_nop 0
	v_mfma_f32_16x16x32_bf16 v[248:251], v[248:251], v[90:93], 0
	v_mfma_f32_16x16x32_bf16 v[244:247], v[244:247], v[94:97], v[248:251]
	v_mfma_f32_16x16x32_bf16 v[240:243], v[240:243], v[98:101], v[244:247]
	v_mfma_f32_16x16x32_bf16 v[236:239], v[236:239], v[102:105], v[240:243]
	v_mfma_f32_16x16x32_bf16 v[232:235], v[232:235], v[106:109], v[236:239]
	v_mfma_f32_16x16x32_bf16 v[196:199], v[196:199], v[110:113], v[232:235]
	v_mfma_f32_16x16x32_bf16 v[122:125], v[122:125], v[114:117], v[196:199]
	v_mfma_f32_16x16x32_bf16 v[86:89], v[86:89], v[118:121], v[122:125]
	s_nop 5
	ds_read_b128 v[196:199], v134
	ds_read_b128 v[232:235], v133
	ds_read_b128 v[236:239], v252
	ds_read_b128 v[240:243], v128
	ds_read_b128 v[244:247], v253
	ds_read_b128 v[248:251], v129
	ds_read_b128 v[128:131], v132
	ds_read_b128 v[122:125], v127
	s_waitcnt lgkmcnt(8)
	s_nop 0
	v_mfma_f32_16x16x32_bf16 v[228:231], v[228:231], v[90:93], 0
	v_mfma_f32_16x16x32_bf16 v[224:227], v[224:227], v[94:97], v[228:231]
	v_mfma_f32_16x16x32_bf16 v[220:223], v[220:223], v[98:101], v[224:227]
	v_mfma_f32_16x16x32_bf16 v[216:219], v[216:219], v[102:105], v[220:223]
	v_mfma_f32_16x16x32_bf16 v[212:215], v[212:215], v[106:109], v[216:219]
	v_mfma_f32_16x16x32_bf16 v[208:211], v[208:211], v[110:113], v[212:215]
	v_mfma_f32_16x16x32_bf16 v[204:207], v[204:207], v[114:117], v[208:211]
	v_mfma_f32_16x16x32_bf16 v[200:203], v[200:203], v[118:121], v[204:207]
	s_waitcnt lgkmcnt(0)
; __device__ __forceinline__ void xattn_unit(const Params& P, LAS unsigned char* lds, int unit, int tid, int lane, int wave) {
;     ...
;             for (int s = 0; s < 8; ++s) acc = __builtin_amdgcn_mfma_f32_16x16x32_bf16(fr[kap & 1][s], Bq[s], acc, 0, 0, 0);
;             St[kap] = acc;
;             __builtin_amdgcn_sched_barrier(0);
;         }
;         float mx = -3.0e38f;
; #pragma unroll
;         for (int kap = 0; kap < 16; ++kap) mx = fmaxf(fmaxf(fmaxf(St[kap].x, St[kap].y), fmaxf(St[kap].z, St[kap].w)), mx);
;         mx = fmaxf(mx, __shfl_xor(mx, 16)); mx = fmaxf(mx, __shfl_xor(mx, 32));
;         float l = 0.f;
; #pragma unroll
;         for (int kap = 0; kap < 16; ++kap) { St[kap].x = __expf(St[kap].x - mx); St[kap].y = __expf(St[kap].y - mx); St[kap].z = __expf(St[kap].z - mx); St[kap].w = __expf(St[kap].w - mx);
;             l += (St[kap].x + St[kap].y) + (St[kap].z + St[kap].w); }
	s_nop 0
	v_mfma_f32_16x16x32_bf16 v[90:93], v[122:125], v[90:93], 0
	v_mfma_f32_16x16x32_bf16 v[90:93], v[128:131], v[94:97], v[90:93]
	v_mfma_f32_16x16x32_bf16 v[90:93], v[248:251], v[98:101], v[90:93]
	v_mfma_f32_16x16x32_bf16 v[90:93], v[244:247], v[102:105], v[90:93]
	v_mfma_f32_16x16x32_bf16 v[90:93], v[240:243], v[106:109], v[90:93]
	v_mfma_f32_16x16x32_bf16 v[90:93], v[236:239], v[110:113], v[90:93]
	v_mfma_f32_16x16x32_bf16 v[90:93], v[232:235], v[114:117], v[90:93]
	v_mfma_f32_16x16x32_bf16 v[90:93], v[196:199], v[118:121], v[90:93]
	v_max_f32_e32 v94, v35, v35
	v_max_f32_e32 v95, v34, v34
	v_max_f32_e32 v94, v95, v94
	v_max_f32_e32 v95, v37, v37
	v_max_f32_e32 v96, v36, v36
	v_max_f32_e32 v95, v96, v95
	v_max3_f32 v94, v94, v95, s29
	v_max_f32_e32 v95, v39, v39
	v_max_f32_e32 v96, v38, v38
	v_max_f32_e32 v95, v96, v95
	v_max_f32_e32 v96, v41, v41
	v_max_f32_e32 v97, v40, v40
	v_max_f32_e32 v96, v97, v96
	v_max3_f32 v94, v95, v96, v94
	v_max_f32_e32 v95, v43, v43
	v_max_f32_e32 v96, v42, v42
	v_max_f32_e32 v95, v96, v95
	v_max_f32_e32 v96, v45, v45
	v_max_f32_e32 v97, v44, v44
	v_max_f32_e32 v96, v97, v96
	v_max3_f32 v94, v95, v96, v94
	v_max_f32_e32 v95, v47, v47
	v_max_f32_e32 v96, v46, v46
	v_max_f32_e32 v95, v96, v95
	v_max_f32_e32 v96, v49, v49
	v_max_f32_e32 v97, v48, v48
	v_max_f32_e32 v96, v97, v96
	v_max3_f32 v94, v95, v96, v94
	v_max_f32_e32 v95, v51, v51
	v_max_f32_e32 v96, v50, v50
	v_max_f32_e32 v95, v96, v95
	v_max_f32_e32 v96, v53, v53
	v_max_f32_e32 v97, v52, v52
	v_max_f32_e32 v96, v97, v96
	v_max3_f32 v94, v95, v96, v94
	v_max_f32_e32 v95, v55, v55
	v_max_f32_e32 v96, v54, v54
	v_max_f32_e32 v95, v96, v95
	v_max_f32_e32 v96, v57, v57
	v_max_f32_e32 v97, v56, v56
	v_max_f32_e32 v96, v97, v96
	v_max3_f32 v94, v95, v96, v94
	v_max_f32_e32 v95, v59, v59
	v_max_f32_e32 v96, v58, v58
	v_max_f32_e32 v95, v96, v95
	v_max_f32_e32 v96, v61, v61
	v_max_f32_e32 v97, v60, v60
	v_max_f32_e32 v96, v97, v96
	v_max3_f32 v94, v95, v96, v94
	v_max_f32_e32 v95, v63, v63
	v_max_f32_e32 v96, v62, v62
	v_max_f32_e32 v95, v96, v95
	v_max_f32_e32 v96, v65, v65
	v_max_f32_e32 v97, v64, v64
	v_max_f32_e32 v96, v97, v96
	v_max3_f32 v94, v95, v96, v94
	v_max_f32_e32 v95, v67, v67
	v_max_f32_e32 v96, v66, v66
	v_max_f32_e32 v95, v96, v95
	v_max_f32_e32 v96, v69, v69
	v_max_f32_e32 v97, v68, v68
	v_max_f32_e32 v96, v97, v96
	v_max3_f32 v94, v95, v96, v94
	v_max_f32_e32 v95, v71, v71
	v_max_f32_e32 v96, v70, v70
	v_max_f32_e32 v95, v96, v95
	v_max_f32_e32 v96, v73, v73
	v_max_f32_e32 v97, v72, v72
	v_max_f32_e32 v96, v97, v96
	v_max3_f32 v94, v95, v96, v94
	v_max_f32_e32 v95, v75, v75
	v_max_f32_e32 v96, v74, v74
	v_max_f32_e32 v95, v96, v95
	v_max_f32_e32 v96, v77, v77
	v_max_f32_e32 v97, v76, v76
	v_max_f32_e32 v96, v97, v96
	v_max3_f32 v94, v95, v96, v94
	v_max_f32_e32 v95, v79, v79
	v_max_f32_e32 v96, v78, v78
	v_max_f32_e32 v95, v96, v95
	v_max_f32_e32 v96, v81, v81
	v_max_f32_e32 v97, v80, v80
	v_max_f32_e32 v96, v97, v96
	v_max3_f32 v94, v95, v96, v94
	v_max_f32_e32 v95, v83, v83
	v_max_f32_e32 v96, v82, v82
	v_max_f32_e32 v95, v96, v95
	v_max_f32_e32 v96, v85, v85
	v_max_f32_e32 v97, v84, v84
	v_max_f32_e32 v96, v97, v96
	v_max3_f32 v94, v95, v96, v94
	v_max_f32_e32 v95, v87, v87
	v_max_f32_e32 v96, v86, v86
	v_max_f32_e32 v95, v96, v95
	v_max_f32_e32 v96, v89, v89
	v_max_f32_e32 v97, v88, v88
	v_max_f32_e32 v96, v97, v96
	v_max3_f32 v94, v95, v96, v94
	v_max_f32_e32 v95, v201, v201
	v_max_f32_e32 v96, v200, v200
	v_max_f32_e32 v95, v96, v95
	v_max_f32_e32 v96, v203, v203
	v_max_f32_e32 v97, v202, v202
	v_max_f32_e32 v96, v97, v96
	v_max3_f32 v94, v95, v96, v94
	v_max_f32_e32 v95, v91, v91
	v_max_f32_e32 v96, v90, v90
	v_max_f32_e32 v95, v96, v95
	v_max_f32_e32 v96, v93, v93
	v_max_f32_e32 v97, v92, v92
	v_max_f32_e32 v96, v97, v96
	v_max3_f32 v94, v95, v96, v94
	ds_bpermute_b32 v95, v193, v94
	s_waitcnt lgkmcnt(0)
	s_barrier
	v_max_f32_e32 v95, v95, v95
	v_max_f32_e32 v94, v94, v95
	ds_bpermute_b32 v95, v194, v94
	s_waitcnt lgkmcnt(0)
	v_max_f32_e32 v95, v95, v95
	v_max_f32_e32 v106, v94, v95
	v_sub_f32_e32 v35, v35, v106
	v_mul_f32_e32 v35, 0x3fb8aa3b, v35
	v_sub_f32_e32 v34, v34, v106
	v_exp_f32_e32 v94, v35
	v_sub_f32_e32 v35, v36, v106
	v_sub_f32_e32 v36, v37, v106
	v_sub_f32_e32 v37, v39, v106
	v_mul_f32_e32 v34, 0x3fb8aa3b, v34
	v_mul_f32_e32 v35, 0x3fb8aa3b, v35
	v_mul_f32_e32 v36, 0x3fb8aa3b, v36
	v_mul_f32_e32 v37, 0x3fb8aa3b, v37
	v_exp_f32_e32 v34, v34
	v_exp_f32_e32 v35, v35
	v_exp_f32_e32 v95, v36
	v_sub_f32_e32 v36, v38, v106
	v_exp_f32_e32 v96, v37
	v_sub_f32_e32 v37, v40, v106
	v_sub_f32_e32 v38, v41, v106
	v_mul_f32_e32 v36, 0x3fb8aa3b, v36
	v_mul_f32_e32 v37, 0x3fb8aa3b, v37
	v_mul_f32_e32 v38, 0x3fb8aa3b, v38
	v_exp_f32_e32 v36, v36
	v_exp_f32_e32 v37, v37
	v_exp_f32_e32 v97, v38
	v_pk_add_f32 v[38:39], v[34:35], v[94:95]
	v_sub_f32_e32 v40, v49, v106
	v_add_f32_e32 v38, v38, v39
	v_add_f32_e32 v41, 0, v38
	v_pk_add_f32 v[38:39], v[36:37], v[96:97]
	v_mul_f32_e32 v40, 0x3fb8aa3b, v40
	v_pk_add_f32 v[38:39], v[38:39], v[38:39] op_sel_hi:[0,1]
	v_sub_f32_e32 v38, v42, v106
	v_mul_f32_e32 v38, 0x3fb8aa3b, v38
	v_exp_f32_e32 v107, v38
	v_sub_f32_e32 v38, v43, v106
	v_mul_f32_e32 v38, 0x3fb8aa3b, v38
	v_exp_f32_e32 v108, v38
	v_sub_f32_e32 v38, v44, v106
	v_mul_f32_e32 v38, 0x3fb8aa3b, v38
	v_exp_f32_e32 v109, v38
	v_sub_f32_e32 v38, v45, v106
	v_mul_f32_e32 v38, 0x3fb8aa3b, v38
	v_exp_f32_e32 v110, v38
	v_sub_f32_e32 v38, v46, v106
	v_mul_f32_e32 v38, 0x3fb8aa3b, v38
	v_exp_f32_e32 v44, v38
	v_sub_f32_e32 v38, v47, v106
	v_mul_f32_e32 v38, 0x3fb8aa3b, v38
	v_exp_f32_e32 v100, v38
	v_sub_f32_e32 v38, v48, v106
; __device__ __forceinline__ void xattn_unit(const Params& P, LAS unsigned char* lds, int unit, int tid, int lane, int wave) {
;     ...
;         for (int kap = 0; kap < 16; ++kap) { St[kap].x = __expf(St[kap].x - mx); St[kap].y = __expf(St[kap].y - mx); St[kap].z = __expf(St[kap].z - mx); St[kap].w = __expf(St[kap].w - mx);
;             l += (St[kap].x + St[kap].y) + (St[kap].z + St[kap].w); }
;         l += __shfl_xor(l, 16); l += __shfl_xor(l, 32);
;         inv[ps] = 1.0f / l;
; #pragma unroll
;         for (int s = 0; s < 8; ++s) Bp[ps][s] = pack_b(St[2 * s], St[2 * s + 1]);
	v_mul_f32_e32 v38, 0x3fb8aa3b, v38
	v_exp_f32_e32 v38, v38
	v_exp_f32_e32 v40, v40
	v_add_f32_e32 v45, v107, v108
	v_add_f32_e32 v101, v109, v110
	v_pk_add_f32 v[42:43], v[44:45], v[100:101]
	v_pk_add_f32 v[46:47], v[38:39], v[40:41]
	v_sub_f32_e32 v39, v50, v106
	v_pk_add_f32 v[42:43], v[42:43], v[46:47]
	v_mul_f32_e32 v39, 0x3fb8aa3b, v39
	v_pk_add_f32 v[46:47], v[42:43], v[42:43] op_sel_hi:[0,1]
	v_exp_f32_e32 v42, v39
	v_sub_f32_e32 v39, v51, v106
	v_mul_f32_e32 v39, 0x3fb8aa3b, v39
	v_exp_f32_e32 v98, v39
	v_sub_f32_e32 v39, v52, v106
	v_mul_f32_e32 v39, 0x3fb8aa3b, v39
	v_exp_f32_e32 v43, v39
	v_sub_f32_e32 v39, v53, v106
	v_mul_f32_e32 v39, 0x3fb8aa3b, v39
	v_exp_f32_e32 v99, v39
	v_sub_f32_e32 v39, v54, v106
	v_mul_f32_e32 v39, 0x3fb8aa3b, v39
	v_exp_f32_e32 v45, v39
	v_sub_f32_e32 v39, v55, v106
	v_mul_f32_e32 v39, 0x3fb8aa3b, v39
	v_exp_f32_e32 v101, v39
	v_sub_f32_e32 v39, v56, v106
	v_mul_f32_e32 v39, 0x3fb8aa3b, v39
	v_exp_f32_e32 v111, v39
	v_sub_f32_e32 v39, v57, v106
	v_mul_f32_e32 v39, 0x3fb8aa3b, v39
	v_exp_f32_e32 v112, v39
	v_sub_f32_e32 v39, v58, v106
	v_pk_add_f32 v[48:49], v[42:43], v[98:99]
	v_mul_f32_e32 v39, 0x3fb8aa3b, v39
	v_pk_add_f32 v[50:51], v[48:49], v[48:49] op_sel_hi:[0,1]
	v_exp_f32_e32 v48, v39
	v_sub_f32_e32 v39, v59, v106
	v_mul_f32_e32 v39, 0x3fb8aa3b, v39
	v_exp_f32_e32 v52, v39
	v_sub_f32_e32 v39, v60, v106
	v_mul_f32_e32 v39, 0x3fb8aa3b, v39
	v_exp_f32_e32 v50, v39
	v_sub_f32_e32 v39, v61, v106
	v_mul_f32_e32 v39, 0x3fb8aa3b, v39
	v_exp_f32_e32 v46, v39
	v_sub_f32_e32 v39, v62, v106
	v_mul_f32_e32 v39, 0x3fb8aa3b, v39
	v_exp_f32_e32 v60, v39
	v_sub_f32_e32 v39, v63, v106
	v_mul_f32_e32 v39, 0x3fb8aa3b, v39
	v_exp_f32_e32 v102, v39
	v_sub_f32_e32 v39, v64, v106
	v_mul_f32_e32 v39, 0x3fb8aa3b, v39
	v_exp_f32_e32 v61, v39
	v_sub_f32_e32 v39, v65, v106
	v_mul_f32_e32 v39, 0x3fb8aa3b, v39
	v_exp_f32_e32 v103, v39
	v_sub_f32_e32 v39, v66, v106
	v_mul_f32_e32 v39, 0x3fb8aa3b, v39
	v_pk_add_f32 v[56:57], v[50:51], v[46:47]
	v_exp_f32_e32 v51, v39
	v_sub_f32_e32 v39, v67, v106
	v_add_f32_e32 v49, v45, v101
	v_add_f32_e32 v53, v111, v112
	v_mul_f32_e32 v39, 0x3fb8aa3b, v39
	v_pk_add_f32 v[54:55], v[48:49], v[52:53]
	v_exp_f32_e32 v53, v39
	v_sub_f32_e32 v39, v68, v106
	v_mul_f32_e32 v39, 0x3fb8aa3b, v39
	v_exp_f32_e32 v113, v39
	v_sub_f32_e32 v39, v69, v106
	v_mul_f32_e32 v39, 0x3fb8aa3b, v39
	v_exp_f32_e32 v114, v39
	v_sub_f32_e32 v39, v70, v106
	v_mul_f32_e32 v39, 0x3fb8aa3b, v39
	v_exp_f32_e32 v70, v39
	v_sub_f32_e32 v39, v71, v106
	v_pk_add_f32 v[54:55], v[54:55], v[56:57]
	v_mul_f32_e32 v39, 0x3fb8aa3b, v39
	v_pk_add_f32 v[56:57], v[54:55], v[54:55] op_sel_hi:[0,1]
	v_pk_add_f32 v[54:55], v[60:61], v[102:103]
	v_exp_f32_e32 v104, v39
	v_sub_f32_e32 v39, v72, v106
	v_pk_add_f32 v[54:55], v[54:55], v[54:55] op_sel_hi:[0,1]
	v_mul_f32_e32 v39, 0x3fb8aa3b, v39
	v_exp_f32_e32 v54, v39
	v_sub_f32_e32 v39, v73, v106
	v_mul_f32_e32 v39, 0x3fb8aa3b, v39
	v_exp_f32_e32 v56, v39
	v_add_f32_e32 v71, v51, v53
	v_add_f32_e32 v105, v113, v114
	v_sub_f32_e32 v39, v74, v106
	v_pk_add_f32 v[58:59], v[70:71], v[104:105]
	v_pk_add_f32 v[62:63], v[54:55], v[56:57]
	v_mul_f32_e32 v39, 0x3fb8aa3b, v39
	v_pk_add_f32 v[58:59], v[58:59], v[62:63]
	v_exp_f32_e32 v62, v39
	v_sub_f32_e32 v39, v75, v106
	v_mul_f32_e32 v39, 0x3fb8aa3b, v39
	v_exp_f32_e32 v74, v39
	v_sub_f32_e32 v39, v76, v106
	v_mul_f32_e32 v39, 0x3fb8aa3b, v39
	v_exp_f32_e32 v63, v39
	v_sub_f32_e32 v39, v77, v106
	v_mul_f32_e32 v39, 0x3fb8aa3b, v39
	v_exp_f32_e32 v75, v39
	v_sub_f32_e32 v39, v78, v106
	v_mul_f32_e32 v39, 0x3fb8aa3b, v39
	v_exp_f32_e32 v55, v39
	v_sub_f32_e32 v39, v79, v106
	v_mul_f32_e32 v39, 0x3fb8aa3b, v39
	v_exp_f32_e32 v57, v39
	v_sub_f32_e32 v39, v80, v106
	v_mul_f32_e32 v39, 0x3fb8aa3b, v39
	v_exp_f32_e32 v71, v39
	v_sub_f32_e32 v39, v81, v106
	v_mul_f32_e32 v39, 0x3fb8aa3b, v39
	v_exp_f32_e32 v105, v39
	v_sub_f32_e32 v39, v82, v106
	v_pk_add_f32 v[64:65], v[62:63], v[74:75]
	v_mul_f32_e32 v39, 0x3fb8aa3b, v39
	v_pk_add_f32 v[68:69], v[64:65], v[64:65] op_sel_hi:[0,1]
	v_exp_f32_e32 v64, v39
	v_sub_f32_e32 v39, v83, v106
	v_mul_f32_e32 v39, 0x3fb8aa3b, v39
	v_exp_f32_e32 v72, v39
	v_sub_f32_e32 v39, v84, v106
	v_mul_f32_e32 v39, 0x3fb8aa3b, v39
	v_exp_f32_e32 v68, v39
	v_sub_f32_e32 v39, v85, v106
	v_pk_add_f32 v[58:59], v[58:59], v[58:59] op_sel_hi:[0,1]
	v_mul_f32_e32 v39, 0x3fb8aa3b, v39
	v_exp_f32_e32 v58, v39
	v_sub_f32_e32 v39, v86, v106
	v_mul_f32_e32 v39, 0x3fb8aa3b, v39
	v_exp_f32_e32 v80, v39
	v_sub_f32_e32 v39, v87, v106
	v_mul_f32_e32 v39, 0x3fb8aa3b, v39
	v_exp_f32_e32 v82, v39
	v_sub_f32_e32 v39, v88, v106
	v_mul_f32_e32 v39, 0x3fb8aa3b, v39
	v_exp_f32_e32 v81, v39
	v_sub_f32_e32 v39, v89, v106
	v_mul_f32_e32 v39, 0x3fb8aa3b, v39
	v_exp_f32_e32 v83, v39
	v_sub_f32_e32 v39, v200, v106
	v_add_f32_e32 v65, v55, v57
	v_add_f32_e32 v73, v71, v105
	v_mul_f32_e32 v39, 0x3fb8aa3b, v39
	v_pk_add_f32 v[66:67], v[64:65], v[72:73]
	v_exp_f32_e32 v65, v39
	v_sub_f32_e32 v39, v201, v106
	v_mul_f32_e32 v39, 0x3fb8aa3b, v39
	v_pk_add_f32 v[76:77], v[68:69], v[58:59]
	v_exp_f32_e32 v69, v39
	v_sub_f32_e32 v39, v202, v106
	v_mul_f32_e32 v39, 0x3fb8aa3b, v39
	v_exp_f32_e32 v73, v39
	v_sub_f32_e32 v39, v203, v106
	v_mul_f32_e32 v39, 0x3fb8aa3b, v39
	v_exp_f32_e32 v115, v39
	v_sub_f32_e32 v39, v90, v106
	v_mul_f32_e32 v39, 0x3fb8aa3b, v39
	v_exp_f32_e32 v84, v39
	v_sub_f32_e32 v39, v91, v106
	v_pk_add_f32 v[66:67], v[66:67], v[76:77]
	v_mul_f32_e32 v39, 0x3fb8aa3b, v39
	v_pk_add_f32 v[78:79], v[66:67], v[66:67] op_sel_hi:[0,1]
	v_pk_add_f32 v[66:67], v[80:81], v[82:83]
	v_exp_f32_e32 v86, v39
	v_sub_f32_e32 v39, v92, v106
	v_pk_add_f32 v[76:77], v[66:67], v[66:67] op_sel_hi:[0,1]
	v_mul_f32_e32 v39, 0x3fb8aa3b, v39
	v_exp_f32_e32 v76, v39
	v_sub_f32_e32 v39, v93, v106
	v_mul_f32_e32 v39, 0x3fb8aa3b, v39
	v_exp_f32_e32 v78, v39
	v_add_f32_e32 v85, v65, v69
	v_add_f32_e32 v87, v73, v115
	v_pk_add_f32 v[66:67], v[84:85], v[86:87]
	v_pk_add_f32 v[88:89], v[76:77], v[78:79]
	v_bfe_u32 v77, v36, 16, 1
	v_pk_add_f32 v[66:67], v[66:67], v[88:89]
	v_bfe_u32 v79, v37, 16, 1
	v_add_f32_e32 v39, v66, v67
	ds_bpermute_b32 v41, v193, v39
	v_add3_u32 v37, v37, v79, s22
	v_add3_u32 v36, v36, v77, s22
	v_bfe_u32 v67, v35, 16, 1
	v_lshrrev_b32_e32 v36, 16, v36
	s_waitcnt lgkmcnt(0)
; __device__ __forceinline__ unsigned pk2(float lo, float hi) { return f2bf(lo) | (f2bf(hi) << 16); }
; __device__ __forceinline__ bf16x8 pack_b(const f32x4 a, const f32x4 b) {
;     v4u r; r.x = pk2(a.x, a.y); r.y = pk2(a.z, a.w); r.z = pk2(b.x, b.y); r.w = pk2(b.z, b.w);
;     return __builtin_bit_cast(bf16x8, r);
; __device__ __forceinline__ void xattn_unit(const Params& P, LAS unsigned char* lds, int unit, int tid, int lane, int wave) {
;     ...
;         l += __shfl_xor(l, 16); l += __shfl_xor(l, 32);
;         inv[ps] = 1.0f / l;
; #pragma unroll
;         for (int s = 0; s < 8; ++s) Bp[ps][s] = pack_b(St[2 * s], St[2 * s + 1]);
	v_add_f32_e32 v39, v39, v41
	ds_bpermute_b32 v41, v194, v39
	v_lshrrev_b32_e32 v37, 16, v37
	v_add3_u32 v35, v35, v67, s22
	v_lshrrev_b32_e32 v35, 16, v35
	v_bfe_u32 v67, v109, 16, 1
	s_waitcnt lgkmcnt(0)
	v_add_f32_e32 v39, v39, v41
	v_div_scale_f32 v41, s[30:31], v39, v39, 1.0
	v_rcp_f32_e32 v47, v41
	v_bfe_u32 v77, v44, 16, 1
	v_bfe_u32 v79, v45, 16, 1
	v_bfe_u32 v85, v111, 16, 1
	v_fma_f32 v49, -v41, v47, 1.0
	v_fmac_f32_e32 v47, v49, v47
	v_div_scale_f32 v49, vcc, 1.0, v39, 1.0
	v_mul_f32_e32 v59, v49, v47
	v_fma_f32 v66, -v41, v59, v49
	v_fmac_f32_e32 v59, v66, v47
	v_fma_f32 v41, -v41, v59, v49
	v_div_fmas_f32 v41, v41, v47, v59
	v_div_fixup_f32 v66, v41, v39, 1.0
	v_bfe_u32 v39, v97, 16, 1
	v_bfe_u32 v41, v96, 16, 1
	v_add3_u32 v41, v96, v41, s22
	v_add3_u32 v39, v97, v39, s22
	v_bfe_u32 v47, v95, 16, 1
	v_and_or_b32 v37, v39, s28, v37
	v_and_or_b32 v36, v41, s28, v36
	v_bfe_u32 v39, v40, 16, 1
	v_bfe_u32 v41, v100, 16, 1
	v_add3_u32 v47, v95, v47, s22
	v_bfe_u32 v59, v34, 16, 1
	v_add3_u32 v39, v40, v39, s22
	v_add3_u32 v40, v100, v41, s22
	v_bfe_u32 v41, v38, 16, 1
	v_bfe_u32 v49, v94, 16, 1
	v_add3_u32 v34, v34, v59, s22
	v_and_or_b32 v35, v47, s28, v35
	v_bfe_u32 v47, v110, 16, 1
	v_add3_u32 v38, v38, v41, s22
	v_add3_u32 v41, v44, v77, s22
	v_add3_u32 v44, v109, v67, s22
	v_add3_u32 v49, v94, v49, s22
	v_lshrrev_b32_e32 v34, 16, v34
	v_add3_u32 v47, v110, v47, s22
	v_bfe_u32 v59, v107, 16, 1
	v_lshrrev_b32_e32 v38, 16, v38
	v_lshrrev_b32_e32 v44, 16, v44
	v_lshrrev_b32_e32 v67, 16, v41
	v_and_or_b32 v34, v49, s28, v34
	v_bfe_u32 v49, v108, 16, 1
	v_add3_u32 v59, v107, v59, s22
	v_and_or_b32 v41, v39, s28, v38
	v_and_or_b32 v40, v40, s28, v67
	v_and_or_b32 v39, v47, s28, v44
	v_bfe_u32 v44, v112, 16, 1
	v_bfe_u32 v47, v101, 16, 1
	v_bfe_u32 v67, v42, 16, 1
	v_add3_u32 v85, v111, v85, s22
	v_add3_u32 v45, v45, v79, s22
	v_add3_u32 v49, v108, v49, s22
	v_lshrrev_b32_e32 v59, 16, v59
	v_add3_u32 v47, v101, v47, s22
	v_add3_u32 v44, v112, v44, s22
	v_bfe_u32 v77, v43, 16, 1
	v_add3_u32 v42, v42, v67, s22
	v_lshrrev_b32_e32 v67, 16, v45
	v_lshrrev_b32_e32 v45, 16, v85
	v_and_or_b32 v38, v49, s28, v59
	v_bfe_u32 v49, v99, 16, 1
	v_add3_u32 v43, v43, v77, s22
	v_and_or_b32 v45, v44, s28, v45
	v_and_or_b32 v44, v47, s28, v67
	v_bfe_u32 v47, v46, 16, 1
	v_add3_u32 v49, v99, v49, s22
	v_lshrrev_b32_e32 v43, 16, v43
	v_bfe_u32 v67, v52, 16, 1
	v_add3_u32 v46, v46, v47, s22
	v_bfe_u32 v47, v50, 16, 1
	v_bfe_u32 v79, v61, 16, 1
	v_bfe_u32 v59, v98, 16, 1
	v_and_or_b32 v43, v49, s28, v43
	v_bfe_u32 v49, v103, 16, 1
	v_add3_u32 v52, v52, v67, s22
	v_bfe_u32 v67, v48, 16, 1
	v_bfe_u32 v77, v60, 16, 1
	v_add3_u32 v47, v50, v47, s22
	v_add3_u32 v50, v61, v79, s22
	v_add3_u32 v59, v98, v59, s22
	v_lshrrev_b32_e32 v42, 16, v42
	v_add3_u32 v49, v103, v49, s22
	v_add3_u32 v60, v60, v77, s22
	v_add3_u32 v48, v48, v67, s22
	v_lshrrev_b32_e32 v50, 16, v50
	v_and_or_b32 v42, v59, s28, v42
	v_bfe_u32 v59, v102, 16, 1
	v_lshrrev_b32_e32 v47, 16, v47
	v_lshrrev_b32_e32 v61, 16, v48
	v_lshrrev_b32_e32 v48, 16, v60
	v_and_or_b32 v49, v49, s28, v50
	v_bfe_u32 v50, v56, 16, 1
	v_bfe_u32 v60, v53, 16, 1
	v_add3_u32 v59, v102, v59, s22
	v_and_or_b32 v47, v46, s28, v47
	v_and_or_b32 v46, v52, s28, v61
	v_add3_u32 v50, v56, v50, s22
	v_add3_u32 v56, v53, v60, s22
	v_bfe_u32 v53, v54, 16, 1
	v_bfe_u32 v60, v51, 16, 1
	v_bfe_u32 v61, v113, 16, 1
	v_and_or_b32 v48, v59, s28, v48
	v_bfe_u32 v59, v114, 16, 1
	v_bfe_u32 v67, v70, 16, 1
	v_add3_u32 v53, v54, v53, s22
	v_add3_u32 v61, v113, v61, s22
	v_add3_u32 v51, v51, v60, s22
	v_add3_u32 v59, v114, v59, s22
	v_add3_u32 v54, v70, v67, s22
	v_lshrrev_b32_e32 v53, 16, v53
	v_lshrrev_b32_e32 v60, 16, v51
	v_lshrrev_b32_e32 v51, 16, v61
	v_bfe_u32 v61, v63, 16, 1
	v_bfe_u32 v67, v55, 16, 1
	v_bfe_u32 v52, v104, 16, 1
	v_and_or_b32 v53, v50, s28, v53
	v_and_or_b32 v51, v59, s28, v51
	v_and_or_b32 v50, v56, s28, v60
	v_bfe_u32 v56, v57, 16, 1
	v_bfe_u32 v59, v75, 16, 1
	v_add3_u32 v55, v55, v67, s22
	v_add3_u32 v61, v63, v61, s22
	v_add3_u32 v52, v104, v52, s22
	v_lshrrev_b32_e32 v54, 16, v54
	v_add3_u32 v59, v75, v59, s22
	v_add3_u32 v56, v57, v56, s22
	v_bfe_u32 v57, v62, 16, 1
	v_bfe_u32 v70, v71, 16, 1
	v_lshrrev_b32_e32 v61, 16, v61
	v_lshrrev_b32_e32 v55, 16, v55
	v_and_or_b32 v52, v52, s28, v54
	v_bfe_u32 v54, v105, 16, 1
	v_bfe_u32 v60, v74, 16, 1
	v_add3_u32 v70, v71, v70, s22
	v_add3_u32 v57, v62, v57, s22
	v_and_or_b32 v56, v56, s28, v55
	v_and_or_b32 v55, v59, s28, v61
	v_bfe_u32 v59, v58, 16, 1
	v_bfe_u32 v61, v82, 16, 1
	v_add3_u32 v60, v74, v60, s22
	v_add3_u32 v54, v105, v54, s22
	v_lshrrev_b32_e32 v62, 16, v57
	v_lshrrev_b32_e32 v57, 16, v70
	v_add3_u32 v58, v58, v59, s22
	v_add3_u32 v63, v82, v61, s22
	v_bfe_u32 v59, v68, 16, 1
	v_bfe_u32 v61, v64, 16, 1
	v_bfe_u32 v67, v80, 16, 1
	v_bfe_u32 v70, v81, 16, 1
	v_and_or_b32 v57, v54, s28, v57
	v_and_or_b32 v54, v60, s28, v62
	v_bfe_u32 v60, v83, 16, 1
	v_bfe_u32 v62, v72, 16, 1
	v_add3_u32 v59, v68, v59, s22
	v_add3_u32 v68, v81, v70, s22
	v_add3_u32 v67, v80, v67, s22
	v_add3_u32 v61, v64, v61, s22
	v_add3_u32 v62, v72, v62, s22
	v_add3_u32 v60, v83, v60, s22
	v_lshrrev_b32_e32 v59, 16, v59
	v_lshrrev_b32_e32 v64, 16, v61
	v_lshrrev_b32_e32 v67, 16, v67
	v_lshrrev_b32_e32 v61, 16, v68
	v_and_or_b32 v59, v58, s28, v59
	v_and_or_b32 v61, v60, s28, v61
	v_and_or_b32 v60, v63, s28, v67
	v_and_or_b32 v58, v62, s28, v64
	v_bfe_u32 v64, v115, 16, 1
	v_bfe_u32 v67, v69, 16, 1
	v_add3_u32 v67, v69, v67, s22
	v_add3_u32 v68, v115, v64, s22
	v_bfe_u32 v64, v76, 16, 1
	v_bfe_u32 v69, v65, 16, 1
	v_bfe_u32 v62, v78, 16, 1
	v_bfe_u32 v70, v73, 16, 1
	v_bfe_u32 v71, v84, 16, 1
; #define LAS __attribute__((address_space(3)))
; __device__ __forceinline__ void xattn_stage(LAS unsigned char* lds, const bf16* src, int tid) {
;     v4u tmp[16];
;     asm volatile("" : "+v"(tid));
;     const unsigned voff = (unsigned)tid * 16u;
; #pragma unroll
;     for (int r = 0; r < 16; ++r) { const unsigned char* sb = (const unsigned char*)src + r * 8192;
;         asm volatile("s_nop 4\n\tglobal_load_dwordx4 %0, %1, %2" : "=&v"(tmp[r]) : "v"(voff), "s"(sb) : "memory"); }
;     asm volatile("s_waitcnt vmcnt(0)" : "+v"(tmp[0]), "+v"(tmp[1]), "+v"(tmp[2]), "+v"(tmp[3]), "+v"(tmp[4]), "+v"(tmp[5]), "+v"(tmp[6]), "+v"(tmp[7]),
;                                         "+v"(tmp[8]), "+v"(tmp[9]), "+v"(tmp[10]), "+v"(tmp[11]), "+v"(tmp[12]), "+v"(tmp[13]), "+v"(tmp[14]), "+v"(tmp[15]) :: "memory");
; #pragma unroll
;     for (int r = 0; r < 16; ++r) { const int id = tid + 512 * r; *(LAS v4u*)(lds + (id >> 5) * 528 + (id & 31) * 16) = tmp[r]; }
; }
; __device__ __forceinline__ void xattn_unit(const Params& P, LAS unsigned char* lds, int unit, int tid, int lane, int wave) {
;     ...
;     __syncthreads();
;     xattn_stage(lds, Vt, tid);
;     __syncthreads();
; #pragma unroll
;     for (int ps = 0; ps < XA_NPS; ++ps) {
;         __builtin_amdgcn_sched_barrier(0); asm volatile("" : "+v"(col), "+v"(g) :: "memory");
;         bf16* AO = (bf16*)(P.ws + WS_AO) + (size_t)(tw + 128 * ps + col) * 1024 + h * 256 + 4 * g;
;         bf16x8 fr[2][8];
; #pragma unroll
;         for (int s = 0; s < 8; ++s) fr[0][s] = *(const LAS bf16x8*)(arow + 64 * s);
	v_add3_u32 v64, v76, v64, s22
	v_add3_u32 v65, v65, v69, s22
	v_bfe_u32 v63, v86, 16, 1
	v_add3_u32 v62, v78, v62, s22
	v_add3_u32 v71, v84, v71, s22
	v_add3_u32 v70, v73, v70, s22
	v_lshrrev_b32_e32 v64, 16, v64
	v_lshrrev_b32_e32 v69, 16, v65
	v_add3_u32 v63, v86, v63, s22
	v_lshrrev_b32_e32 v70, 16, v70
	v_lshrrev_b32_e32 v71, 16, v71
	v_and_or_b32 v65, v62, s28, v64
	v_and_or_b32 v62, v67, s28, v69
	v_mov_b32_e32 v67, v0
	v_and_or_b32 v64, v63, s28, v71
	v_and_or_b32 v63, v68, s28, v70
	s_nop 0
	v_lshlrev_b32_e32 v124, 4, v67
	s_nop 4
	global_load_dwordx4 v[68:71], v124, s[4:5]
	s_nop 4
	global_load_dwordx4 v[72:75], v124, s[6:7]
	s_nop 4
	global_load_dwordx4 v[76:79], v124, s[8:9]
	s_nop 4
	global_load_dwordx4 v[80:83], v124, s[10:11]
	s_nop 4
	global_load_dwordx4 v[84:87], v124, s[12:13]
	s_nop 4
	global_load_dwordx4 v[88:91], v124, s[14:15]
	s_nop 4
	global_load_dwordx4 v[92:95], v124, s[16:17]
	s_nop 4
	global_load_dwordx4 v[96:99], v124, s[18:19]
	s_nop 4
	global_load_dwordx4 v[100:103], v124, s[20:21]
	s_nop 4
	global_load_dwordx4 v[104:107], v124, s[36:37]
	s_nop 4
	global_load_dwordx4 v[108:111], v124, s[38:39]
	s_nop 4
	global_load_dwordx4 v[112:115], v124, s[40:41]
	s_nop 4
	global_load_dwordx4 v[116:119], v124, s[42:43]
	s_nop 4
	global_load_dwordx4 v[120:123], v124, s[44:45]
	s_nop 4
	global_load_dwordx4 v[128:131], v124, s[46:47]
	s_nop 4
	global_load_dwordx4 v[194:197], v124, s[48:49]
	v_and_b32_e32 v124, 0x1f0, v124
	v_add_u32_e32 v124, 0, v124
	v_ashrrev_i32_e32 v125, 5, v67
	s_waitcnt vmcnt(0)
	v_mad_u64_u32 v[198:199], s[4:5], v125, s27, v[124:125]
	ds_write_b128 v198, v[68:71]
	v_add_u32_e32 v68, 0x200, v67
	v_ashrrev_i32_e32 v68, 5, v68
	v_mad_u64_u32 v[68:69], s[4:5], v68, s27, v[124:125]
	ds_write_b128 v68, v[72:75]
	v_add_u32_e32 v68, 0x400, v67
	v_ashrrev_i32_e32 v68, 5, v68
	v_mad_u64_u32 v[68:69], s[4:5], v68, s27, v[124:125]
	ds_write_b128 v68, v[76:79]
	v_add_u32_e32 v68, 0x600, v67
	v_ashrrev_i32_e32 v68, 5, v68
	v_mad_u64_u32 v[68:69], s[4:5], v68, s27, v[124:125]
	ds_write_b128 v68, v[80:83]
	v_add_u32_e32 v68, 0x800, v67
	v_ashrrev_i32_e32 v68, 5, v68
	v_mad_u64_u32 v[68:69], s[4:5], v68, s27, v[124:125]
	ds_write_b128 v68, v[84:87]
	v_add_u32_e32 v68, 0xa00, v67
	v_ashrrev_i32_e32 v68, 5, v68
	v_mad_u64_u32 v[68:69], s[4:5], v68, s27, v[124:125]
	ds_write_b128 v68, v[88:91]
	v_add_u32_e32 v68, 0xc00, v67
	v_ashrrev_i32_e32 v68, 5, v68
	v_mad_u64_u32 v[68:69], s[4:5], v68, s27, v[124:125]
	ds_write_b128 v68, v[92:95]
	v_add_u32_e32 v68, 0xe00, v67
	v_ashrrev_i32_e32 v68, 5, v68
	v_mad_u64_u32 v[68:69], s[4:5], v68, s27, v[124:125]
	ds_write_b128 v68, v[96:99]
	v_add_u32_e32 v68, 0x1000, v67
	v_ashrrev_i32_e32 v68, 5, v68
	v_mad_u64_u32 v[68:69], s[4:5], v68, s27, v[124:125]
	ds_write_b128 v68, v[100:103]
	v_add_u32_e32 v68, 0x1200, v67
	v_ashrrev_i32_e32 v68, 5, v68
	v_mad_u64_u32 v[68:69], s[4:5], v68, s27, v[124:125]
	ds_write_b128 v68, v[104:107]
	v_add_u32_e32 v68, 0x1400, v67
	v_ashrrev_i32_e32 v68, 5, v68
	v_mad_u64_u32 v[68:69], s[4:5], v68, s27, v[124:125]
	ds_write_b128 v68, v[108:111]
	v_add_u32_e32 v68, 0x1600, v67
	v_ashrrev_i32_e32 v68, 5, v68
	v_mad_u64_u32 v[68:69], s[4:5], v68, s27, v[124:125]
	ds_write_b128 v68, v[112:115]
	v_add_u32_e32 v68, 0x1800, v67
	v_ashrrev_i32_e32 v68, 5, v68
	v_mad_u64_u32 v[68:69], s[4:5], v68, s27, v[124:125]
	ds_write_b128 v68, v[116:119]
	v_add_u32_e32 v68, 0x1a00, v67
	v_ashrrev_i32_e32 v68, 5, v68
	v_mad_u64_u32 v[68:69], s[4:5], v68, s27, v[124:125]
	ds_write_b128 v68, v[120:123]
	v_add_u32_e32 v68, 0x1c00, v67
	v_ashrrev_i32_e32 v68, 5, v68
	v_add_u32_e32 v67, 0x1e00, v67
	v_mad_u64_u32 v[68:69], s[4:5], v68, s27, v[124:125]
	v_ashrrev_i32_e32 v67, 5, v67
	ds_write_b128 v68, v[128:131]
	v_mad_u64_u32 v[68:69], s[4:5], v67, s27, v[124:125]
	ds_write_b128 v68, v[194:197]
	s_waitcnt lgkmcnt(0)
	s_barrier
	ds_read_b128 v[70:73], v191 offset:448
	ds_read_b128 v[74:77], v191 offset:384
	ds_read_b128 v[78:81], v191 offset:320
	ds_read_b128 v[82:85], v191 offset:256
	ds_read_b128 v[86:89], v191 offset:192
	ds_read_b128 v[90:93], v191 offset:128
	ds_read_b128 v[94:97], v191 offset:64
	ds_read_b128 v[98:101], v191
	ds_read_b128 v[102:105], v191 offset:8896
	ds_read_b128 v[106:109], v191 offset:8832
	ds_read_b128 v[110:113], v191 offset:8768
	ds_read_b128 v[114:117], v191 offset:8704
	ds_read_b128 v[118:121], v191 offset:8640
	ds_read_b128 v[122:125], v191 offset:8576
	ds_read_b128 v[128:131], v191 offset:8512
	ds_read_b128 v[194:197], v191 offset:8448
	v_add_u32_e32 v68, s23, v1
	v_ashrrev_i32_e32 v69, 31, v68
	v_lshlrev_b64 v[68:69], 11, v[68:69]
	v_lshlrev_b32_e32 v198, 2, v192
	v_ashrrev_i32_e32 v199, 31, v198
	v_lshl_add_u64 v[68:69], s[0:1], 0, v[68:69]
	v_lshl_add_u64 v[68:69], v[198:199], 1, v[68:69]
	s_waitcnt lgkmcnt(8)
; #define LAS __attribute__((address_space(3)))
; __device__ __forceinline__ unsigned pk2(float lo, float hi) { return f2bf(lo) | (f2bf(hi) << 16); }
; #define PIN8(a) asm volatile("" : "+v"(a[0]), "+v"(a[1]), "+v"(a[2]), "+v"(a[3]), "+v"(a[4]), "+v"(a[5]), "+v"(a[6]), "+v"(a[7]))
; __device__ __forceinline__ void xattn_unit(const Params& P, LAS unsigned char* lds, int unit, int tid, int lane, int wave) {
;     ...
;         for (int del = 0; del < 16; ++del) {
;             if (del + 1 < 16) {
; #pragma unroll
;                 for (int s = 0; s < 8; ++s) fr[(del + 1) & 1][s] = *(const LAS bf16x8*)(arow + (16 * (del + 1)) * 528 + 64 * s);
;             }
;             __builtin_amdgcn_sched_barrier(0);
;             PIN8(fr[del & 1]);
;             f32x4 acc = (f32x4){0.f, 0.f, 0.f, 0.f};
; #pragma unroll
;             for (int s = 0; s < 8; ++s) acc = __builtin_amdgcn_mfma_f32_16x16x32_bf16(fr[del & 1][s], Bp[ps][s], acc, 0, 0, 0);
;             v2u o; o.x = pk2(acc.x * inv[ps], acc.y * inv[ps]); o.y = pk2(acc.z * inv[ps], acc.w * inv[ps]);
;             *(v2u*)(AO + 16 * del) = o;
;             __builtin_amdgcn_sched_barrier(0);
;         }
	v_mov_b32_e32 v67, 1
	v_mfma_f32_16x16x32_bf16 v[98:101], v[98:101], v[2:5], 0
	v_mfma_f32_16x16x32_bf16 v[94:97], v[94:97], v[6:9], v[98:101]
	v_mfma_f32_16x16x32_bf16 v[90:93], v[90:93], v[10:13], v[94:97]
	v_mfma_f32_16x16x32_bf16 v[86:89], v[86:89], v[14:17], v[90:93]
	v_mfma_f32_16x16x32_bf16 v[82:85], v[82:85], v[18:21], v[86:89]
	v_mfma_f32_16x16x32_bf16 v[78:81], v[78:81], v[22:25], v[82:85]
	v_mfma_f32_16x16x32_bf16 v[74:77], v[74:77], v[26:29], v[78:81]
	v_mfma_f32_16x16x32_bf16 v[70:73], v[70:73], v[30:33], v[74:77]
	s_nop 7
	v_mov_b32_e32 v75, v72
	v_mov_b32_e32 v72, v71
	v_mov_b32_e32 v74, v70
	v_pk_mul_f32 v[72:73], v[126:127], v[72:73] op_sel_hi:[0,1]
	v_pk_mul_f32 v[70:71], v[126:127], v[74:75] op_sel_hi:[0,1]
	v_and_b32_sdwa v76, v73, v67 dst_sel:DWORD dst_unused:UNUSED_PAD src0_sel:WORD_1 src1_sel:DWORD
	v_and_b32_sdwa v77, v72, v67 dst_sel:DWORD dst_unused:UNUSED_PAD src0_sel:WORD_1 src1_sel:DWORD
	v_and_b32_sdwa v74, v71, v67 dst_sel:DWORD dst_unused:UNUSED_PAD src0_sel:WORD_1 src1_sel:DWORD
	v_and_b32_sdwa v75, v70, v67 dst_sel:DWORD dst_unused:UNUSED_PAD src0_sel:WORD_1 src1_sel:DWORD
	v_add3_u32 v73, v73, v76, s22
	v_add3_u32 v72, v72, v77, s22
	v_add3_u32 v70, v70, v75, s22
	v_add3_u32 v71, v71, v74, s22
	v_and_b32_e32 v73, 0xffff0000, v73
	v_and_b32_e32 v72, 0xffff0000, v72
	v_or_b32_sdwa v71, v73, v71 dst_sel:DWORD dst_unused:UNUSED_PAD src0_sel:DWORD src1_sel:WORD_1
	v_or_b32_sdwa v70, v72, v70 dst_sel:DWORD dst_unused:UNUSED_PAD src0_sel:DWORD src1_sel:WORD_1
	global_store_dwordx2 v[68:69], v[70:71], off sc0 sc1
	ds_read_b128 v[70:73], v191 offset:17344
	ds_read_b128 v[74:77], v191 offset:17280
	ds_read_b128 v[78:81], v191 offset:17216
	ds_read_b128 v[82:85], v191 offset:17152
	ds_read_b128 v[86:89], v191 offset:17088
	ds_read_b128 v[90:93], v191 offset:17024
	ds_read_b128 v[94:97], v191 offset:16960
	ds_read_b128 v[98:101], v191 offset:16896
	s_waitcnt lgkmcnt(8)
	s_nop 0
	v_mfma_f32_16x16x32_bf16 v[194:197], v[194:197], v[2:5], 0
	v_mfma_f32_16x16x32_bf16 v[128:131], v[128:131], v[6:9], v[194:197]
	v_mfma_f32_16x16x32_bf16 v[122:125], v[122:125], v[10:13], v[128:131]
	v_mfma_f32_16x16x32_bf16 v[118:121], v[118:121], v[14:17], v[122:125]
	v_mfma_f32_16x16x32_bf16 v[114:117], v[114:117], v[18:21], v[118:121]
	v_mfma_f32_16x16x32_bf16 v[110:113], v[110:113], v[22:25], v[114:117]
	v_mfma_f32_16x16x32_bf16 v[106:109], v[106:109], v[26:29], v[110:113]
	v_mfma_f32_16x16x32_bf16 v[102:105], v[102:105], v[30:33], v[106:109]
	s_nop 7
	v_mov_b32_e32 v107, v104
	v_mov_b32_e32 v104, v103
	v_mov_b32_e32 v106, v102
	v_pk_mul_f32 v[104:105], v[126:127], v[104:105] op_sel_hi:[0,1]
	v_pk_mul_f32 v[102:103], v[126:127], v[106:107] op_sel_hi:[0,1]
	v_and_b32_sdwa v108, v105, v67 dst_sel:DWORD dst_unused:UNUSED_PAD src0_sel:WORD_1 src1_sel:DWORD
	v_and_b32_sdwa v109, v104, v67 dst_sel:DWORD dst_unused:UNUSED_PAD src0_sel:WORD_1 src1_sel:DWORD
	v_and_b32_sdwa v106, v103, v67 dst_sel:DWORD dst_unused:UNUSED_PAD src0_sel:WORD_1 src1_sel:DWORD
	v_and_b32_sdwa v107, v102, v67 dst_sel:DWORD dst_unused:UNUSED_PAD src0_sel:WORD_1 src1_sel:DWORD
	v_add3_u32 v105, v105, v108, s22
	v_add3_u32 v104, v104, v109, s22
	v_add3_u32 v102, v102, v107, s22
	v_add3_u32 v103, v103, v106, s22
	v_and_b32_e32 v105, 0xffff0000, v105
	v_and_b32_e32 v104, 0xffff0000, v104
	v_or_b32_sdwa v103, v105, v103 dst_sel:DWORD dst_unused:UNUSED_PAD src0_sel:DWORD src1_sel:WORD_1
	v_or_b32_sdwa v102, v104, v102 dst_sel:DWORD dst_unused:UNUSED_PAD src0_sel:DWORD src1_sel:WORD_1
	global_store_dwordx2 v[68:69], v[102:103], off offset:32 sc0 sc1
	ds_read_b128 v[102:105], v191 offset:25792
	ds_read_b128 v[106:109], v191 offset:25728
	ds_read_b128 v[110:113], v191 offset:25664
	ds_read_b128 v[114:117], v191 offset:25600
	ds_read_b128 v[118:121], v191 offset:25536
	ds_read_b128 v[122:125], v191 offset:25472
	ds_read_b128 v[128:131], v191 offset:25408
	ds_read_b128 v[194:197], v191 offset:25344
	s_waitcnt lgkmcnt(8)
	s_nop 0
	v_mfma_f32_16x16x32_bf16 v[98:101], v[98:101], v[2:5], 0
	v_mfma_f32_16x16x32_bf16 v[94:97], v[94:97], v[6:9], v[98:101]
	v_mfma_f32_16x16x32_bf16 v[90:93], v[90:93], v[10:13], v[94:97]
	v_mfma_f32_16x16x32_bf16 v[86:89], v[86:89], v[14:17], v[90:93]
	v_mfma_f32_16x16x32_bf16 v[82:85], v[82:85], v[18:21], v[86:89]
	v_mfma_f32_16x16x32_bf16 v[78:81], v[78:81], v[22:25], v[82:85]
	v_mfma_f32_16x16x32_bf16 v[74:77], v[74:77], v[26:29], v[78:81]
	v_mfma_f32_16x16x32_bf16 v[70:73], v[70:73], v[30:33], v[74:77]
	s_nop 7
	v_mov_b32_e32 v75, v72
	v_mov_b32_e32 v72, v71
	v_mov_b32_e32 v74, v70
	v_pk_mul_f32 v[72:73], v[126:127], v[72:73] op_sel_hi:[0,1]
	v_pk_mul_f32 v[70:71], v[126:127], v[74:75] op_sel_hi:[0,1]
	v_and_b32_sdwa v76, v73, v67 dst_sel:DWORD dst_unused:UNUSED_PAD src0_sel:WORD_1 src1_sel:DWORD
	v_and_b32_sdwa v77, v72, v67 dst_sel:DWORD dst_unused:UNUSED_PAD src0_sel:WORD_1 src1_sel:DWORD
	v_and_b32_sdwa v74, v71, v67 dst_sel:DWORD dst_unused:UNUSED_PAD src0_sel:WORD_1 src1_sel:DWORD
	v_and_b32_sdwa v75, v70, v67 dst_sel:DWORD dst_unused:UNUSED_PAD src0_sel:WORD_1 src1_sel:DWORD
	v_add3_u32 v73, v73, v76, s22
	v_add3_u32 v72, v72, v77, s22
	v_add3_u32 v70, v70, v75, s22
	v_add3_u32 v71, v71, v74, s22
	v_and_b32_e32 v73, 0xffff0000, v73
	v_and_b32_e32 v72, 0xffff0000, v72
	v_or_b32_sdwa v71, v73, v71 dst_sel:DWORD dst_unused:UNUSED_PAD src0_sel:DWORD src1_sel:WORD_1
	v_or_b32_sdwa v70, v72, v70 dst_sel:DWORD dst_unused:UNUSED_PAD src0_sel:DWORD src1_sel:WORD_1
	global_store_dwordx2 v[68:69], v[70:71], off offset:64 sc0 sc1
	ds_read_b128 v[70:73], v191 offset:34240
	ds_read_b128 v[74:77], v191 offset:34176
	ds_read_b128 v[78:81], v191 offset:34112
	ds_read_b128 v[82:85], v191 offset:34048
	ds_read_b128 v[86:89], v191 offset:33984
	ds_read_b128 v[90:93], v191 offset:33920
	ds_read_b128 v[94:97], v191 offset:33856
	ds_read_b128 v[98:101], v191 offset:33792
	s_waitcnt lgkmcnt(8)
; #define LAS __attribute__((address_space(3)))
; __device__ __forceinline__ unsigned pk2(float lo, float hi) { return f2bf(lo) | (f2bf(hi) << 16); }
; #define PIN8(a) asm volatile("" : "+v"(a[0]), "+v"(a[1]), "+v"(a[2]), "+v"(a[3]), "+v"(a[4]), "+v"(a[5]), "+v"(a[6]), "+v"(a[7]))
; __device__ __forceinline__ void xattn_unit(const Params& P, LAS unsigned char* lds, int unit, int tid, int lane, int wave) {
;     ...
;         for (int del = 0; del < 16; ++del) {
;             if (del + 1 < 16) {
; #pragma unroll
;                 for (int s = 0; s < 8; ++s) fr[(del + 1) & 1][s] = *(const LAS bf16x8*)(arow + (16 * (del + 1)) * 528 + 64 * s);
;             }
;             __builtin_amdgcn_sched_barrier(0);
;             PIN8(fr[del & 1]);
;             f32x4 acc = (f32x4){0.f, 0.f, 0.f, 0.f};
; #pragma unroll
;             for (int s = 0; s < 8; ++s) acc = __builtin_amdgcn_mfma_f32_16x16x32_bf16(fr[del & 1][s], Bp[ps][s], acc, 0, 0, 0);
;             v2u o; o.x = pk2(acc.x * inv[ps], acc.y * inv[ps]); o.y = pk2(acc.z * inv[ps], acc.w * inv[ps]);
;             *(v2u*)(AO + 16 * del) = o;
;             __builtin_amdgcn_sched_barrier(0);
;         }
	s_nop 0
	v_mfma_f32_16x16x32_bf16 v[194:197], v[194:197], v[2:5], 0
	v_mfma_f32_16x16x32_bf16 v[128:131], v[128:131], v[6:9], v[194:197]
	v_mfma_f32_16x16x32_bf16 v[122:125], v[122:125], v[10:13], v[128:131]
	v_mfma_f32_16x16x32_bf16 v[118:121], v[118:121], v[14:17], v[122:125]
	v_mfma_f32_16x16x32_bf16 v[114:117], v[114:117], v[18:21], v[118:121]
	v_mfma_f32_16x16x32_bf16 v[110:113], v[110:113], v[22:25], v[114:117]
	v_mfma_f32_16x16x32_bf16 v[106:109], v[106:109], v[26:29], v[110:113]
	v_mfma_f32_16x16x32_bf16 v[102:105], v[102:105], v[30:33], v[106:109]
	s_nop 7
	v_mov_b32_e32 v107, v104
	v_mov_b32_e32 v104, v103
	v_mov_b32_e32 v106, v102
	v_pk_mul_f32 v[104:105], v[126:127], v[104:105] op_sel_hi:[0,1]
	v_pk_mul_f32 v[102:103], v[126:127], v[106:107] op_sel_hi:[0,1]
	v_and_b32_sdwa v108, v105, v67 dst_sel:DWORD dst_unused:UNUSED_PAD src0_sel:WORD_1 src1_sel:DWORD
	v_and_b32_sdwa v109, v104, v67 dst_sel:DWORD dst_unused:UNUSED_PAD src0_sel:WORD_1 src1_sel:DWORD
	v_and_b32_sdwa v106, v103, v67 dst_sel:DWORD dst_unused:UNUSED_PAD src0_sel:WORD_1 src1_sel:DWORD
	v_and_b32_sdwa v107, v102, v67 dst_sel:DWORD dst_unused:UNUSED_PAD src0_sel:WORD_1 src1_sel:DWORD
	v_add3_u32 v105, v105, v108, s22
	v_add3_u32 v104, v104, v109, s22
	v_add3_u32 v102, v102, v107, s22
	v_add3_u32 v103, v103, v106, s22
	v_and_b32_e32 v105, 0xffff0000, v105
	v_and_b32_e32 v104, 0xffff0000, v104
	v_or_b32_sdwa v103, v105, v103 dst_sel:DWORD dst_unused:UNUSED_PAD src0_sel:DWORD src1_sel:WORD_1
	v_or_b32_sdwa v102, v104, v102 dst_sel:DWORD dst_unused:UNUSED_PAD src0_sel:DWORD src1_sel:WORD_1
	global_store_dwordx2 v[68:69], v[102:103], off offset:96 sc0 sc1
	ds_read_b128 v[102:105], v191 offset:42688
	ds_read_b128 v[106:109], v191 offset:42624
	ds_read_b128 v[110:113], v191 offset:42560
	ds_read_b128 v[114:117], v191 offset:42496
	ds_read_b128 v[118:121], v191 offset:42432
	ds_read_b128 v[122:125], v191 offset:42368
	ds_read_b128 v[128:131], v191 offset:42304
	ds_read_b128 v[194:197], v191 offset:42240
	s_waitcnt lgkmcnt(8)
	s_nop 0
	v_mfma_f32_16x16x32_bf16 v[98:101], v[98:101], v[2:5], 0
	v_mfma_f32_16x16x32_bf16 v[94:97], v[94:97], v[6:9], v[98:101]
	v_mfma_f32_16x16x32_bf16 v[90:93], v[90:93], v[10:13], v[94:97]
	v_mfma_f32_16x16x32_bf16 v[86:89], v[86:89], v[14:17], v[90:93]
	v_mfma_f32_16x16x32_bf16 v[82:85], v[82:85], v[18:21], v[86:89]
	v_mfma_f32_16x16x32_bf16 v[78:81], v[78:81], v[22:25], v[82:85]
	v_mfma_f32_16x16x32_bf16 v[74:77], v[74:77], v[26:29], v[78:81]
	v_mfma_f32_16x16x32_bf16 v[70:73], v[70:73], v[30:33], v[74:77]
	s_nop 7
	v_mov_b32_e32 v75, v72
	v_mov_b32_e32 v72, v71
	v_mov_b32_e32 v74, v70
	v_pk_mul_f32 v[72:73], v[126:127], v[72:73] op_sel_hi:[0,1]
	v_pk_mul_f32 v[70:71], v[126:127], v[74:75] op_sel_hi:[0,1]
	v_and_b32_sdwa v76, v73, v67 dst_sel:DWORD dst_unused:UNUSED_PAD src0_sel:WORD_1 src1_sel:DWORD
	v_and_b32_sdwa v77, v72, v67 dst_sel:DWORD dst_unused:UNUSED_PAD src0_sel:WORD_1 src1_sel:DWORD
	v_and_b32_sdwa v74, v71, v67 dst_sel:DWORD dst_unused:UNUSED_PAD src0_sel:WORD_1 src1_sel:DWORD
	v_and_b32_sdwa v75, v70, v67 dst_sel:DWORD dst_unused:UNUSED_PAD src0_sel:WORD_1 src1_sel:DWORD
	v_add3_u32 v73, v73, v76, s22
	v_add3_u32 v72, v72, v77, s22
	v_add3_u32 v70, v70, v75, s22
	v_add3_u32 v71, v71, v74, s22
	v_and_b32_e32 v73, 0xffff0000, v73
	v_and_b32_e32 v72, 0xffff0000, v72
	v_or_b32_sdwa v71, v73, v71 dst_sel:DWORD dst_unused:UNUSED_PAD src0_sel:DWORD src1_sel:WORD_1
	v_or_b32_sdwa v70, v72, v70 dst_sel:DWORD dst_unused:UNUSED_PAD src0_sel:DWORD src1_sel:WORD_1
	global_store_dwordx2 v[68:69], v[70:71], off offset:128 sc0 sc1
	ds_read_b128 v[70:73], v191 offset:51136
	ds_read_b128 v[74:77], v191 offset:51072
	ds_read_b128 v[78:81], v191 offset:51008
	ds_read_b128 v[82:85], v191 offset:50944
	ds_read_b128 v[86:89], v191 offset:50880
	ds_read_b128 v[90:93], v191 offset:50816
	ds_read_b128 v[94:97], v191 offset:50752
	ds_read_b128 v[98:101], v191 offset:50688
	s_waitcnt lgkmcnt(8)
	s_nop 0
	v_mfma_f32_16x16x32_bf16 v[194:197], v[194:197], v[2:5], 0
	v_mfma_f32_16x16x32_bf16 v[128:131], v[128:131], v[6:9], v[194:197]
	v_mfma_f32_16x16x32_bf16 v[122:125], v[122:125], v[10:13], v[128:131]
	v_mfma_f32_16x16x32_bf16 v[118:121], v[118:121], v[14:17], v[122:125]
	v_mfma_f32_16x16x32_bf16 v[114:117], v[114:117], v[18:21], v[118:121]
	v_mfma_f32_16x16x32_bf16 v[110:113], v[110:113], v[22:25], v[114:117]
	v_mfma_f32_16x16x32_bf16 v[106:109], v[106:109], v[26:29], v[110:113]
	v_mfma_f32_16x16x32_bf16 v[102:105], v[102:105], v[30:33], v[106:109]
	s_nop 7
	v_mov_b32_e32 v107, v104
	v_mov_b32_e32 v104, v103
	v_mov_b32_e32 v106, v102
	v_pk_mul_f32 v[104:105], v[126:127], v[104:105] op_sel_hi:[0,1]
	v_pk_mul_f32 v[102:103], v[126:127], v[106:107] op_sel_hi:[0,1]
	v_and_b32_sdwa v108, v105, v67 dst_sel:DWORD dst_unused:UNUSED_PAD src0_sel:WORD_1 src1_sel:DWORD
	v_and_b32_sdwa v109, v104, v67 dst_sel:DWORD dst_unused:UNUSED_PAD src0_sel:WORD_1 src1_sel:DWORD
	v_and_b32_sdwa v106, v103, v67 dst_sel:DWORD dst_unused:UNUSED_PAD src0_sel:WORD_1 src1_sel:DWORD
	v_and_b32_sdwa v107, v102, v67 dst_sel:DWORD dst_unused:UNUSED_PAD src0_sel:WORD_1 src1_sel:DWORD
	v_add3_u32 v105, v105, v108, s22
	v_add3_u32 v104, v104, v109, s22
	v_add3_u32 v102, v102, v107, s22
	v_add3_u32 v103, v103, v106, s22
	v_and_b32_e32 v105, 0xffff0000, v105
	v_and_b32_e32 v104, 0xffff0000, v104
	v_or_b32_sdwa v103, v105, v103 dst_sel:DWORD dst_unused:UNUSED_PAD src0_sel:DWORD src1_sel:WORD_1
	v_or_b32_sdwa v102, v104, v102 dst_sel:DWORD dst_unused:UNUSED_PAD src0_sel:DWORD src1_sel:WORD_1
	global_store_dwordx2 v[68:69], v[102:103], off offset:160 sc0 sc1
	ds_read_b128 v[102:105], v191 offset:59584
	ds_read_b128 v[106:109], v191 offset:59520
	ds_read_b128 v[110:113], v191 offset:59456
	ds_read_b128 v[114:117], v191 offset:59392
	ds_read_b128 v[118:121], v191 offset:59328
	ds_read_b128 v[122:125], v191 offset:59264
	ds_read_b128 v[128:131], v191 offset:59200
	ds_read_b128 v[194:197], v191 offset:59136
	s_waitcnt lgkmcnt(8)
; #define LAS __attribute__((address_space(3)))
; __device__ __forceinline__ unsigned pk2(float lo, float hi) { return f2bf(lo) | (f2bf(hi) << 16); }
; #define PIN8(a) asm volatile("" : "+v"(a[0]), "+v"(a[1]), "+v"(a[2]), "+v"(a[3]), "+v"(a[4]), "+v"(a[5]), "+v"(a[6]), "+v"(a[7]))
; __device__ __forceinline__ void xattn_unit(const Params& P, LAS unsigned char* lds, int unit, int tid, int lane, int wave) {
;     ...
;         for (int del = 0; del < 16; ++del) {
;             if (del + 1 < 16) {
; #pragma unroll
;                 for (int s = 0; s < 8; ++s) fr[(del + 1) & 1][s] = *(const LAS bf16x8*)(arow + (16 * (del + 1)) * 528 + 64 * s);
;             }
;             __builtin_amdgcn_sched_barrier(0);
;             PIN8(fr[del & 1]);
;             f32x4 acc = (f32x4){0.f, 0.f, 0.f, 0.f};
; #pragma unroll
;             for (int s = 0; s < 8; ++s) acc = __builtin_amdgcn_mfma_f32_16x16x32_bf16(fr[del & 1][s], Bp[ps][s], acc, 0, 0, 0);
;             v2u o; o.x = pk2(acc.x * inv[ps], acc.y * inv[ps]); o.y = pk2(acc.z * inv[ps], acc.w * inv[ps]);
;             *(v2u*)(AO + 16 * del) = o;
;             __builtin_amdgcn_sched_barrier(0);
;         }
	s_nop 0
	v_mfma_f32_16x16x32_bf16 v[98:101], v[98:101], v[2:5], 0
	v_mfma_f32_16x16x32_bf16 v[94:97], v[94:97], v[6:9], v[98:101]
	v_mfma_f32_16x16x32_bf16 v[90:93], v[90:93], v[10:13], v[94:97]
	v_mfma_f32_16x16x32_bf16 v[86:89], v[86:89], v[14:17], v[90:93]
	v_mfma_f32_16x16x32_bf16 v[82:85], v[82:85], v[18:21], v[86:89]
	v_mfma_f32_16x16x32_bf16 v[78:81], v[78:81], v[22:25], v[82:85]
	v_mfma_f32_16x16x32_bf16 v[74:77], v[74:77], v[26:29], v[78:81]
	v_mfma_f32_16x16x32_bf16 v[70:73], v[70:73], v[30:33], v[74:77]
	s_nop 7
	v_mov_b32_e32 v75, v72
	v_mov_b32_e32 v72, v71
	v_mov_b32_e32 v74, v70
	v_pk_mul_f32 v[72:73], v[126:127], v[72:73] op_sel_hi:[0,1]
	v_pk_mul_f32 v[70:71], v[126:127], v[74:75] op_sel_hi:[0,1]
	v_and_b32_sdwa v76, v73, v67 dst_sel:DWORD dst_unused:UNUSED_PAD src0_sel:WORD_1 src1_sel:DWORD
	v_and_b32_sdwa v77, v72, v67 dst_sel:DWORD dst_unused:UNUSED_PAD src0_sel:WORD_1 src1_sel:DWORD
	v_and_b32_sdwa v74, v71, v67 dst_sel:DWORD dst_unused:UNUSED_PAD src0_sel:WORD_1 src1_sel:DWORD
	v_and_b32_sdwa v75, v70, v67 dst_sel:DWORD dst_unused:UNUSED_PAD src0_sel:WORD_1 src1_sel:DWORD
	v_add3_u32 v73, v73, v76, s22
	v_add3_u32 v72, v72, v77, s22
	v_add3_u32 v70, v70, v75, s22
	v_add3_u32 v71, v71, v74, s22
	v_and_b32_e32 v73, 0xffff0000, v73
	v_and_b32_e32 v72, 0xffff0000, v72
	v_or_b32_sdwa v71, v73, v71 dst_sel:DWORD dst_unused:UNUSED_PAD src0_sel:DWORD src1_sel:WORD_1
	v_or_b32_sdwa v70, v72, v70 dst_sel:DWORD dst_unused:UNUSED_PAD src0_sel:DWORD src1_sel:WORD_1
	global_store_dwordx2 v[68:69], v[70:71], off offset:192 sc0 sc1
	ds_read_b128 v[70:73], v190
	ds_read_b128 v[74:77], v189
	ds_read_b128 v[78:81], v188
	ds_read_b128 v[82:85], v187
	ds_read_b128 v[86:89], v186
	ds_read_b128 v[90:93], v185
	ds_read_b128 v[94:97], v184
	ds_read_b128 v[98:101], v183
	s_waitcnt lgkmcnt(8)
	s_nop 0
	v_mfma_f32_16x16x32_bf16 v[194:197], v[194:197], v[2:5], 0
	v_mfma_f32_16x16x32_bf16 v[128:131], v[128:131], v[6:9], v[194:197]
	v_mfma_f32_16x16x32_bf16 v[122:125], v[122:125], v[10:13], v[128:131]
	v_mfma_f32_16x16x32_bf16 v[118:121], v[118:121], v[14:17], v[122:125]
	v_mfma_f32_16x16x32_bf16 v[114:117], v[114:117], v[18:21], v[118:121]
	v_mfma_f32_16x16x32_bf16 v[110:113], v[110:113], v[22:25], v[114:117]
	v_mfma_f32_16x16x32_bf16 v[106:109], v[106:109], v[26:29], v[110:113]
	v_mfma_f32_16x16x32_bf16 v[102:105], v[102:105], v[30:33], v[106:109]
	s_nop 7
	v_mov_b32_e32 v107, v104
	v_mov_b32_e32 v104, v103
	v_mov_b32_e32 v106, v102
	v_pk_mul_f32 v[104:105], v[126:127], v[104:105] op_sel_hi:[0,1]
	v_pk_mul_f32 v[102:103], v[126:127], v[106:107] op_sel_hi:[0,1]
	v_and_b32_sdwa v108, v105, v67 dst_sel:DWORD dst_unused:UNUSED_PAD src0_sel:WORD_1 src1_sel:DWORD
	v_and_b32_sdwa v109, v104, v67 dst_sel:DWORD dst_unused:UNUSED_PAD src0_sel:WORD_1 src1_sel:DWORD
	v_and_b32_sdwa v106, v103, v67 dst_sel:DWORD dst_unused:UNUSED_PAD src0_sel:WORD_1 src1_sel:DWORD
	v_and_b32_sdwa v107, v102, v67 dst_sel:DWORD dst_unused:UNUSED_PAD src0_sel:WORD_1 src1_sel:DWORD
	v_add3_u32 v105, v105, v108, s22
	v_add3_u32 v104, v104, v109, s22
	v_add3_u32 v102, v102, v107, s22
	v_add3_u32 v103, v103, v106, s22
	v_and_b32_e32 v105, 0xffff0000, v105
	v_and_b32_e32 v104, 0xffff0000, v104
	v_or_b32_sdwa v103, v105, v103 dst_sel:DWORD dst_unused:UNUSED_PAD src0_sel:DWORD src1_sel:WORD_1
	v_or_b32_sdwa v102, v104, v102 dst_sel:DWORD dst_unused:UNUSED_PAD src0_sel:DWORD src1_sel:WORD_1
	global_store_dwordx2 v[68:69], v[102:103], off offset:224 sc0 sc1
	ds_read_b128 v[102:105], v182
	ds_read_b128 v[106:109], v181
	ds_read_b128 v[110:113], v180
	ds_read_b128 v[114:117], v179
	ds_read_b128 v[118:121], v178
	ds_read_b128 v[122:125], v177
	ds_read_b128 v[128:131], v176
	ds_read_b128 v[194:197], v175
	s_waitcnt lgkmcnt(8)
	s_nop 0
	v_mfma_f32_16x16x32_bf16 v[98:101], v[98:101], v[2:5], 0
	v_mfma_f32_16x16x32_bf16 v[94:97], v[94:97], v[6:9], v[98:101]
	v_mfma_f32_16x16x32_bf16 v[90:93], v[90:93], v[10:13], v[94:97]
	v_mfma_f32_16x16x32_bf16 v[86:89], v[86:89], v[14:17], v[90:93]
	v_mfma_f32_16x16x32_bf16 v[82:85], v[82:85], v[18:21], v[86:89]
	v_mfma_f32_16x16x32_bf16 v[78:81], v[78:81], v[22:25], v[82:85]
	v_mfma_f32_16x16x32_bf16 v[74:77], v[74:77], v[26:29], v[78:81]
	v_mfma_f32_16x16x32_bf16 v[70:73], v[70:73], v[30:33], v[74:77]
	s_nop 7
	v_mov_b32_e32 v75, v72
	v_mov_b32_e32 v72, v71
	v_mov_b32_e32 v74, v70
	v_pk_mul_f32 v[72:73], v[126:127], v[72:73] op_sel_hi:[0,1]
	v_pk_mul_f32 v[70:71], v[126:127], v[74:75] op_sel_hi:[0,1]
	v_and_b32_sdwa v76, v73, v67 dst_sel:DWORD dst_unused:UNUSED_PAD src0_sel:WORD_1 src1_sel:DWORD
	v_and_b32_sdwa v77, v72, v67 dst_sel:DWORD dst_unused:UNUSED_PAD src0_sel:WORD_1 src1_sel:DWORD
	v_and_b32_sdwa v74, v71, v67 dst_sel:DWORD dst_unused:UNUSED_PAD src0_sel:WORD_1 src1_sel:DWORD
	v_and_b32_sdwa v75, v70, v67 dst_sel:DWORD dst_unused:UNUSED_PAD src0_sel:WORD_1 src1_sel:DWORD
	v_add3_u32 v73, v73, v76, s22
	v_add3_u32 v72, v72, v77, s22
	v_add3_u32 v70, v70, v75, s22
	v_add3_u32 v71, v71, v74, s22
	v_and_b32_e32 v73, 0xffff0000, v73
	v_and_b32_e32 v72, 0xffff0000, v72
	v_or_b32_sdwa v71, v73, v71 dst_sel:DWORD dst_unused:UNUSED_PAD src0_sel:DWORD src1_sel:WORD_1
	v_or_b32_sdwa v70, v72, v70 dst_sel:DWORD dst_unused:UNUSED_PAD src0_sel:DWORD src1_sel:WORD_1
	global_store_dwordx2 v[68:69], v[70:71], off offset:256 sc0 sc1
	ds_read_b128 v[70:73], v174
	ds_read_b128 v[74:77], v173
	ds_read_b128 v[78:81], v172
	ds_read_b128 v[82:85], v171
	ds_read_b128 v[86:89], v170
	ds_read_b128 v[90:93], v169
	ds_read_b128 v[94:97], v168
	ds_read_b128 v[98:101], v167
	s_waitcnt lgkmcnt(8)
; #define LAS __attribute__((address_space(3)))
; __device__ __forceinline__ unsigned pk2(float lo, float hi) { return f2bf(lo) | (f2bf(hi) << 16); }
; #define PIN8(a) asm volatile("" : "+v"(a[0]), "+v"(a[1]), "+v"(a[2]), "+v"(a[3]), "+v"(a[4]), "+v"(a[5]), "+v"(a[6]), "+v"(a[7]))
; __device__ __forceinline__ void xattn_unit(const Params& P, LAS unsigned char* lds, int unit, int tid, int lane, int wave) {
;     ...
;         for (int del = 0; del < 16; ++del) {
;             if (del + 1 < 16) {
; #pragma unroll
;                 for (int s = 0; s < 8; ++s) fr[(del + 1) & 1][s] = *(const LAS bf16x8*)(arow + (16 * (del + 1)) * 528 + 64 * s);
;             }
;             __builtin_amdgcn_sched_barrier(0);
;             PIN8(fr[del & 1]);
;             f32x4 acc = (f32x4){0.f, 0.f, 0.f, 0.f};
; #pragma unroll
;             for (int s = 0; s < 8; ++s) acc = __builtin_amdgcn_mfma_f32_16x16x32_bf16(fr[del & 1][s], Bp[ps][s], acc, 0, 0, 0);
;             v2u o; o.x = pk2(acc.x * inv[ps], acc.y * inv[ps]); o.y = pk2(acc.z * inv[ps], acc.w * inv[ps]);
;             *(v2u*)(AO + 16 * del) = o;
;             __builtin_amdgcn_sched_barrier(0);
;         }
	s_nop 0
	v_mfma_f32_16x16x32_bf16 v[194:197], v[194:197], v[2:5], 0
	v_mfma_f32_16x16x32_bf16 v[128:131], v[128:131], v[6:9], v[194:197]
	v_mfma_f32_16x16x32_bf16 v[122:125], v[122:125], v[10:13], v[128:131]
	v_mfma_f32_16x16x32_bf16 v[118:121], v[118:121], v[14:17], v[122:125]
	v_mfma_f32_16x16x32_bf16 v[114:117], v[114:117], v[18:21], v[118:121]
	v_mfma_f32_16x16x32_bf16 v[110:113], v[110:113], v[22:25], v[114:117]
	v_mfma_f32_16x16x32_bf16 v[106:109], v[106:109], v[26:29], v[110:113]
	v_mfma_f32_16x16x32_bf16 v[102:105], v[102:105], v[30:33], v[106:109]
	s_nop 7
	v_mov_b32_e32 v107, v104
	v_mov_b32_e32 v104, v103
	v_mov_b32_e32 v106, v102
	v_pk_mul_f32 v[104:105], v[126:127], v[104:105] op_sel_hi:[0,1]
	v_pk_mul_f32 v[102:103], v[126:127], v[106:107] op_sel_hi:[0,1]
	v_and_b32_sdwa v108, v105, v67 dst_sel:DWORD dst_unused:UNUSED_PAD src0_sel:WORD_1 src1_sel:DWORD
	v_and_b32_sdwa v109, v104, v67 dst_sel:DWORD dst_unused:UNUSED_PAD src0_sel:WORD_1 src1_sel:DWORD
	v_and_b32_sdwa v106, v103, v67 dst_sel:DWORD dst_unused:UNUSED_PAD src0_sel:WORD_1 src1_sel:DWORD
	v_and_b32_sdwa v107, v102, v67 dst_sel:DWORD dst_unused:UNUSED_PAD src0_sel:WORD_1 src1_sel:DWORD
	v_add3_u32 v105, v105, v108, s22
	v_add3_u32 v104, v104, v109, s22
	v_add3_u32 v102, v102, v107, s22
	v_add3_u32 v103, v103, v106, s22
	v_and_b32_e32 v105, 0xffff0000, v105
	v_and_b32_e32 v104, 0xffff0000, v104
	v_or_b32_sdwa v103, v105, v103 dst_sel:DWORD dst_unused:UNUSED_PAD src0_sel:DWORD src1_sel:WORD_1
	v_or_b32_sdwa v102, v104, v102 dst_sel:DWORD dst_unused:UNUSED_PAD src0_sel:DWORD src1_sel:WORD_1
	global_store_dwordx2 v[68:69], v[102:103], off offset:288 sc0 sc1
	ds_read_b128 v[102:105], v166
	ds_read_b128 v[106:109], v165
	ds_read_b128 v[110:113], v164
	ds_read_b128 v[114:117], v163
	ds_read_b128 v[118:121], v162
	ds_read_b128 v[122:125], v161
	ds_read_b128 v[128:131], v160
	ds_read_b128 v[194:197], v159
	s_waitcnt lgkmcnt(8)
	s_nop 0
	v_mfma_f32_16x16x32_bf16 v[98:101], v[98:101], v[2:5], 0
	v_mfma_f32_16x16x32_bf16 v[94:97], v[94:97], v[6:9], v[98:101]
	v_mfma_f32_16x16x32_bf16 v[90:93], v[90:93], v[10:13], v[94:97]
	v_mfma_f32_16x16x32_bf16 v[86:89], v[86:89], v[14:17], v[90:93]
	v_mfma_f32_16x16x32_bf16 v[82:85], v[82:85], v[18:21], v[86:89]
	v_mfma_f32_16x16x32_bf16 v[78:81], v[78:81], v[22:25], v[82:85]
	v_mfma_f32_16x16x32_bf16 v[74:77], v[74:77], v[26:29], v[78:81]
	v_mfma_f32_16x16x32_bf16 v[70:73], v[70:73], v[30:33], v[74:77]
	s_nop 7
	v_mov_b32_e32 v75, v72
	v_mov_b32_e32 v72, v71
	v_mov_b32_e32 v74, v70
	v_pk_mul_f32 v[72:73], v[126:127], v[72:73] op_sel_hi:[0,1]
	v_pk_mul_f32 v[70:71], v[126:127], v[74:75] op_sel_hi:[0,1]
	v_and_b32_sdwa v76, v73, v67 dst_sel:DWORD dst_unused:UNUSED_PAD src0_sel:WORD_1 src1_sel:DWORD
	v_and_b32_sdwa v77, v72, v67 dst_sel:DWORD dst_unused:UNUSED_PAD src0_sel:WORD_1 src1_sel:DWORD
	v_and_b32_sdwa v74, v71, v67 dst_sel:DWORD dst_unused:UNUSED_PAD src0_sel:WORD_1 src1_sel:DWORD
	v_and_b32_sdwa v75, v70, v67 dst_sel:DWORD dst_unused:UNUSED_PAD src0_sel:WORD_1 src1_sel:DWORD
	v_add3_u32 v73, v73, v76, s22
	v_add3_u32 v72, v72, v77, s22
	v_add3_u32 v70, v70, v75, s22
	v_add3_u32 v71, v71, v74, s22
	v_and_b32_e32 v73, 0xffff0000, v73
	v_and_b32_e32 v72, 0xffff0000, v72
	v_or_b32_sdwa v71, v73, v71 dst_sel:DWORD dst_unused:UNUSED_PAD src0_sel:DWORD src1_sel:WORD_1
	v_or_b32_sdwa v70, v72, v70 dst_sel:DWORD dst_unused:UNUSED_PAD src0_sel:DWORD src1_sel:WORD_1
	global_store_dwordx2 v[68:69], v[70:71], off offset:320 sc0 sc1
	ds_read_b128 v[70:73], v158
	ds_read_b128 v[74:77], v157
	ds_read_b128 v[78:81], v156
	ds_read_b128 v[82:85], v155
	ds_read_b128 v[86:89], v154
	ds_read_b128 v[90:93], v153
	ds_read_b128 v[94:97], v152
	ds_read_b128 v[98:101], v151
	s_waitcnt lgkmcnt(8)
	s_nop 0
	v_mfma_f32_16x16x32_bf16 v[194:197], v[194:197], v[2:5], 0
	v_mfma_f32_16x16x32_bf16 v[128:131], v[128:131], v[6:9], v[194:197]
	v_mfma_f32_16x16x32_bf16 v[122:125], v[122:125], v[10:13], v[128:131]
	v_mfma_f32_16x16x32_bf16 v[118:121], v[118:121], v[14:17], v[122:125]
	v_mfma_f32_16x16x32_bf16 v[114:117], v[114:117], v[18:21], v[118:121]
	v_mfma_f32_16x16x32_bf16 v[110:113], v[110:113], v[22:25], v[114:117]
	v_mfma_f32_16x16x32_bf16 v[106:109], v[106:109], v[26:29], v[110:113]
	v_mfma_f32_16x16x32_bf16 v[102:105], v[102:105], v[30:33], v[106:109]
	s_nop 7
	v_mov_b32_e32 v107, v104
	v_mov_b32_e32 v104, v103
	v_mov_b32_e32 v106, v102
	v_pk_mul_f32 v[104:105], v[126:127], v[104:105] op_sel_hi:[0,1]
	v_pk_mul_f32 v[102:103], v[126:127], v[106:107] op_sel_hi:[0,1]
	v_and_b32_sdwa v108, v105, v67 dst_sel:DWORD dst_unused:UNUSED_PAD src0_sel:WORD_1 src1_sel:DWORD
	v_and_b32_sdwa v109, v104, v67 dst_sel:DWORD dst_unused:UNUSED_PAD src0_sel:WORD_1 src1_sel:DWORD
	v_and_b32_sdwa v106, v103, v67 dst_sel:DWORD dst_unused:UNUSED_PAD src0_sel:WORD_1 src1_sel:DWORD
	v_and_b32_sdwa v107, v102, v67 dst_sel:DWORD dst_unused:UNUSED_PAD src0_sel:WORD_1 src1_sel:DWORD
	v_add3_u32 v105, v105, v108, s22
	v_add3_u32 v104, v104, v109, s22
	v_add3_u32 v102, v102, v107, s22
	v_add3_u32 v103, v103, v106, s22
	v_and_b32_e32 v105, 0xffff0000, v105
	v_and_b32_e32 v104, 0xffff0000, v104
	v_or_b32_sdwa v103, v105, v103 dst_sel:DWORD dst_unused:UNUSED_PAD src0_sel:DWORD src1_sel:WORD_1
	v_or_b32_sdwa v102, v104, v102 dst_sel:DWORD dst_unused:UNUSED_PAD src0_sel:DWORD src1_sel:WORD_1
	global_store_dwordx2 v[68:69], v[102:103], off offset:352 sc0 sc1
	ds_read_b128 v[102:105], v150
	ds_read_b128 v[106:109], v149
	ds_read_b128 v[110:113], v148
	ds_read_b128 v[114:117], v147
	ds_read_b128 v[118:121], v146
	ds_read_b128 v[122:125], v145
	ds_read_b128 v[128:131], v144
	ds_read_b128 v[194:197], v143
	s_waitcnt lgkmcnt(8)
; #define LAS __attribute__((address_space(3)))
; __device__ __forceinline__ unsigned pk2(float lo, float hi) { return f2bf(lo) | (f2bf(hi) << 16); }
; #define PIN8(a) asm volatile("" : "+v"(a[0]), "+v"(a[1]), "+v"(a[2]), "+v"(a[3]), "+v"(a[4]), "+v"(a[5]), "+v"(a[6]), "+v"(a[7]))
; __device__ __forceinline__ void xattn_unit(const Params& P, LAS unsigned char* lds, int unit, int tid, int lane, int wave) {
;     ...
;         for (int del = 0; del < 16; ++del) {
;             if (del + 1 < 16) {
; #pragma unroll
;                 for (int s = 0; s < 8; ++s) fr[(del + 1) & 1][s] = *(const LAS bf16x8*)(arow + (16 * (del + 1)) * 528 + 64 * s);
;             }
;             __builtin_amdgcn_sched_barrier(0);
;             PIN8(fr[del & 1]);
;             f32x4 acc = (f32x4){0.f, 0.f, 0.f, 0.f};
; #pragma unroll
;             for (int s = 0; s < 8; ++s) acc = __builtin_amdgcn_mfma_f32_16x16x32_bf16(fr[del & 1][s], Bp[ps][s], acc, 0, 0, 0);
;             v2u o; o.x = pk2(acc.x * inv[ps], acc.y * inv[ps]); o.y = pk2(acc.z * inv[ps], acc.w * inv[ps]);
;             *(v2u*)(AO + 16 * del) = o;
;             __builtin_amdgcn_sched_barrier(0);
;         }
	s_nop 0
	v_mfma_f32_16x16x32_bf16 v[98:101], v[98:101], v[2:5], 0
	v_mfma_f32_16x16x32_bf16 v[94:97], v[94:97], v[6:9], v[98:101]
	v_mfma_f32_16x16x32_bf16 v[90:93], v[90:93], v[10:13], v[94:97]
	v_mfma_f32_16x16x32_bf16 v[86:89], v[86:89], v[14:17], v[90:93]
	v_mfma_f32_16x16x32_bf16 v[82:85], v[82:85], v[18:21], v[86:89]
	v_mfma_f32_16x16x32_bf16 v[78:81], v[78:81], v[22:25], v[82:85]
	v_mfma_f32_16x16x32_bf16 v[74:77], v[74:77], v[26:29], v[78:81]
	v_mfma_f32_16x16x32_bf16 v[70:73], v[70:73], v[30:33], v[74:77]
	s_nop 7
	v_mov_b32_e32 v75, v72
	v_mov_b32_e32 v72, v71
	v_mov_b32_e32 v74, v70
	v_pk_mul_f32 v[72:73], v[126:127], v[72:73] op_sel_hi:[0,1]
	v_pk_mul_f32 v[70:71], v[126:127], v[74:75] op_sel_hi:[0,1]
	v_and_b32_sdwa v76, v73, v67 dst_sel:DWORD dst_unused:UNUSED_PAD src0_sel:WORD_1 src1_sel:DWORD
	v_and_b32_sdwa v77, v72, v67 dst_sel:DWORD dst_unused:UNUSED_PAD src0_sel:WORD_1 src1_sel:DWORD
	v_and_b32_sdwa v74, v71, v67 dst_sel:DWORD dst_unused:UNUSED_PAD src0_sel:WORD_1 src1_sel:DWORD
	v_and_b32_sdwa v75, v70, v67 dst_sel:DWORD dst_unused:UNUSED_PAD src0_sel:WORD_1 src1_sel:DWORD
	v_add3_u32 v73, v73, v76, s22
	v_add3_u32 v72, v72, v77, s22
	v_add3_u32 v70, v70, v75, s22
	v_add3_u32 v71, v71, v74, s22
	v_and_b32_e32 v73, 0xffff0000, v73
	v_and_b32_e32 v72, 0xffff0000, v72
	v_or_b32_sdwa v71, v73, v71 dst_sel:DWORD dst_unused:UNUSED_PAD src0_sel:DWORD src1_sel:WORD_1
	v_or_b32_sdwa v70, v72, v70 dst_sel:DWORD dst_unused:UNUSED_PAD src0_sel:DWORD src1_sel:WORD_1
	global_store_dwordx2 v[68:69], v[70:71], off offset:384 sc0 sc1
	ds_read_b128 v[70:73], v142
	ds_read_b128 v[74:77], v141
	ds_read_b128 v[78:81], v140
	ds_read_b128 v[82:85], v139
	ds_read_b128 v[86:89], v138
	ds_read_b128 v[90:93], v137
	ds_read_b128 v[94:97], v136
	ds_read_b128 v[98:101], v135
	s_waitcnt lgkmcnt(8)
	s_nop 0
	v_mfma_f32_16x16x32_bf16 v[194:197], v[194:197], v[2:5], 0
	v_mfma_f32_16x16x32_bf16 v[128:131], v[128:131], v[6:9], v[194:197]
	v_mfma_f32_16x16x32_bf16 v[122:125], v[122:125], v[10:13], v[128:131]
	v_mfma_f32_16x16x32_bf16 v[118:121], v[118:121], v[14:17], v[122:125]
	v_mfma_f32_16x16x32_bf16 v[114:117], v[114:117], v[18:21], v[118:121]
	v_mfma_f32_16x16x32_bf16 v[110:113], v[110:113], v[22:25], v[114:117]
	v_mfma_f32_16x16x32_bf16 v[106:109], v[106:109], v[26:29], v[110:113]
	v_mfma_f32_16x16x32_bf16 v[102:105], v[102:105], v[30:33], v[106:109]
	s_nop 7
	v_mov_b32_e32 v107, v104
	v_mov_b32_e32 v104, v103
	v_mov_b32_e32 v106, v102
	v_pk_mul_f32 v[104:105], v[126:127], v[104:105] op_sel_hi:[0,1]
	v_pk_mul_f32 v[102:103], v[126:127], v[106:107] op_sel_hi:[0,1]
	v_and_b32_sdwa v108, v105, v67 dst_sel:DWORD dst_unused:UNUSED_PAD src0_sel:WORD_1 src1_sel:DWORD
	v_and_b32_sdwa v109, v104, v67 dst_sel:DWORD dst_unused:UNUSED_PAD src0_sel:WORD_1 src1_sel:DWORD
	v_and_b32_sdwa v106, v103, v67 dst_sel:DWORD dst_unused:UNUSED_PAD src0_sel:WORD_1 src1_sel:DWORD
	v_and_b32_sdwa v107, v102, v67 dst_sel:DWORD dst_unused:UNUSED_PAD src0_sel:WORD_1 src1_sel:DWORD
	v_add3_u32 v105, v105, v108, s22
	v_add3_u32 v104, v104, v109, s22
	v_add3_u32 v102, v102, v107, s22
	v_add3_u32 v103, v103, v106, s22
	v_and_b32_e32 v105, 0xffff0000, v105
	v_and_b32_e32 v104, 0xffff0000, v104
	v_or_b32_sdwa v103, v105, v103 dst_sel:DWORD dst_unused:UNUSED_PAD src0_sel:DWORD src1_sel:WORD_1
	v_or_b32_sdwa v102, v104, v102 dst_sel:DWORD dst_unused:UNUSED_PAD src0_sel:DWORD src1_sel:WORD_1
	global_store_dwordx2 v[68:69], v[102:103], off offset:416 sc0 sc1
	v_add_u32_e32 v198, 0x1f000, v191
	v_add_u32_e32 v200, 0x1ef80, v191
	ds_read_b128 v[102:105], v134
	ds_read_b128 v[106:109], v133
	ds_read_b128 v[110:113], v252
	ds_read_b128 v[114:117], v198
	ds_read_b128 v[118:121], v253
	ds_read_b128 v[122:125], v200
	ds_read_b128 v[128:131], v132
	ds_read_b128 v[194:197], v127
	s_waitcnt lgkmcnt(8)
	s_nop 0
	v_mfma_f32_16x16x32_bf16 v[98:101], v[98:101], v[2:5], 0
	v_mfma_f32_16x16x32_bf16 v[94:97], v[94:97], v[6:9], v[98:101]
	v_mfma_f32_16x16x32_bf16 v[90:93], v[90:93], v[10:13], v[94:97]
	v_mfma_f32_16x16x32_bf16 v[86:89], v[86:89], v[14:17], v[90:93]
	v_mfma_f32_16x16x32_bf16 v[82:85], v[82:85], v[18:21], v[86:89]
	v_mfma_f32_16x16x32_bf16 v[78:81], v[78:81], v[22:25], v[82:85]
	v_mfma_f32_16x16x32_bf16 v[74:77], v[74:77], v[26:29], v[78:81]
	v_mfma_f32_16x16x32_bf16 v[70:73], v[70:73], v[30:33], v[74:77]
	s_nop 7
	v_mov_b32_e32 v75, v72
	v_mov_b32_e32 v72, v71
	v_mov_b32_e32 v74, v70
	v_pk_mul_f32 v[72:73], v[126:127], v[72:73] op_sel_hi:[0,1]
	v_pk_mul_f32 v[70:71], v[126:127], v[74:75] op_sel_hi:[0,1]
	v_and_b32_sdwa v76, v73, v67 dst_sel:DWORD dst_unused:UNUSED_PAD src0_sel:WORD_1 src1_sel:DWORD
	v_and_b32_sdwa v77, v72, v67 dst_sel:DWORD dst_unused:UNUSED_PAD src0_sel:WORD_1 src1_sel:DWORD
	v_and_b32_sdwa v74, v71, v67 dst_sel:DWORD dst_unused:UNUSED_PAD src0_sel:WORD_1 src1_sel:DWORD
	v_and_b32_sdwa v75, v70, v67 dst_sel:DWORD dst_unused:UNUSED_PAD src0_sel:WORD_1 src1_sel:DWORD
	v_add3_u32 v73, v73, v76, s22
	v_add3_u32 v72, v72, v77, s22
	v_add3_u32 v70, v70, v75, s22
	v_add3_u32 v71, v71, v74, s22
	v_and_b32_e32 v73, 0xffff0000, v73
	v_and_b32_e32 v72, 0xffff0000, v72
	v_or_b32_sdwa v71, v73, v71 dst_sel:DWORD dst_unused:UNUSED_PAD src0_sel:DWORD src1_sel:WORD_1
	v_or_b32_sdwa v70, v72, v70 dst_sel:DWORD dst_unused:UNUSED_PAD src0_sel:DWORD src1_sel:WORD_1
	global_store_dwordx2 v[68:69], v[70:71], off offset:448 sc0 sc1
	s_waitcnt lgkmcnt(0)
; #define LAS __attribute__((address_space(3)))
; __device__ __forceinline__ unsigned pk2(float lo, float hi) { return f2bf(lo) | (f2bf(hi) << 16); }
; __device__ __forceinline__ void xattn_unit(const Params& P, LAS unsigned char* lds, int unit, int tid, int lane, int wave) {
;     ...
;     for (int ps = 0; ps < XA_NPS; ++ps) {
;         __builtin_amdgcn_sched_barrier(0); asm volatile("" : "+v"(col), "+v"(g) :: "memory");
;         bf16* AO = (bf16*)(P.ws + WS_AO) + (size_t)(tw + 128 * ps + col) * 1024 + h * 256 + 4 * g;
;         bf16x8 fr[2][8];
; #pragma unroll
;         for (int s = 0; s < 8; ++s) fr[0][s] = *(const LAS bf16x8*)(arow + 64 * s);
;     ...
;             for (int s = 0; s < 8; ++s) acc = __builtin_amdgcn_mfma_f32_16x16x32_bf16(fr[del & 1][s], Bp[ps][s], acc, 0, 0, 0);
;             v2u o; o.x = pk2(acc.x * inv[ps], acc.y * inv[ps]); o.y = pk2(acc.z * inv[ps], acc.w * inv[ps]);
;             *(v2u*)(AO + 16 * del) = o;
;             __builtin_amdgcn_sched_barrier(0);
;         }
	s_nop 0
	v_mfma_f32_16x16x32_bf16 v[2:5], v[194:197], v[2:5], 0
	v_mfma_f32_16x16x32_bf16 v[2:5], v[128:131], v[6:9], v[2:5]
	v_mfma_f32_16x16x32_bf16 v[2:5], v[122:125], v[10:13], v[2:5]
	v_mfma_f32_16x16x32_bf16 v[2:5], v[118:121], v[14:17], v[2:5]
	v_mfma_f32_16x16x32_bf16 v[2:5], v[114:117], v[18:21], v[2:5]
	v_mfma_f32_16x16x32_bf16 v[2:5], v[110:113], v[22:25], v[2:5]
	v_mfma_f32_16x16x32_bf16 v[2:5], v[106:109], v[26:29], v[2:5]
	v_mfma_f32_16x16x32_bf16 v[2:5], v[102:105], v[30:33], v[2:5]
	s_nop 7
	v_mov_b32_e32 v7, v4
	v_mov_b32_e32 v4, v3
	v_mov_b32_e32 v6, v2
	v_pk_mul_f32 v[4:5], v[126:127], v[4:5] op_sel_hi:[0,1]
	v_pk_mul_f32 v[2:3], v[126:127], v[6:7] op_sel_hi:[0,1]
	v_and_b32_sdwa v8, v5, v67 dst_sel:DWORD dst_unused:UNUSED_PAD src0_sel:WORD_1 src1_sel:DWORD
	v_and_b32_sdwa v9, v4, v67 dst_sel:DWORD dst_unused:UNUSED_PAD src0_sel:WORD_1 src1_sel:DWORD
	v_and_b32_sdwa v6, v3, v67 dst_sel:DWORD dst_unused:UNUSED_PAD src0_sel:WORD_1 src1_sel:DWORD
	v_and_b32_sdwa v7, v2, v67 dst_sel:DWORD dst_unused:UNUSED_PAD src0_sel:WORD_1 src1_sel:DWORD
	v_add3_u32 v5, v5, v8, s22
	v_add3_u32 v4, v4, v9, s22
	v_add3_u32 v2, v2, v7, s22
	v_add3_u32 v3, v3, v6, s22
	v_and_b32_e32 v5, 0xffff0000, v5
	v_and_b32_e32 v4, 0xffff0000, v4
	v_or_b32_sdwa v3, v5, v3 dst_sel:DWORD dst_unused:UNUSED_PAD src0_sel:DWORD src1_sel:WORD_1
	v_or_b32_sdwa v2, v4, v2 dst_sel:DWORD dst_unused:UNUSED_PAD src0_sel:DWORD src1_sel:WORD_1
	global_store_dwordx2 v[68:69], v[2:3], off offset:480 sc0 sc1
	ds_read_b128 v[4:7], v191 offset:448
	ds_read_b128 v[8:11], v191 offset:384
	ds_read_b128 v[12:15], v191 offset:320
	ds_read_b128 v[16:19], v191 offset:256
	ds_read_b128 v[20:23], v191 offset:192
	ds_read_b128 v[24:27], v191 offset:128
	ds_read_b128 v[28:31], v191 offset:64
	ds_read_b128 v[68:71], v191
	ds_read_b128 v[72:75], v191 offset:8896
	ds_read_b128 v[76:79], v191 offset:8832
	ds_read_b128 v[80:83], v191 offset:8768
	ds_read_b128 v[84:87], v191 offset:8704
	ds_read_b128 v[88:91], v191 offset:8640
	ds_read_b128 v[92:95], v191 offset:8576
	ds_read_b128 v[96:99], v191 offset:8512
	ds_read_b128 v[100:103], v191 offset:8448
	v_add_u32_e32 v2, s3, v1
	v_ashrrev_i32_e32 v3, 31, v2
	v_lshlrev_b64 v[2:3], 11, v[2:3]
	v_lshlrev_b32_e32 v32, 2, v192
	v_ashrrev_i32_e32 v33, 31, v32
	v_lshl_add_u64 v[2:3], s[0:1], 0, v[2:3]
	v_lshl_add_u64 v[2:3], v[32:33], 1, v[2:3]
	s_waitcnt lgkmcnt(8)
	s_nop 0
	v_mfma_f32_16x16x32_bf16 v[68:71], v[68:71], v[34:37], 0
	v_mfma_f32_16x16x32_bf16 v[28:31], v[28:31], v[38:41], v[68:71]
	v_mfma_f32_16x16x32_bf16 v[24:27], v[24:27], v[42:45], v[28:31]
	v_mfma_f32_16x16x32_bf16 v[20:23], v[20:23], v[46:49], v[24:27]
	v_mfma_f32_16x16x32_bf16 v[16:19], v[16:19], v[50:53], v[20:23]
	v_mfma_f32_16x16x32_bf16 v[12:15], v[12:15], v[54:57], v[16:19]
	v_mfma_f32_16x16x32_bf16 v[8:11], v[8:11], v[58:61], v[12:15]
	v_mfma_f32_16x16x32_bf16 v[4:7], v[4:7], v[62:65], v[8:11]
	s_nop 7
	v_mov_b32_e32 v8, v4
	v_mov_b32_e32 v9, v6
	v_mov_b32_e32 v6, v5
	v_pk_mul_f32 v[4:5], v[66:67], v[8:9] op_sel_hi:[0,1]
	v_pk_mul_f32 v[6:7], v[66:67], v[6:7] op_sel_hi:[0,1]
	v_and_b32_sdwa v1, v5, v67 dst_sel:DWORD dst_unused:UNUSED_PAD src0_sel:WORD_1 src1_sel:DWORD
	v_and_b32_sdwa v9, v7, v67 dst_sel:DWORD dst_unused:UNUSED_PAD src0_sel:WORD_1 src1_sel:DWORD
	v_and_b32_sdwa v10, v6, v67 dst_sel:DWORD dst_unused:UNUSED_PAD src0_sel:WORD_1 src1_sel:DWORD
	v_and_b32_sdwa v8, v4, v67 dst_sel:DWORD dst_unused:UNUSED_PAD src0_sel:WORD_1 src1_sel:DWORD
	v_add3_u32 v1, v5, v1, s22
	v_add3_u32 v5, v7, v9, s22
	v_add3_u32 v6, v6, v10, s22
	v_add3_u32 v4, v4, v8, s22
	v_and_b32_e32 v5, 0xffff0000, v5
	v_and_b32_e32 v6, 0xffff0000, v6
	v_or_b32_sdwa v5, v5, v1 dst_sel:DWORD dst_unused:UNUSED_PAD src0_sel:DWORD src1_sel:WORD_1
	v_or_b32_sdwa v4, v6, v4 dst_sel:DWORD dst_unused:UNUSED_PAD src0_sel:DWORD src1_sel:WORD_1
	global_store_dwordx2 v[2:3], v[4:5], off sc0 sc1
	ds_read_b128 v[4:7], v191 offset:17344
	ds_read_b128 v[8:11], v191 offset:17280
	ds_read_b128 v[12:15], v191 offset:17216
	ds_read_b128 v[16:19], v191 offset:17152
	ds_read_b128 v[20:23], v191 offset:17088
	ds_read_b128 v[24:27], v191 offset:17024
	ds_read_b128 v[28:31], v191 offset:16960
	ds_read_b128 v[68:71], v191 offset:16896
	s_waitcnt lgkmcnt(8)
	s_nop 0
	v_mfma_f32_16x16x32_bf16 v[100:103], v[100:103], v[34:37], 0
	v_mfma_f32_16x16x32_bf16 v[96:99], v[96:99], v[38:41], v[100:103]
	v_mfma_f32_16x16x32_bf16 v[92:95], v[92:95], v[42:45], v[96:99]
	v_mfma_f32_16x16x32_bf16 v[88:91], v[88:91], v[46:49], v[92:95]
	v_mfma_f32_16x16x32_bf16 v[84:87], v[84:87], v[50:53], v[88:91]
	v_mfma_f32_16x16x32_bf16 v[80:83], v[80:83], v[54:57], v[84:87]
	v_mfma_f32_16x16x32_bf16 v[76:79], v[76:79], v[58:61], v[80:83]
	v_mfma_f32_16x16x32_bf16 v[72:75], v[72:75], v[62:65], v[76:79]
	s_nop 7
	v_mov_b32_e32 v32, v72
	v_mov_b32_e32 v33, v74
	v_mov_b32_e32 v74, v73
	v_pk_mul_f32 v[32:33], v[66:67], v[32:33] op_sel_hi:[0,1]
	v_pk_mul_f32 v[72:73], v[66:67], v[74:75] op_sel_hi:[0,1]
	v_and_b32_sdwa v1, v33, v67 dst_sel:DWORD dst_unused:UNUSED_PAD src0_sel:WORD_1 src1_sel:DWORD
	v_and_b32_sdwa v75, v73, v67 dst_sel:DWORD dst_unused:UNUSED_PAD src0_sel:WORD_1 src1_sel:DWORD
	v_and_b32_sdwa v76, v72, v67 dst_sel:DWORD dst_unused:UNUSED_PAD src0_sel:WORD_1 src1_sel:DWORD
	v_and_b32_sdwa v74, v32, v67 dst_sel:DWORD dst_unused:UNUSED_PAD src0_sel:WORD_1 src1_sel:DWORD
	v_add3_u32 v1, v33, v1, s22
	v_add3_u32 v33, v73, v75, s22
	v_add3_u32 v72, v72, v76, s22
	v_add3_u32 v32, v32, v74, s22
	v_and_b32_e32 v33, 0xffff0000, v33
	v_and_b32_e32 v72, 0xffff0000, v72
	v_or_b32_sdwa v33, v33, v1 dst_sel:DWORD dst_unused:UNUSED_PAD src0_sel:DWORD src1_sel:WORD_1
	v_or_b32_sdwa v32, v72, v32 dst_sel:DWORD dst_unused:UNUSED_PAD src0_sel:DWORD src1_sel:WORD_1
	global_store_dwordx2 v[2:3], v[32:33], off offset:32 sc0 sc1
	ds_read_b128 v[72:75], v191 offset:25792
	ds_read_b128 v[76:79], v191 offset:25728
	ds_read_b128 v[80:83], v191 offset:25664
	ds_read_b128 v[84:87], v191 offset:25600
	ds_read_b128 v[88:91], v191 offset:25536
	ds_read_b128 v[92:95], v191 offset:25472
	ds_read_b128 v[96:99], v191 offset:25408
	ds_read_b128 v[100:103], v191 offset:25344
	s_waitcnt lgkmcnt(8)
; #define LAS __attribute__((address_space(3)))
; __device__ __forceinline__ unsigned pk2(float lo, float hi) { return f2bf(lo) | (f2bf(hi) << 16); }
; #define PIN8(a) asm volatile("" : "+v"(a[0]), "+v"(a[1]), "+v"(a[2]), "+v"(a[3]), "+v"(a[4]), "+v"(a[5]), "+v"(a[6]), "+v"(a[7]))
; __device__ __forceinline__ void xattn_unit(const Params& P, LAS unsigned char* lds, int unit, int tid, int lane, int wave) {
;     ...
;         for (int del = 0; del < 16; ++del) {
;             if (del + 1 < 16) {
; #pragma unroll
;                 for (int s = 0; s < 8; ++s) fr[(del + 1) & 1][s] = *(const LAS bf16x8*)(arow + (16 * (del + 1)) * 528 + 64 * s);
;             }
;             __builtin_amdgcn_sched_barrier(0);
;             PIN8(fr[del & 1]);
;             f32x4 acc = (f32x4){0.f, 0.f, 0.f, 0.f};
; #pragma unroll
;             for (int s = 0; s < 8; ++s) acc = __builtin_amdgcn_mfma_f32_16x16x32_bf16(fr[del & 1][s], Bp[ps][s], acc, 0, 0, 0);
;             v2u o; o.x = pk2(acc.x * inv[ps], acc.y * inv[ps]); o.y = pk2(acc.z * inv[ps], acc.w * inv[ps]);
;             *(v2u*)(AO + 16 * del) = o;
;             __builtin_amdgcn_sched_barrier(0);
;         }
	s_nop 0
	v_mfma_f32_16x16x32_bf16 v[68:71], v[68:71], v[34:37], 0
	v_mfma_f32_16x16x32_bf16 v[28:31], v[28:31], v[38:41], v[68:71]
	v_mfma_f32_16x16x32_bf16 v[24:27], v[24:27], v[42:45], v[28:31]
	v_mfma_f32_16x16x32_bf16 v[20:23], v[20:23], v[46:49], v[24:27]
	v_mfma_f32_16x16x32_bf16 v[16:19], v[16:19], v[50:53], v[20:23]
	v_mfma_f32_16x16x32_bf16 v[12:15], v[12:15], v[54:57], v[16:19]
	v_mfma_f32_16x16x32_bf16 v[8:11], v[8:11], v[58:61], v[12:15]
	v_mfma_f32_16x16x32_bf16 v[4:7], v[4:7], v[62:65], v[8:11]
	s_nop 7
	v_mov_b32_e32 v8, v4
	v_mov_b32_e32 v9, v6
	v_mov_b32_e32 v6, v5
	v_pk_mul_f32 v[4:5], v[66:67], v[8:9] op_sel_hi:[0,1]
	v_pk_mul_f32 v[6:7], v[66:67], v[6:7] op_sel_hi:[0,1]
	v_and_b32_sdwa v1, v5, v67 dst_sel:DWORD dst_unused:UNUSED_PAD src0_sel:WORD_1 src1_sel:DWORD
	v_and_b32_sdwa v9, v7, v67 dst_sel:DWORD dst_unused:UNUSED_PAD src0_sel:WORD_1 src1_sel:DWORD
	v_and_b32_sdwa v10, v6, v67 dst_sel:DWORD dst_unused:UNUSED_PAD src0_sel:WORD_1 src1_sel:DWORD
	v_and_b32_sdwa v8, v4, v67 dst_sel:DWORD dst_unused:UNUSED_PAD src0_sel:WORD_1 src1_sel:DWORD
	v_add3_u32 v1, v5, v1, s22
	v_add3_u32 v5, v7, v9, s22
	v_add3_u32 v6, v6, v10, s22
	v_add3_u32 v4, v4, v8, s22
	v_and_b32_e32 v5, 0xffff0000, v5
	v_and_b32_e32 v6, 0xffff0000, v6
	v_or_b32_sdwa v5, v5, v1 dst_sel:DWORD dst_unused:UNUSED_PAD src0_sel:DWORD src1_sel:WORD_1
	v_or_b32_sdwa v4, v6, v4 dst_sel:DWORD dst_unused:UNUSED_PAD src0_sel:DWORD src1_sel:WORD_1
	global_store_dwordx2 v[2:3], v[4:5], off offset:64 sc0 sc1
	ds_read_b128 v[4:7], v191 offset:34240
	ds_read_b128 v[8:11], v191 offset:34176
	ds_read_b128 v[12:15], v191 offset:34112
	ds_read_b128 v[16:19], v191 offset:34048
	ds_read_b128 v[20:23], v191 offset:33984
	ds_read_b128 v[24:27], v191 offset:33920
	ds_read_b128 v[28:31], v191 offset:33856
	ds_read_b128 v[68:71], v191 offset:33792
	s_waitcnt lgkmcnt(8)
	s_nop 0
	v_mfma_f32_16x16x32_bf16 v[100:103], v[100:103], v[34:37], 0
	v_mfma_f32_16x16x32_bf16 v[96:99], v[96:99], v[38:41], v[100:103]
	v_mfma_f32_16x16x32_bf16 v[92:95], v[92:95], v[42:45], v[96:99]
	v_mfma_f32_16x16x32_bf16 v[88:91], v[88:91], v[46:49], v[92:95]
	v_mfma_f32_16x16x32_bf16 v[84:87], v[84:87], v[50:53], v[88:91]
	v_mfma_f32_16x16x32_bf16 v[80:83], v[80:83], v[54:57], v[84:87]
	v_mfma_f32_16x16x32_bf16 v[76:79], v[76:79], v[58:61], v[80:83]
	v_mfma_f32_16x16x32_bf16 v[72:75], v[72:75], v[62:65], v[76:79]
	s_nop 7
	v_mov_b32_e32 v32, v72
	v_mov_b32_e32 v33, v74
	v_mov_b32_e32 v74, v73
	v_pk_mul_f32 v[32:33], v[66:67], v[32:33] op_sel_hi:[0,1]
	v_pk_mul_f32 v[72:73], v[66:67], v[74:75] op_sel_hi:[0,1]
	v_and_b32_sdwa v1, v33, v67 dst_sel:DWORD dst_unused:UNUSED_PAD src0_sel:WORD_1 src1_sel:DWORD
	v_and_b32_sdwa v75, v73, v67 dst_sel:DWORD dst_unused:UNUSED_PAD src0_sel:WORD_1 src1_sel:DWORD
	v_and_b32_sdwa v76, v72, v67 dst_sel:DWORD dst_unused:UNUSED_PAD src0_sel:WORD_1 src1_sel:DWORD
	v_and_b32_sdwa v74, v32, v67 dst_sel:DWORD dst_unused:UNUSED_PAD src0_sel:WORD_1 src1_sel:DWORD
	v_add3_u32 v1, v33, v1, s22
	v_add3_u32 v33, v73, v75, s22
	v_add3_u32 v72, v72, v76, s22
	v_add3_u32 v32, v32, v74, s22
	v_and_b32_e32 v33, 0xffff0000, v33
	v_and_b32_e32 v72, 0xffff0000, v72
	v_or_b32_sdwa v33, v33, v1 dst_sel:DWORD dst_unused:UNUSED_PAD src0_sel:DWORD src1_sel:WORD_1
	v_or_b32_sdwa v32, v72, v32 dst_sel:DWORD dst_unused:UNUSED_PAD src0_sel:DWORD src1_sel:WORD_1
	global_store_dwordx2 v[2:3], v[32:33], off offset:96 sc0 sc1
	ds_read_b128 v[72:75], v191 offset:42688
	ds_read_b128 v[76:79], v191 offset:42624
	ds_read_b128 v[80:83], v191 offset:42560
	ds_read_b128 v[84:87], v191 offset:42496
	ds_read_b128 v[88:91], v191 offset:42432
	ds_read_b128 v[92:95], v191 offset:42368
	ds_read_b128 v[96:99], v191 offset:42304
	ds_read_b128 v[100:103], v191 offset:42240
	s_waitcnt lgkmcnt(8)
	s_nop 0
	v_mfma_f32_16x16x32_bf16 v[68:71], v[68:71], v[34:37], 0
	v_mfma_f32_16x16x32_bf16 v[28:31], v[28:31], v[38:41], v[68:71]
	v_mfma_f32_16x16x32_bf16 v[24:27], v[24:27], v[42:45], v[28:31]
	v_mfma_f32_16x16x32_bf16 v[20:23], v[20:23], v[46:49], v[24:27]
	v_mfma_f32_16x16x32_bf16 v[16:19], v[16:19], v[50:53], v[20:23]
	v_mfma_f32_16x16x32_bf16 v[12:15], v[12:15], v[54:57], v[16:19]
	v_mfma_f32_16x16x32_bf16 v[8:11], v[8:11], v[58:61], v[12:15]
	v_mfma_f32_16x16x32_bf16 v[4:7], v[4:7], v[62:65], v[8:11]
	s_nop 7
	v_mov_b32_e32 v8, v4
	v_mov_b32_e32 v9, v6
	v_mov_b32_e32 v6, v5
	v_pk_mul_f32 v[4:5], v[66:67], v[8:9] op_sel_hi:[0,1]
	v_pk_mul_f32 v[6:7], v[66:67], v[6:7] op_sel_hi:[0,1]
	v_and_b32_sdwa v1, v5, v67 dst_sel:DWORD dst_unused:UNUSED_PAD src0_sel:WORD_1 src1_sel:DWORD
	v_and_b32_sdwa v9, v7, v67 dst_sel:DWORD dst_unused:UNUSED_PAD src0_sel:WORD_1 src1_sel:DWORD
	v_and_b32_sdwa v10, v6, v67 dst_sel:DWORD dst_unused:UNUSED_PAD src0_sel:WORD_1 src1_sel:DWORD
	v_and_b32_sdwa v8, v4, v67 dst_sel:DWORD dst_unused:UNUSED_PAD src0_sel:WORD_1 src1_sel:DWORD
	v_add3_u32 v1, v5, v1, s22
	v_add3_u32 v5, v7, v9, s22
	v_add3_u32 v6, v6, v10, s22
	v_add3_u32 v4, v4, v8, s22
	v_and_b32_e32 v5, 0xffff0000, v5
	v_and_b32_e32 v6, 0xffff0000, v6
	v_or_b32_sdwa v5, v5, v1 dst_sel:DWORD dst_unused:UNUSED_PAD src0_sel:DWORD src1_sel:WORD_1
	v_or_b32_sdwa v4, v6, v4 dst_sel:DWORD dst_unused:UNUSED_PAD src0_sel:DWORD src1_sel:WORD_1
	global_store_dwordx2 v[2:3], v[4:5], off offset:128 sc0 sc1
	ds_read_b128 v[4:7], v191 offset:51136
	ds_read_b128 v[8:11], v191 offset:51072
	ds_read_b128 v[12:15], v191 offset:51008
	ds_read_b128 v[16:19], v191 offset:50944
	ds_read_b128 v[20:23], v191 offset:50880
	ds_read_b128 v[24:27], v191 offset:50816
	ds_read_b128 v[28:31], v191 offset:50752
	ds_read_b128 v[68:71], v191 offset:50688
	s_waitcnt lgkmcnt(8)
; #define LAS __attribute__((address_space(3)))
; __device__ __forceinline__ unsigned pk2(float lo, float hi) { return f2bf(lo) | (f2bf(hi) << 16); }
; #define PIN8(a) asm volatile("" : "+v"(a[0]), "+v"(a[1]), "+v"(a[2]), "+v"(a[3]), "+v"(a[4]), "+v"(a[5]), "+v"(a[6]), "+v"(a[7]))
; __device__ __forceinline__ void xattn_unit(const Params& P, LAS unsigned char* lds, int unit, int tid, int lane, int wave) {
;     ...
;         for (int del = 0; del < 16; ++del) {
;             if (del + 1 < 16) {
; #pragma unroll
;                 for (int s = 0; s < 8; ++s) fr[(del + 1) & 1][s] = *(const LAS bf16x8*)(arow + (16 * (del + 1)) * 528 + 64 * s);
;             }
;             __builtin_amdgcn_sched_barrier(0);
;             PIN8(fr[del & 1]);
;             f32x4 acc = (f32x4){0.f, 0.f, 0.f, 0.f};
; #pragma unroll
;             for (int s = 0; s < 8; ++s) acc = __builtin_amdgcn_mfma_f32_16x16x32_bf16(fr[del & 1][s], Bp[ps][s], acc, 0, 0, 0);
;             v2u o; o.x = pk2(acc.x * inv[ps], acc.y * inv[ps]); o.y = pk2(acc.z * inv[ps], acc.w * inv[ps]);
;             *(v2u*)(AO + 16 * del) = o;
;             __builtin_amdgcn_sched_barrier(0);
;         }
	s_nop 0
	v_mfma_f32_16x16x32_bf16 v[100:103], v[100:103], v[34:37], 0
	v_mfma_f32_16x16x32_bf16 v[96:99], v[96:99], v[38:41], v[100:103]
	v_mfma_f32_16x16x32_bf16 v[92:95], v[92:95], v[42:45], v[96:99]
	v_mfma_f32_16x16x32_bf16 v[88:91], v[88:91], v[46:49], v[92:95]
	v_mfma_f32_16x16x32_bf16 v[84:87], v[84:87], v[50:53], v[88:91]
	v_mfma_f32_16x16x32_bf16 v[80:83], v[80:83], v[54:57], v[84:87]
	v_mfma_f32_16x16x32_bf16 v[76:79], v[76:79], v[58:61], v[80:83]
	v_mfma_f32_16x16x32_bf16 v[72:75], v[72:75], v[62:65], v[76:79]
	s_nop 7
	v_mov_b32_e32 v32, v72
	v_mov_b32_e32 v33, v74
	v_mov_b32_e32 v74, v73
	v_pk_mul_f32 v[32:33], v[66:67], v[32:33] op_sel_hi:[0,1]
	v_pk_mul_f32 v[72:73], v[66:67], v[74:75] op_sel_hi:[0,1]
	v_and_b32_sdwa v1, v33, v67 dst_sel:DWORD dst_unused:UNUSED_PAD src0_sel:WORD_1 src1_sel:DWORD
	v_and_b32_sdwa v75, v73, v67 dst_sel:DWORD dst_unused:UNUSED_PAD src0_sel:WORD_1 src1_sel:DWORD
	v_and_b32_sdwa v76, v72, v67 dst_sel:DWORD dst_unused:UNUSED_PAD src0_sel:WORD_1 src1_sel:DWORD
	v_and_b32_sdwa v74, v32, v67 dst_sel:DWORD dst_unused:UNUSED_PAD src0_sel:WORD_1 src1_sel:DWORD
	v_add3_u32 v1, v33, v1, s22
	v_add3_u32 v33, v73, v75, s22
	v_add3_u32 v72, v72, v76, s22
	v_add3_u32 v32, v32, v74, s22
	v_and_b32_e32 v33, 0xffff0000, v33
	v_and_b32_e32 v72, 0xffff0000, v72
	v_or_b32_sdwa v33, v33, v1 dst_sel:DWORD dst_unused:UNUSED_PAD src0_sel:DWORD src1_sel:WORD_1
	v_or_b32_sdwa v32, v72, v32 dst_sel:DWORD dst_unused:UNUSED_PAD src0_sel:DWORD src1_sel:WORD_1
	global_store_dwordx2 v[2:3], v[32:33], off offset:160 sc0 sc1
	ds_read_b128 v[72:75], v191 offset:59584
	ds_read_b128 v[76:79], v191 offset:59520
	ds_read_b128 v[80:83], v191 offset:59456
	ds_read_b128 v[84:87], v191 offset:59392
	ds_read_b128 v[88:91], v191 offset:59328
	ds_read_b128 v[92:95], v191 offset:59264
	ds_read_b128 v[96:99], v191 offset:59200
	ds_read_b128 v[100:103], v191 offset:59136
	s_waitcnt lgkmcnt(8)
	s_nop 0
	v_mfma_f32_16x16x32_bf16 v[68:71], v[68:71], v[34:37], 0
	v_mfma_f32_16x16x32_bf16 v[28:31], v[28:31], v[38:41], v[68:71]
	v_mfma_f32_16x16x32_bf16 v[24:27], v[24:27], v[42:45], v[28:31]
	v_mfma_f32_16x16x32_bf16 v[20:23], v[20:23], v[46:49], v[24:27]
	v_mfma_f32_16x16x32_bf16 v[16:19], v[16:19], v[50:53], v[20:23]
	v_mfma_f32_16x16x32_bf16 v[12:15], v[12:15], v[54:57], v[16:19]
	v_mfma_f32_16x16x32_bf16 v[8:11], v[8:11], v[58:61], v[12:15]
	v_mfma_f32_16x16x32_bf16 v[4:7], v[4:7], v[62:65], v[8:11]
	s_nop 7
	v_mov_b32_e32 v8, v4
	v_mov_b32_e32 v9, v6
	v_mov_b32_e32 v6, v5
	v_pk_mul_f32 v[4:5], v[66:67], v[8:9] op_sel_hi:[0,1]
	v_pk_mul_f32 v[6:7], v[66:67], v[6:7] op_sel_hi:[0,1]
	v_and_b32_sdwa v1, v5, v67 dst_sel:DWORD dst_unused:UNUSED_PAD src0_sel:WORD_1 src1_sel:DWORD
	v_and_b32_sdwa v9, v7, v67 dst_sel:DWORD dst_unused:UNUSED_PAD src0_sel:WORD_1 src1_sel:DWORD
	v_and_b32_sdwa v10, v6, v67 dst_sel:DWORD dst_unused:UNUSED_PAD src0_sel:WORD_1 src1_sel:DWORD
	v_and_b32_sdwa v8, v4, v67 dst_sel:DWORD dst_unused:UNUSED_PAD src0_sel:WORD_1 src1_sel:DWORD
	v_add3_u32 v1, v5, v1, s22
	v_add3_u32 v5, v7, v9, s22
	v_add3_u32 v6, v6, v10, s22
	v_add3_u32 v4, v4, v8, s22
	v_and_b32_e32 v5, 0xffff0000, v5
	v_and_b32_e32 v6, 0xffff0000, v6
	v_or_b32_sdwa v5, v5, v1 dst_sel:DWORD dst_unused:UNUSED_PAD src0_sel:DWORD src1_sel:WORD_1
	v_or_b32_sdwa v4, v6, v4 dst_sel:DWORD dst_unused:UNUSED_PAD src0_sel:DWORD src1_sel:WORD_1
	global_store_dwordx2 v[2:3], v[4:5], off offset:192 sc0 sc1
	ds_read_b128 v[4:7], v190
	ds_read_b128 v[8:11], v189
	ds_read_b128 v[12:15], v188
	ds_read_b128 v[16:19], v187
	ds_read_b128 v[20:23], v186
	ds_read_b128 v[24:27], v185
	ds_read_b128 v[28:31], v184
	ds_read_b128 v[68:71], v183
	s_waitcnt lgkmcnt(8)
	s_nop 0
	v_mfma_f32_16x16x32_bf16 v[100:103], v[100:103], v[34:37], 0
	v_mfma_f32_16x16x32_bf16 v[96:99], v[96:99], v[38:41], v[100:103]
	v_mfma_f32_16x16x32_bf16 v[92:95], v[92:95], v[42:45], v[96:99]
	v_mfma_f32_16x16x32_bf16 v[88:91], v[88:91], v[46:49], v[92:95]
	v_mfma_f32_16x16x32_bf16 v[84:87], v[84:87], v[50:53], v[88:91]
	v_mfma_f32_16x16x32_bf16 v[80:83], v[80:83], v[54:57], v[84:87]
	v_mfma_f32_16x16x32_bf16 v[76:79], v[76:79], v[58:61], v[80:83]
	v_mfma_f32_16x16x32_bf16 v[72:75], v[72:75], v[62:65], v[76:79]
	s_nop 7
	v_mov_b32_e32 v32, v72
	v_mov_b32_e32 v33, v74
	v_mov_b32_e32 v74, v73
	v_pk_mul_f32 v[32:33], v[66:67], v[32:33] op_sel_hi:[0,1]
	v_pk_mul_f32 v[72:73], v[66:67], v[74:75] op_sel_hi:[0,1]
	v_and_b32_sdwa v1, v33, v67 dst_sel:DWORD dst_unused:UNUSED_PAD src0_sel:WORD_1 src1_sel:DWORD
	v_and_b32_sdwa v75, v73, v67 dst_sel:DWORD dst_unused:UNUSED_PAD src0_sel:WORD_1 src1_sel:DWORD
	v_and_b32_sdwa v76, v72, v67 dst_sel:DWORD dst_unused:UNUSED_PAD src0_sel:WORD_1 src1_sel:DWORD
	v_and_b32_sdwa v74, v32, v67 dst_sel:DWORD dst_unused:UNUSED_PAD src0_sel:WORD_1 src1_sel:DWORD
	v_add3_u32 v1, v33, v1, s22
	v_add3_u32 v33, v73, v75, s22
	v_add3_u32 v72, v72, v76, s22
	v_add3_u32 v32, v32, v74, s22
	v_and_b32_e32 v33, 0xffff0000, v33
	v_and_b32_e32 v72, 0xffff0000, v72
	v_or_b32_sdwa v33, v33, v1 dst_sel:DWORD dst_unused:UNUSED_PAD src0_sel:DWORD src1_sel:WORD_1
	v_or_b32_sdwa v32, v72, v32 dst_sel:DWORD dst_unused:UNUSED_PAD src0_sel:DWORD src1_sel:WORD_1
	global_store_dwordx2 v[2:3], v[32:33], off offset:224 sc0 sc1
	ds_read_b128 v[72:75], v182
	ds_read_b128 v[76:79], v181
	ds_read_b128 v[80:83], v180
	ds_read_b128 v[84:87], v179
	ds_read_b128 v[88:91], v178
	ds_read_b128 v[92:95], v177
	ds_read_b128 v[96:99], v176
	ds_read_b128 v[100:103], v175
	s_waitcnt lgkmcnt(8)
; #define LAS __attribute__((address_space(3)))
; __device__ __forceinline__ unsigned pk2(float lo, float hi) { return f2bf(lo) | (f2bf(hi) << 16); }
; #define PIN8(a) asm volatile("" : "+v"(a[0]), "+v"(a[1]), "+v"(a[2]), "+v"(a[3]), "+v"(a[4]), "+v"(a[5]), "+v"(a[6]), "+v"(a[7]))
; __device__ __forceinline__ void xattn_unit(const Params& P, LAS unsigned char* lds, int unit, int tid, int lane, int wave) {
;     ...
;         for (int del = 0; del < 16; ++del) {
;             if (del + 1 < 16) {
; #pragma unroll
;                 for (int s = 0; s < 8; ++s) fr[(del + 1) & 1][s] = *(const LAS bf16x8*)(arow + (16 * (del + 1)) * 528 + 64 * s);
;             }
;             __builtin_amdgcn_sched_barrier(0);
;             PIN8(fr[del & 1]);
;             f32x4 acc = (f32x4){0.f, 0.f, 0.f, 0.f};
; #pragma unroll
;             for (int s = 0; s < 8; ++s) acc = __builtin_amdgcn_mfma_f32_16x16x32_bf16(fr[del & 1][s], Bp[ps][s], acc, 0, 0, 0);
;             v2u o; o.x = pk2(acc.x * inv[ps], acc.y * inv[ps]); o.y = pk2(acc.z * inv[ps], acc.w * inv[ps]);
;             *(v2u*)(AO + 16 * del) = o;
;             __builtin_amdgcn_sched_barrier(0);
;         }
	s_nop 0
	v_mfma_f32_16x16x32_bf16 v[68:71], v[68:71], v[34:37], 0
	v_mfma_f32_16x16x32_bf16 v[28:31], v[28:31], v[38:41], v[68:71]
	v_mfma_f32_16x16x32_bf16 v[24:27], v[24:27], v[42:45], v[28:31]
	v_mfma_f32_16x16x32_bf16 v[20:23], v[20:23], v[46:49], v[24:27]
	v_mfma_f32_16x16x32_bf16 v[16:19], v[16:19], v[50:53], v[20:23]
	v_mfma_f32_16x16x32_bf16 v[12:15], v[12:15], v[54:57], v[16:19]
	v_mfma_f32_16x16x32_bf16 v[8:11], v[8:11], v[58:61], v[12:15]
	v_mfma_f32_16x16x32_bf16 v[4:7], v[4:7], v[62:65], v[8:11]
	s_nop 7
	v_mov_b32_e32 v8, v4
	v_mov_b32_e32 v9, v6
	v_mov_b32_e32 v6, v5
	v_pk_mul_f32 v[4:5], v[66:67], v[8:9] op_sel_hi:[0,1]
	v_pk_mul_f32 v[6:7], v[66:67], v[6:7] op_sel_hi:[0,1]
	v_and_b32_sdwa v1, v5, v67 dst_sel:DWORD dst_unused:UNUSED_PAD src0_sel:WORD_1 src1_sel:DWORD
	v_and_b32_sdwa v9, v7, v67 dst_sel:DWORD dst_unused:UNUSED_PAD src0_sel:WORD_1 src1_sel:DWORD
	v_and_b32_sdwa v10, v6, v67 dst_sel:DWORD dst_unused:UNUSED_PAD src0_sel:WORD_1 src1_sel:DWORD
	v_and_b32_sdwa v8, v4, v67 dst_sel:DWORD dst_unused:UNUSED_PAD src0_sel:WORD_1 src1_sel:DWORD
	v_add3_u32 v1, v5, v1, s22
	v_add3_u32 v5, v7, v9, s22
	v_add3_u32 v6, v6, v10, s22
	v_add3_u32 v4, v4, v8, s22
	v_and_b32_e32 v5, 0xffff0000, v5
	v_and_b32_e32 v6, 0xffff0000, v6
	v_or_b32_sdwa v5, v5, v1 dst_sel:DWORD dst_unused:UNUSED_PAD src0_sel:DWORD src1_sel:WORD_1
	v_or_b32_sdwa v4, v6, v4 dst_sel:DWORD dst_unused:UNUSED_PAD src0_sel:DWORD src1_sel:WORD_1
	global_store_dwordx2 v[2:3], v[4:5], off offset:256 sc0 sc1
	ds_read_b128 v[4:7], v174
	ds_read_b128 v[8:11], v173
	ds_read_b128 v[12:15], v172
	ds_read_b128 v[16:19], v171
	ds_read_b128 v[20:23], v170
	ds_read_b128 v[24:27], v169
	ds_read_b128 v[28:31], v168
	ds_read_b128 v[68:71], v167
	s_waitcnt lgkmcnt(8)
	s_nop 0
	v_mfma_f32_16x16x32_bf16 v[100:103], v[100:103], v[34:37], 0
	v_mfma_f32_16x16x32_bf16 v[96:99], v[96:99], v[38:41], v[100:103]
	v_mfma_f32_16x16x32_bf16 v[92:95], v[92:95], v[42:45], v[96:99]
	v_mfma_f32_16x16x32_bf16 v[88:91], v[88:91], v[46:49], v[92:95]
	v_mfma_f32_16x16x32_bf16 v[84:87], v[84:87], v[50:53], v[88:91]
	v_mfma_f32_16x16x32_bf16 v[80:83], v[80:83], v[54:57], v[84:87]
	v_mfma_f32_16x16x32_bf16 v[76:79], v[76:79], v[58:61], v[80:83]
	v_mfma_f32_16x16x32_bf16 v[72:75], v[72:75], v[62:65], v[76:79]
	s_nop 7
	v_mov_b32_e32 v32, v72
	v_mov_b32_e32 v33, v74
	v_mov_b32_e32 v74, v73
	v_pk_mul_f32 v[32:33], v[66:67], v[32:33] op_sel_hi:[0,1]
	v_pk_mul_f32 v[72:73], v[66:67], v[74:75] op_sel_hi:[0,1]
	v_and_b32_sdwa v1, v33, v67 dst_sel:DWORD dst_unused:UNUSED_PAD src0_sel:WORD_1 src1_sel:DWORD
	v_and_b32_sdwa v75, v73, v67 dst_sel:DWORD dst_unused:UNUSED_PAD src0_sel:WORD_1 src1_sel:DWORD
	v_and_b32_sdwa v76, v72, v67 dst_sel:DWORD dst_unused:UNUSED_PAD src0_sel:WORD_1 src1_sel:DWORD
	v_and_b32_sdwa v74, v32, v67 dst_sel:DWORD dst_unused:UNUSED_PAD src0_sel:WORD_1 src1_sel:DWORD
	v_add3_u32 v1, v33, v1, s22
	v_add3_u32 v33, v73, v75, s22
	v_add3_u32 v72, v72, v76, s22
	v_add3_u32 v32, v32, v74, s22
	v_and_b32_e32 v33, 0xffff0000, v33
	v_and_b32_e32 v72, 0xffff0000, v72
	v_or_b32_sdwa v33, v33, v1 dst_sel:DWORD dst_unused:UNUSED_PAD src0_sel:DWORD src1_sel:WORD_1
	v_or_b32_sdwa v32, v72, v32 dst_sel:DWORD dst_unused:UNUSED_PAD src0_sel:DWORD src1_sel:WORD_1
	global_store_dwordx2 v[2:3], v[32:33], off offset:288 sc0 sc1
	ds_read_b128 v[72:75], v166
	ds_read_b128 v[76:79], v165
	ds_read_b128 v[80:83], v164
	ds_read_b128 v[84:87], v163
	ds_read_b128 v[88:91], v162
	ds_read_b128 v[92:95], v161
	ds_read_b128 v[96:99], v160
	ds_read_b128 v[100:103], v159
	s_waitcnt lgkmcnt(8)
	s_nop 0
	v_mfma_f32_16x16x32_bf16 v[68:71], v[68:71], v[34:37], 0
	v_mfma_f32_16x16x32_bf16 v[28:31], v[28:31], v[38:41], v[68:71]
	v_mfma_f32_16x16x32_bf16 v[24:27], v[24:27], v[42:45], v[28:31]
	v_mfma_f32_16x16x32_bf16 v[20:23], v[20:23], v[46:49], v[24:27]
	v_mfma_f32_16x16x32_bf16 v[16:19], v[16:19], v[50:53], v[20:23]
	v_mfma_f32_16x16x32_bf16 v[12:15], v[12:15], v[54:57], v[16:19]
	v_mfma_f32_16x16x32_bf16 v[8:11], v[8:11], v[58:61], v[12:15]
	v_mfma_f32_16x16x32_bf16 v[4:7], v[4:7], v[62:65], v[8:11]
	s_nop 7
	v_mov_b32_e32 v8, v4
	v_mov_b32_e32 v9, v6
	v_mov_b32_e32 v6, v5
	v_pk_mul_f32 v[4:5], v[66:67], v[8:9] op_sel_hi:[0,1]
	v_pk_mul_f32 v[6:7], v[66:67], v[6:7] op_sel_hi:[0,1]
	v_and_b32_sdwa v1, v5, v67 dst_sel:DWORD dst_unused:UNUSED_PAD src0_sel:WORD_1 src1_sel:DWORD
	v_and_b32_sdwa v9, v7, v67 dst_sel:DWORD dst_unused:UNUSED_PAD src0_sel:WORD_1 src1_sel:DWORD
	v_and_b32_sdwa v10, v6, v67 dst_sel:DWORD dst_unused:UNUSED_PAD src0_sel:WORD_1 src1_sel:DWORD
	v_and_b32_sdwa v8, v4, v67 dst_sel:DWORD dst_unused:UNUSED_PAD src0_sel:WORD_1 src1_sel:DWORD
	v_add3_u32 v1, v5, v1, s22
	v_add3_u32 v5, v7, v9, s22
	v_add3_u32 v6, v6, v10, s22
	v_add3_u32 v4, v4, v8, s22
	v_and_b32_e32 v5, 0xffff0000, v5
	v_and_b32_e32 v6, 0xffff0000, v6
	v_or_b32_sdwa v5, v5, v1 dst_sel:DWORD dst_unused:UNUSED_PAD src0_sel:DWORD src1_sel:WORD_1
	v_or_b32_sdwa v4, v6, v4 dst_sel:DWORD dst_unused:UNUSED_PAD src0_sel:DWORD src1_sel:WORD_1
	global_store_dwordx2 v[2:3], v[4:5], off offset:320 sc0 sc1
	ds_read_b128 v[4:7], v158
	ds_read_b128 v[8:11], v157
	ds_read_b128 v[12:15], v156
	ds_read_b128 v[16:19], v155
	ds_read_b128 v[20:23], v154
	ds_read_b128 v[24:27], v153
	ds_read_b128 v[28:31], v152
	ds_read_b128 v[68:71], v151
	s_waitcnt lgkmcnt(8)
; #define LAS __attribute__((address_space(3)))
; __device__ __forceinline__ unsigned pk2(float lo, float hi) { return f2bf(lo) | (f2bf(hi) << 16); }
; #define PIN8(a) asm volatile("" : "+v"(a[0]), "+v"(a[1]), "+v"(a[2]), "+v"(a[3]), "+v"(a[4]), "+v"(a[5]), "+v"(a[6]), "+v"(a[7]))
; __device__ __forceinline__ void xattn_unit(const Params& P, LAS unsigned char* lds, int unit, int tid, int lane, int wave) {
;     ...
;         for (int del = 0; del < 16; ++del) {
;             if (del + 1 < 16) {
; #pragma unroll
;                 for (int s = 0; s < 8; ++s) fr[(del + 1) & 1][s] = *(const LAS bf16x8*)(arow + (16 * (del + 1)) * 528 + 64 * s);
;             }
;             __builtin_amdgcn_sched_barrier(0);
;             PIN8(fr[del & 1]);
;             f32x4 acc = (f32x4){0.f, 0.f, 0.f, 0.f};
; #pragma unroll
;             for (int s = 0; s < 8; ++s) acc = __builtin_amdgcn_mfma_f32_16x16x32_bf16(fr[del & 1][s], Bp[ps][s], acc, 0, 0, 0);
;             v2u o; o.x = pk2(acc.x * inv[ps], acc.y * inv[ps]); o.y = pk2(acc.z * inv[ps], acc.w * inv[ps]);
;             *(v2u*)(AO + 16 * del) = o;
;             __builtin_amdgcn_sched_barrier(0);
;         }
	s_nop 0
	v_mfma_f32_16x16x32_bf16 v[100:103], v[100:103], v[34:37], 0
	v_mfma_f32_16x16x32_bf16 v[96:99], v[96:99], v[38:41], v[100:103]
	v_mfma_f32_16x16x32_bf16 v[92:95], v[92:95], v[42:45], v[96:99]
	v_mfma_f32_16x16x32_bf16 v[88:91], v[88:91], v[46:49], v[92:95]
	v_mfma_f32_16x16x32_bf16 v[84:87], v[84:87], v[50:53], v[88:91]
	v_mfma_f32_16x16x32_bf16 v[80:83], v[80:83], v[54:57], v[84:87]
	v_mfma_f32_16x16x32_bf16 v[76:79], v[76:79], v[58:61], v[80:83]
	v_mfma_f32_16x16x32_bf16 v[72:75], v[72:75], v[62:65], v[76:79]
	s_nop 7
	v_mov_b32_e32 v32, v72
	v_mov_b32_e32 v33, v74
	v_mov_b32_e32 v74, v73
	v_pk_mul_f32 v[32:33], v[66:67], v[32:33] op_sel_hi:[0,1]
	v_pk_mul_f32 v[72:73], v[66:67], v[74:75] op_sel_hi:[0,1]
	v_and_b32_sdwa v1, v33, v67 dst_sel:DWORD dst_unused:UNUSED_PAD src0_sel:WORD_1 src1_sel:DWORD
	v_and_b32_sdwa v75, v73, v67 dst_sel:DWORD dst_unused:UNUSED_PAD src0_sel:WORD_1 src1_sel:DWORD
	v_and_b32_sdwa v76, v72, v67 dst_sel:DWORD dst_unused:UNUSED_PAD src0_sel:WORD_1 src1_sel:DWORD
	v_and_b32_sdwa v74, v32, v67 dst_sel:DWORD dst_unused:UNUSED_PAD src0_sel:WORD_1 src1_sel:DWORD
	v_add3_u32 v1, v33, v1, s22
	v_add3_u32 v33, v73, v75, s22
	v_add3_u32 v72, v72, v76, s22
	v_add3_u32 v32, v32, v74, s22
	v_and_b32_e32 v33, 0xffff0000, v33
	v_and_b32_e32 v72, 0xffff0000, v72
	v_or_b32_sdwa v33, v33, v1 dst_sel:DWORD dst_unused:UNUSED_PAD src0_sel:DWORD src1_sel:WORD_1
	v_or_b32_sdwa v32, v72, v32 dst_sel:DWORD dst_unused:UNUSED_PAD src0_sel:DWORD src1_sel:WORD_1
	global_store_dwordx2 v[2:3], v[32:33], off offset:352 sc0 sc1
	ds_read_b128 v[72:75], v150
	ds_read_b128 v[76:79], v149
	ds_read_b128 v[80:83], v148
	ds_read_b128 v[84:87], v147
	ds_read_b128 v[88:91], v146
	ds_read_b128 v[92:95], v145
	ds_read_b128 v[96:99], v144
	ds_read_b128 v[100:103], v143
	s_waitcnt lgkmcnt(8)
	s_nop 0
	v_mfma_f32_16x16x32_bf16 v[68:71], v[68:71], v[34:37], 0
	v_mfma_f32_16x16x32_bf16 v[28:31], v[28:31], v[38:41], v[68:71]
	v_mfma_f32_16x16x32_bf16 v[24:27], v[24:27], v[42:45], v[28:31]
	v_mfma_f32_16x16x32_bf16 v[20:23], v[20:23], v[46:49], v[24:27]
	v_mfma_f32_16x16x32_bf16 v[16:19], v[16:19], v[50:53], v[20:23]
	v_mfma_f32_16x16x32_bf16 v[12:15], v[12:15], v[54:57], v[16:19]
	v_mfma_f32_16x16x32_bf16 v[8:11], v[8:11], v[58:61], v[12:15]
	v_mfma_f32_16x16x32_bf16 v[4:7], v[4:7], v[62:65], v[8:11]
	s_nop 7
	v_mov_b32_e32 v8, v4
	v_mov_b32_e32 v9, v6
	v_mov_b32_e32 v6, v5
	v_pk_mul_f32 v[4:5], v[66:67], v[8:9] op_sel_hi:[0,1]
	v_pk_mul_f32 v[6:7], v[66:67], v[6:7] op_sel_hi:[0,1]
	v_and_b32_sdwa v1, v5, v67 dst_sel:DWORD dst_unused:UNUSED_PAD src0_sel:WORD_1 src1_sel:DWORD
	v_and_b32_sdwa v9, v7, v67 dst_sel:DWORD dst_unused:UNUSED_PAD src0_sel:WORD_1 src1_sel:DWORD
	v_and_b32_sdwa v10, v6, v67 dst_sel:DWORD dst_unused:UNUSED_PAD src0_sel:WORD_1 src1_sel:DWORD
	v_and_b32_sdwa v8, v4, v67 dst_sel:DWORD dst_unused:UNUSED_PAD src0_sel:WORD_1 src1_sel:DWORD
	v_add3_u32 v1, v5, v1, s22
	v_add3_u32 v5, v7, v9, s22
	v_add3_u32 v6, v6, v10, s22
	v_add3_u32 v4, v4, v8, s22
	v_and_b32_e32 v5, 0xffff0000, v5
	v_and_b32_e32 v6, 0xffff0000, v6
	v_or_b32_sdwa v5, v5, v1 dst_sel:DWORD dst_unused:UNUSED_PAD src0_sel:DWORD src1_sel:WORD_1
	v_or_b32_sdwa v4, v6, v4 dst_sel:DWORD dst_unused:UNUSED_PAD src0_sel:DWORD src1_sel:WORD_1
	global_store_dwordx2 v[2:3], v[4:5], off offset:384 sc0 sc1
	ds_read_b128 v[4:7], v142
	ds_read_b128 v[8:11], v141
	ds_read_b128 v[12:15], v140
	ds_read_b128 v[16:19], v139
	ds_read_b128 v[20:23], v138
	ds_read_b128 v[24:27], v137
	ds_read_b128 v[28:31], v136
	ds_read_b128 v[68:71], v135
	s_waitcnt lgkmcnt(8)
; #define LAS __attribute__((address_space(3)))
; __device__ __forceinline__ unsigned pk2(float lo, float hi) { return f2bf(lo) | (f2bf(hi) << 16); }
; #define PIN8(a) asm volatile("" : "+v"(a[0]), "+v"(a[1]), "+v"(a[2]), "+v"(a[3]), "+v"(a[4]), "+v"(a[5]), "+v"(a[6]), "+v"(a[7]))
; __device__ __forceinline__ void xattn_unit(const Params& P, LAS unsigned char* lds, int unit, int tid, int lane, int wave) {
;     ...
;         for (int del = 0; del < 16; ++del) {
;             if (del + 1 < 16) {
; #pragma unroll
;                 for (int s = 0; s < 8; ++s) fr[(del + 1) & 1][s] = *(const LAS bf16x8*)(arow + (16 * (del + 1)) * 528 + 64 * s);
;             }
;             __builtin_amdgcn_sched_barrier(0);
;             PIN8(fr[del & 1]);
;             f32x4 acc = (f32x4){0.f, 0.f, 0.f, 0.f};
; #pragma unroll
;             for (int s = 0; s < 8; ++s) acc = __builtin_amdgcn_mfma_f32_16x16x32_bf16(fr[del & 1][s], Bp[ps][s], acc, 0, 0, 0);
;             v2u o; o.x = pk2(acc.x * inv[ps], acc.y * inv[ps]); o.y = pk2(acc.z * inv[ps], acc.w * inv[ps]);
;             *(v2u*)(AO + 16 * del) = o;
;             __builtin_amdgcn_sched_barrier(0);
;         }
;     }
;     __syncthreads();
	s_nop 0
	v_mfma_f32_16x16x32_bf16 v[100:103], v[100:103], v[34:37], 0
	v_mfma_f32_16x16x32_bf16 v[96:99], v[96:99], v[38:41], v[100:103]
	v_mfma_f32_16x16x32_bf16 v[92:95], v[92:95], v[42:45], v[96:99]
	v_mfma_f32_16x16x32_bf16 v[88:91], v[88:91], v[46:49], v[92:95]
	v_mfma_f32_16x16x32_bf16 v[84:87], v[84:87], v[50:53], v[88:91]
	v_mfma_f32_16x16x32_bf16 v[80:83], v[80:83], v[54:57], v[84:87]
	v_mfma_f32_16x16x32_bf16 v[76:79], v[76:79], v[58:61], v[80:83]
	v_mfma_f32_16x16x32_bf16 v[72:75], v[72:75], v[62:65], v[76:79]
	s_nop 7
	v_mov_b32_e32 v32, v72
	v_mov_b32_e32 v33, v74
	v_mov_b32_e32 v74, v73
	v_pk_mul_f32 v[32:33], v[66:67], v[32:33] op_sel_hi:[0,1]
	v_pk_mul_f32 v[72:73], v[66:67], v[74:75] op_sel_hi:[0,1]
	v_and_b32_sdwa v1, v33, v67 dst_sel:DWORD dst_unused:UNUSED_PAD src0_sel:WORD_1 src1_sel:DWORD
	v_and_b32_sdwa v75, v73, v67 dst_sel:DWORD dst_unused:UNUSED_PAD src0_sel:WORD_1 src1_sel:DWORD
	v_and_b32_sdwa v76, v72, v67 dst_sel:DWORD dst_unused:UNUSED_PAD src0_sel:WORD_1 src1_sel:DWORD
	v_and_b32_sdwa v74, v32, v67 dst_sel:DWORD dst_unused:UNUSED_PAD src0_sel:WORD_1 src1_sel:DWORD
	v_add3_u32 v1, v33, v1, s22
	v_add3_u32 v33, v73, v75, s22
	v_add3_u32 v72, v72, v76, s22
	v_add3_u32 v32, v32, v74, s22
	v_and_b32_e32 v33, 0xffff0000, v33
	v_and_b32_e32 v72, 0xffff0000, v72
	v_or_b32_sdwa v33, v33, v1 dst_sel:DWORD dst_unused:UNUSED_PAD src0_sel:DWORD src1_sel:WORD_1
	v_or_b32_sdwa v32, v72, v32 dst_sel:DWORD dst_unused:UNUSED_PAD src0_sel:DWORD src1_sel:WORD_1
	global_store_dwordx2 v[2:3], v[32:33], off offset:416 sc0 sc1
	ds_read_b128 v[72:75], v134
	ds_read_b128 v[76:79], v133
	ds_read_b128 v[80:83], v252
	ds_read_b128 v[84:87], v198
	ds_read_b128 v[88:91], v253
	ds_read_b128 v[92:95], v200
	ds_read_b128 v[96:99], v132
	ds_read_b128 v[100:103], v127
	s_waitcnt lgkmcnt(8)
	s_nop 0
	v_mfma_f32_16x16x32_bf16 v[68:71], v[68:71], v[34:37], 0
	v_mfma_f32_16x16x32_bf16 v[28:31], v[28:31], v[38:41], v[68:71]
	v_mfma_f32_16x16x32_bf16 v[24:27], v[24:27], v[42:45], v[28:31]
	v_mfma_f32_16x16x32_bf16 v[20:23], v[20:23], v[46:49], v[24:27]
	v_mfma_f32_16x16x32_bf16 v[16:19], v[16:19], v[50:53], v[20:23]
	v_mfma_f32_16x16x32_bf16 v[12:15], v[12:15], v[54:57], v[16:19]
	v_mfma_f32_16x16x32_bf16 v[8:11], v[8:11], v[58:61], v[12:15]
	v_mfma_f32_16x16x32_bf16 v[4:7], v[4:7], v[62:65], v[8:11]
	s_nop 7
	v_mov_b32_e32 v8, v4
	v_mov_b32_e32 v9, v6
	v_mov_b32_e32 v6, v5
	v_pk_mul_f32 v[4:5], v[66:67], v[8:9] op_sel_hi:[0,1]
	v_pk_mul_f32 v[6:7], v[66:67], v[6:7] op_sel_hi:[0,1]
	v_and_b32_sdwa v1, v5, v67 dst_sel:DWORD dst_unused:UNUSED_PAD src0_sel:WORD_1 src1_sel:DWORD
	v_and_b32_sdwa v9, v7, v67 dst_sel:DWORD dst_unused:UNUSED_PAD src0_sel:WORD_1 src1_sel:DWORD
	v_and_b32_sdwa v10, v6, v67 dst_sel:DWORD dst_unused:UNUSED_PAD src0_sel:WORD_1 src1_sel:DWORD
	v_and_b32_sdwa v8, v4, v67 dst_sel:DWORD dst_unused:UNUSED_PAD src0_sel:WORD_1 src1_sel:DWORD
	v_add3_u32 v1, v5, v1, s22
	v_add3_u32 v5, v7, v9, s22
	v_add3_u32 v6, v6, v10, s22
	v_add3_u32 v4, v4, v8, s22
	v_and_b32_e32 v5, 0xffff0000, v5
	v_and_b32_e32 v6, 0xffff0000, v6
	v_or_b32_sdwa v5, v5, v1 dst_sel:DWORD dst_unused:UNUSED_PAD src0_sel:DWORD src1_sel:WORD_1
	v_or_b32_sdwa v4, v6, v4 dst_sel:DWORD dst_unused:UNUSED_PAD src0_sel:DWORD src1_sel:WORD_1
	global_store_dwordx2 v[2:3], v[4:5], off offset:448 sc0 sc1
	s_waitcnt lgkmcnt(0)
	s_nop 0
	v_mfma_f32_16x16x32_bf16 v[4:7], v[100:103], v[34:37], 0
	v_mfma_f32_16x16x32_bf16 v[4:7], v[96:99], v[38:41], v[4:7]
	v_mfma_f32_16x16x32_bf16 v[4:7], v[92:95], v[42:45], v[4:7]
	v_mfma_f32_16x16x32_bf16 v[4:7], v[88:91], v[46:49], v[4:7]
	v_mfma_f32_16x16x32_bf16 v[4:7], v[84:87], v[50:53], v[4:7]
	v_mfma_f32_16x16x32_bf16 v[4:7], v[80:83], v[54:57], v[4:7]
	v_mfma_f32_16x16x32_bf16 v[4:7], v[76:79], v[58:61], v[4:7]
	v_mfma_f32_16x16x32_bf16 v[4:7], v[72:75], v[62:65], v[4:7]
	s_nop 7
	v_mov_b32_e32 v8, v4
	v_mov_b32_e32 v9, v6
	v_mov_b32_e32 v6, v5
	v_pk_mul_f32 v[4:5], v[66:67], v[8:9] op_sel_hi:[0,1]
	v_pk_mul_f32 v[6:7], v[66:67], v[6:7] op_sel_hi:[0,1]
	v_and_b32_sdwa v1, v5, v67 dst_sel:DWORD dst_unused:UNUSED_PAD src0_sel:WORD_1 src1_sel:DWORD
	v_and_b32_sdwa v9, v7, v67 dst_sel:DWORD dst_unused:UNUSED_PAD src0_sel:WORD_1 src1_sel:DWORD
	v_and_b32_sdwa v10, v6, v67 dst_sel:DWORD dst_unused:UNUSED_PAD src0_sel:WORD_1 src1_sel:DWORD
	v_and_b32_sdwa v8, v4, v67 dst_sel:DWORD dst_unused:UNUSED_PAD src0_sel:WORD_1 src1_sel:DWORD
	v_add3_u32 v1, v5, v1, s22
	v_add3_u32 v5, v7, v9, s22
	v_add3_u32 v6, v6, v10, s22
	v_add3_u32 v4, v4, v8, s22
	v_and_b32_e32 v5, 0xffff0000, v5
	v_and_b32_e32 v6, 0xffff0000, v6
	v_or_b32_sdwa v5, v5, v1 dst_sel:DWORD dst_unused:UNUSED_PAD src0_sel:DWORD src1_sel:WORD_1
	v_or_b32_sdwa v4, v6, v4 dst_sel:DWORD dst_unused:UNUSED_PAD src0_sel:DWORD src1_sel:WORD_1
	global_store_dwordx2 v[2:3], v[4:5], off offset:480 sc0 sc1
	s_barrier
